# pooling: batched register-resident fast path for chunks that do not start a sequence (all rows loaded up front, same op order, exact 1/W)
# speedup vs baseline: 1.0123x; 1.0107x over previous
; #define GAS __attribute__((address_space(1)))
; template <int W>
; __device__ __forceinline__ void pool_item(const bf16* U, bf16* Z, int b, int t0, int g, int lane) {
;     const size_t base = (size_t)b * SEQ * D + 256 * g + 4 * lane;
;     float s[4] = {0.f, 0.f, 0.f, 0.f};
; #pragma unroll
;     for (int j = 1; j <= W; ++j) { const int t = t0 - j; if (t >= 0) { const u32x2 v = *(const GAS u32x2*)(U + base + (size_t)t * D);
;             s[0] += bf2f(v.x & 0xffffu); s[1] += bf2f(v.x >> 16); s[2] += bf2f(v.y & 0xffffu); s[3] += bf2f(v.y >> 16); } }
; #pragma unroll 8
;     for (int i = 0; i < 32; ++i) { const int t = t0 + i;
; __global__ void __launch_bounds__(NWAVES * 64, 2) mk_fwd(Args args) {
;     ...
;                       const int b = pu.pm >> 3, t0 = (pu.pm & 7) * 256 + 32 * F.wave, g = pu.pn;
;                       if (g == 0) pool_item<2>(U, Z, b, t0, 0, F.lane); else if (g == 1) pool_item<4>(U, Z, b, t0, 1, F.lane);
;                       else if (g == 2) pool_item<8>(U, Z, b, t0, 2, F.lane); else pool_item<16>(U, Z, b, t0, 3, F.lane); }
.LBB0_869:
	s_nop 0
	v_writelane_b32 v255, s8, 3
	s_mov_b64 s[46:47], -1
	s_and_b64 vcc, exec, s[40:41]
	s_cbranch_vccz .LBB0_862
	v_readlane_b32 s8, v255, 4
	s_ashr_i32 s48, s8, 3
	s_lshl_b32 s8, s8, 8
	s_and_b32 s8, s8, 0x700
	s_ashr_i32 s49, s48, 31
	s_add_i32 s46, s8, s5
	s_lshl_b64 s[50:51], s[48:49], 21
	s_cmp_gt_i32 s46, 0
	v_readlane_b32 s9, v255, 3
	s_cselect_b64 s[40:41], -1, 0
	s_mov_b64 s[56:57], -1
	s_mov_b64 s[52:53], 0
	s_cmp_lt_i32 s46, 16
	s_cbranch_scc1 .Lpool_orig
	s_lshl_b64 s[10:11], s[50:51], 1
	s_add_u32 s10, s10, s44
	s_addc_u32 s11, s11, s45
	s_add_i32 s22, s46, -16
	s_lshl_b32 s22, s22, 11
	s_add_u32 s10, s10, s22
	s_addc_u32 s11, s11, 0
	s_add_u32 s28, s10, 0x2008000
	s_addc_u32 s29, s11, 0
	s_lshl_b32 s22, s9, 9
	v_lshl_add_u32 v190, v4, 1, s22
	s_cmp_eq_u32 s9, 0
	s_cbranch_scc1 .Lpool_w2
	s_cmp_eq_u32 s9, 1
	s_cbranch_scc1 .Lpool_w4
	s_cmp_eq_u32 s9, 2
	s_cbranch_scc1 .Lpool_w8
.Lpool_w16:
	v_mov_b32_e32 v188, 0x3d800000
	v_mov_b32_e32 v189, v188
	global_load_dwordx2 v[68:69], v190, s[10:11]
	global_load_dwordx2 v[70:71], v190, s[10:11] offset:2048
	v_add_u32_e32 v192, 0x1000, v190
	global_load_dwordx2 v[72:73], v192, s[10:11]
	global_load_dwordx2 v[74:75], v192, s[10:11] offset:2048
	v_add_u32_e32 v191, 0x2000, v190
	global_load_dwordx2 v[76:77], v191, s[10:11]
	global_load_dwordx2 v[78:79], v191, s[10:11] offset:2048
	v_add_u32_e32 v192, 0x3000, v190
	global_load_dwordx2 v[80:81], v192, s[10:11]
	global_load_dwordx2 v[82:83], v192, s[10:11] offset:2048
	v_add_u32_e32 v191, 0x4000, v190
	global_load_dwordx2 v[84:85], v191, s[10:11]
	global_load_dwordx2 v[86:87], v191, s[10:11] offset:2048
	v_add_u32_e32 v192, 0x5000, v190
	global_load_dwordx2 v[88:89], v192, s[10:11]
	global_load_dwordx2 v[90:91], v192, s[10:11] offset:2048
	v_add_u32_e32 v191, 0x6000, v190
	global_load_dwordx2 v[92:93], v191, s[10:11]
	global_load_dwordx2 v[94:95], v191, s[10:11] offset:2048
	v_add_u32_e32 v192, 0x7000, v190
	global_load_dwordx2 v[96:97], v192, s[10:11]
	global_load_dwordx2 v[98:99], v192, s[10:11] offset:2048
	v_add_u32_e32 v191, 0x8000, v190
	global_load_dwordx2 v[100:101], v191, s[10:11]
	global_load_dwordx2 v[102:103], v191, s[10:11] offset:2048
	v_add_u32_e32 v192, 0x9000, v190
	global_load_dwordx2 v[104:105], v192, s[10:11]
	global_load_dwordx2 v[106:107], v192, s[10:11] offset:2048
	v_add_u32_e32 v191, 0xa000, v190
	global_load_dwordx2 v[108:109], v191, s[10:11]
	global_load_dwordx2 v[110:111], v191, s[10:11] offset:2048
	v_add_u32_e32 v192, 0xb000, v190
	global_load_dwordx2 v[112:113], v192, s[10:11]
	global_load_dwordx2 v[114:115], v192, s[10:11] offset:2048
	v_add_u32_e32 v191, 0xc000, v190
	global_load_dwordx2 v[116:117], v191, s[10:11]
	global_load_dwordx2 v[118:119], v191, s[10:11] offset:2048
	v_add_u32_e32 v192, 0xd000, v190
	global_load_dwordx2 v[120:121], v192, s[10:11]
	global_load_dwordx2 v[122:123], v192, s[10:11] offset:2048
	v_add_u32_e32 v191, 0xe000, v190
	global_load_dwordx2 v[124:125], v191, s[10:11]
	global_load_dwordx2 v[126:127], v191, s[10:11] offset:2048
	v_add_u32_e32 v192, 0xf000, v190
	global_load_dwordx2 v[128:129], v192, s[10:11]
	global_load_dwordx2 v[130:131], v192, s[10:11] offset:2048
	v_add_u32_e32 v191, 0x10000, v190
	global_load_dwordx2 v[132:133], v191, s[10:11]
	global_load_dwordx2 v[134:135], v191, s[10:11] offset:2048
	v_add_u32_e32 v192, 0x11000, v190
	global_load_dwordx2 v[136:137], v192, s[10:11]
	global_load_dwordx2 v[138:139], v192, s[10:11] offset:2048
	v_add_u32_e32 v191, 0x12000, v190
	global_load_dwordx2 v[140:141], v191, s[10:11]
	global_load_dwordx2 v[142:143], v191, s[10:11] offset:2048
	v_add_u32_e32 v192, 0x13000, v190
	global_load_dwordx2 v[144:145], v192, s[10:11]
	global_load_dwordx2 v[146:147], v192, s[10:11] offset:2048
	v_add_u32_e32 v191, 0x14000, v190
	global_load_dwordx2 v[148:149], v191, s[10:11]
	global_load_dwordx2 v[150:151], v191, s[10:11] offset:2048
	v_add_u32_e32 v192, 0x15000, v190
	global_load_dwordx2 v[152:153], v192, s[10:11]
	global_load_dwordx2 v[154:155], v192, s[10:11] offset:2048
	v_add_u32_e32 v191, 0x16000, v190
	global_load_dwordx2 v[156:157], v191, s[10:11]
	global_load_dwordx2 v[158:159], v191, s[10:11] offset:2048
	v_add_u32_e32 v192, 0x17000, v190
	global_load_dwordx2 v[160:161], v192, s[10:11]
	global_load_dwordx2 v[162:163], v192, s[10:11] offset:2048
	s_waitcnt vmcnt(32)
; #define GAS __attribute__((address_space(1)))
; __device__ __forceinline__ unsigned pk2(float lo, float hi) { const f32x2 v = {lo, hi}; return __builtin_bit_cast(unsigned, __builtin_convertvector(v, b16x2)); }
; template <int W>
; __device__ __forceinline__ void pool_item(const bf16* U, bf16* Z, int b, int t0, int g, int lane) {
;     ...
;     for (int j = 1; j <= W; ++j) { const int t = t0 - j; if (t >= 0) { const u32x2 v = *(const GAS u32x2*)(U + base + (size_t)t * D);
;             s[0] += bf2f(v.x & 0xffffu); s[1] += bf2f(v.x >> 16); s[2] += bf2f(v.y & 0xffffu); s[3] += bf2f(v.y >> 16); } }
; #pragma unroll 8
;     for (int i = 0; i < 32; ++i) { const int t = t0 + i;
;         const u32x2 v = *(const GAS u32x2*)(U + base + (size_t)t * D);
;         const float c0 = bf2f(v.x & 0xffffu), c1 = bf2f(v.x >> 16), c2 = bf2f(v.y & 0xffffu), c3 = bf2f(v.y >> 16);
;         s[0] += c0; s[1] += c1; s[2] += c2; s[3] += c3;
;         if (t - W >= 0) { const u32x2 o = *(const GAS u32x2*)(U + base + (size_t)(t - W) * D);
;             s[0] -= bf2f(o.x & 0xffffu); s[1] -= bf2f(o.x >> 16); s[2] -= bf2f(o.y & 0xffffu); s[3] -= bf2f(o.y >> 16); }
;         const float inv = 1.0f / (float)((t + 1) < W ? (t + 1) : W);
;         u32x2 w; w.x = pk2(s[0] * inv - c0, s[1] * inv - c1); w.y = pk2(s[2] * inv - c2, s[3] * inv - c3);
;         *(GAS u32x2*)(Z + base + (size_t)t * D) = w; }
	v_lshlrev_b32_e32 v164, 16, v98
	v_and_b32_e32 v165, 0xffff0000, v98
	v_lshlrev_b32_e32 v166, 16, v99
	v_and_b32_e32 v167, 0xffff0000, v99
	v_pk_add_f32 v[184:185], v[164:165], 0 op_sel_hi:[1,0]
	v_pk_add_f32 v[186:187], v[166:167], 0 op_sel_hi:[1,0]
	v_lshlrev_b32_e32 v164, 16, v96
	v_and_b32_e32 v165, 0xffff0000, v96
	v_lshlrev_b32_e32 v166, 16, v97
	v_and_b32_e32 v167, 0xffff0000, v97
	v_pk_add_f32 v[184:185], v[184:185], v[164:165]
	v_pk_add_f32 v[186:187], v[186:187], v[166:167]
	v_lshlrev_b32_e32 v164, 16, v94
	v_and_b32_e32 v165, 0xffff0000, v94
	v_lshlrev_b32_e32 v166, 16, v95
	v_and_b32_e32 v167, 0xffff0000, v95
	v_pk_add_f32 v[184:185], v[184:185], v[164:165]
	v_pk_add_f32 v[186:187], v[186:187], v[166:167]
	v_lshlrev_b32_e32 v164, 16, v92
	v_and_b32_e32 v165, 0xffff0000, v92
	v_lshlrev_b32_e32 v166, 16, v93
	v_and_b32_e32 v167, 0xffff0000, v93
	v_pk_add_f32 v[184:185], v[184:185], v[164:165]
	v_pk_add_f32 v[186:187], v[186:187], v[166:167]
	v_lshlrev_b32_e32 v164, 16, v90
	v_and_b32_e32 v165, 0xffff0000, v90
	v_lshlrev_b32_e32 v166, 16, v91
	v_and_b32_e32 v167, 0xffff0000, v91
	v_pk_add_f32 v[184:185], v[184:185], v[164:165]
	v_pk_add_f32 v[186:187], v[186:187], v[166:167]
	v_lshlrev_b32_e32 v164, 16, v88
	v_and_b32_e32 v165, 0xffff0000, v88
	v_lshlrev_b32_e32 v166, 16, v89
	v_and_b32_e32 v167, 0xffff0000, v89
	v_pk_add_f32 v[184:185], v[184:185], v[164:165]
	v_pk_add_f32 v[186:187], v[186:187], v[166:167]
	v_lshlrev_b32_e32 v164, 16, v86
	v_and_b32_e32 v165, 0xffff0000, v86
	v_lshlrev_b32_e32 v166, 16, v87
	v_and_b32_e32 v167, 0xffff0000, v87
	v_pk_add_f32 v[184:185], v[184:185], v[164:165]
	v_pk_add_f32 v[186:187], v[186:187], v[166:167]
	v_lshlrev_b32_e32 v164, 16, v84
	v_and_b32_e32 v165, 0xffff0000, v84
	v_lshlrev_b32_e32 v166, 16, v85
	v_and_b32_e32 v167, 0xffff0000, v85
	v_pk_add_f32 v[184:185], v[184:185], v[164:165]
	v_pk_add_f32 v[186:187], v[186:187], v[166:167]
	v_lshlrev_b32_e32 v164, 16, v82
	v_and_b32_e32 v165, 0xffff0000, v82
	v_lshlrev_b32_e32 v166, 16, v83
	v_and_b32_e32 v167, 0xffff0000, v83
	v_pk_add_f32 v[184:185], v[184:185], v[164:165]
	v_pk_add_f32 v[186:187], v[186:187], v[166:167]
	v_lshlrev_b32_e32 v164, 16, v80
	v_and_b32_e32 v165, 0xffff0000, v80
	v_lshlrev_b32_e32 v166, 16, v81
	v_and_b32_e32 v167, 0xffff0000, v81
	v_pk_add_f32 v[184:185], v[184:185], v[164:165]
	v_pk_add_f32 v[186:187], v[186:187], v[166:167]
	v_lshlrev_b32_e32 v164, 16, v78
	v_and_b32_e32 v165, 0xffff0000, v78
	v_lshlrev_b32_e32 v166, 16, v79
	v_and_b32_e32 v167, 0xffff0000, v79
	v_pk_add_f32 v[184:185], v[184:185], v[164:165]
	v_pk_add_f32 v[186:187], v[186:187], v[166:167]
	v_lshlrev_b32_e32 v164, 16, v76
	v_and_b32_e32 v165, 0xffff0000, v76
	v_lshlrev_b32_e32 v166, 16, v77
	v_and_b32_e32 v167, 0xffff0000, v77
	v_pk_add_f32 v[184:185], v[184:185], v[164:165]
	v_pk_add_f32 v[186:187], v[186:187], v[166:167]
	v_lshlrev_b32_e32 v164, 16, v74
	v_and_b32_e32 v165, 0xffff0000, v74
	v_lshlrev_b32_e32 v166, 16, v75
	v_and_b32_e32 v167, 0xffff0000, v75
	v_pk_add_f32 v[184:185], v[184:185], v[164:165]
	v_pk_add_f32 v[186:187], v[186:187], v[166:167]
	v_lshlrev_b32_e32 v164, 16, v72
	v_and_b32_e32 v165, 0xffff0000, v72
	v_lshlrev_b32_e32 v166, 16, v73
	v_and_b32_e32 v167, 0xffff0000, v73
	v_pk_add_f32 v[184:185], v[184:185], v[164:165]
	v_pk_add_f32 v[186:187], v[186:187], v[166:167]
	v_lshlrev_b32_e32 v164, 16, v70
	v_and_b32_e32 v165, 0xffff0000, v70
	v_lshlrev_b32_e32 v166, 16, v71
	v_and_b32_e32 v167, 0xffff0000, v71
	v_pk_add_f32 v[184:185], v[184:185], v[164:165]
	v_pk_add_f32 v[186:187], v[186:187], v[166:167]
	v_lshlrev_b32_e32 v164, 16, v68
	v_and_b32_e32 v165, 0xffff0000, v68
	v_lshlrev_b32_e32 v166, 16, v69
	v_and_b32_e32 v167, 0xffff0000, v69
	v_pk_add_f32 v[184:185], v[184:185], v[164:165]
	v_pk_add_f32 v[186:187], v[186:187], v[166:167]
	s_waitcnt vmcnt(31)
	v_lshlrev_b32_e32 v164, 16, v100
	v_and_b32_e32 v165, 0xffff0000, v100
	v_lshlrev_b32_e32 v166, 16, v101
	v_and_b32_e32 v167, 0xffff0000, v101
	v_pk_add_f32 v[184:185], v[184:185], v[164:165]
	v_pk_add_f32 v[186:187], v[186:187], v[166:167]
	v_lshlrev_b32_e32 v168, 16, v68
	v_and_b32_e32 v169, 0xffff0000, v68
	v_lshlrev_b32_e32 v170, 16, v69
	v_and_b32_e32 v171, 0xffff0000, v69
	v_pk_add_f32 v[184:185], v[184:185], v[168:169] neg_lo:[0,1] neg_hi:[0,1]
	v_pk_add_f32 v[186:187], v[186:187], v[170:171] neg_lo:[0,1] neg_hi:[0,1]
	v_pk_fma_f32 v[172:173], v[188:189], v[184:185], v[164:165] op_sel_hi:[0,1,1] neg_lo:[0,0,1] neg_hi:[0,0,1]
	v_pk_fma_f32 v[174:175], v[188:189], v[186:187], v[166:167] op_sel_hi:[0,1,1] neg_lo:[0,0,1] neg_hi:[0,0,1]
	v_cvt_pk_bf16_f32 v176, v172, v173
	v_cvt_pk_bf16_f32 v177, v174, v175
	global_store_dwordx2 v190, v[176:177], s[28:29]
	s_waitcnt vmcnt(31)
	v_lshlrev_b32_e32 v164, 16, v102
	v_and_b32_e32 v165, 0xffff0000, v102
	v_lshlrev_b32_e32 v166, 16, v103
	v_and_b32_e32 v167, 0xffff0000, v103
	v_pk_add_f32 v[184:185], v[184:185], v[164:165]
	v_pk_add_f32 v[186:187], v[186:187], v[166:167]
	v_lshlrev_b32_e32 v168, 16, v70
	v_and_b32_e32 v169, 0xffff0000, v70
	v_lshlrev_b32_e32 v170, 16, v71
	v_and_b32_e32 v171, 0xffff0000, v71
	v_pk_add_f32 v[184:185], v[184:185], v[168:169] neg_lo:[0,1] neg_hi:[0,1]
	v_pk_add_f32 v[186:187], v[186:187], v[170:171] neg_lo:[0,1] neg_hi:[0,1]
	v_pk_fma_f32 v[172:173], v[188:189], v[184:185], v[164:165] op_sel_hi:[0,1,1] neg_lo:[0,0,1] neg_hi:[0,0,1]
	v_pk_fma_f32 v[174:175], v[188:189], v[186:187], v[166:167] op_sel_hi:[0,1,1] neg_lo:[0,0,1] neg_hi:[0,0,1]
	v_cvt_pk_bf16_f32 v178, v172, v173
	v_cvt_pk_bf16_f32 v179, v174, v175
	global_store_dwordx2 v190, v[178:179], s[28:29] offset:2048
	s_waitcnt vmcnt(31)
; #define GAS __attribute__((address_space(1)))
; __device__ __forceinline__ unsigned pk2(float lo, float hi) { const f32x2 v = {lo, hi}; return __builtin_bit_cast(unsigned, __builtin_convertvector(v, b16x2)); }
; template <int W>
; __device__ __forceinline__ void pool_item(const bf16* U, bf16* Z, int b, int t0, int g, int lane) {
;     ...
;     for (int i = 0; i < 32; ++i) { const int t = t0 + i;
;         const u32x2 v = *(const GAS u32x2*)(U + base + (size_t)t * D);
;         const float c0 = bf2f(v.x & 0xffffu), c1 = bf2f(v.x >> 16), c2 = bf2f(v.y & 0xffffu), c3 = bf2f(v.y >> 16);
;         s[0] += c0; s[1] += c1; s[2] += c2; s[3] += c3;
;         if (t - W >= 0) { const u32x2 o = *(const GAS u32x2*)(U + base + (size_t)(t - W) * D);
;             s[0] -= bf2f(o.x & 0xffffu); s[1] -= bf2f(o.x >> 16); s[2] -= bf2f(o.y & 0xffffu); s[3] -= bf2f(o.y >> 16); }
;         const float inv = 1.0f / (float)((t + 1) < W ? (t + 1) : W);
;         u32x2 w; w.x = pk2(s[0] * inv - c0, s[1] * inv - c1); w.y = pk2(s[2] * inv - c2, s[3] * inv - c3);
;         *(GAS u32x2*)(Z + base + (size_t)t * D) = w; }
	v_lshlrev_b32_e32 v164, 16, v104
	v_and_b32_e32 v165, 0xffff0000, v104
	v_lshlrev_b32_e32 v166, 16, v105
	v_and_b32_e32 v167, 0xffff0000, v105
	v_pk_add_f32 v[184:185], v[184:185], v[164:165]
	v_pk_add_f32 v[186:187], v[186:187], v[166:167]
	v_lshlrev_b32_e32 v168, 16, v72
	v_and_b32_e32 v169, 0xffff0000, v72
	v_lshlrev_b32_e32 v170, 16, v73
	v_and_b32_e32 v171, 0xffff0000, v73
	v_pk_add_f32 v[184:185], v[184:185], v[168:169] neg_lo:[0,1] neg_hi:[0,1]
	v_pk_add_f32 v[186:187], v[186:187], v[170:171] neg_lo:[0,1] neg_hi:[0,1]
	v_pk_fma_f32 v[172:173], v[188:189], v[184:185], v[164:165] op_sel_hi:[0,1,1] neg_lo:[0,0,1] neg_hi:[0,0,1]
	v_pk_fma_f32 v[174:175], v[188:189], v[186:187], v[166:167] op_sel_hi:[0,1,1] neg_lo:[0,0,1] neg_hi:[0,0,1]
	v_cvt_pk_bf16_f32 v180, v172, v173
	v_cvt_pk_bf16_f32 v181, v174, v175
	v_add_u32_e32 v194, 0x1000, v190
	global_store_dwordx2 v194, v[180:181], s[28:29]
	s_waitcnt vmcnt(31)
	v_lshlrev_b32_e32 v164, 16, v106
	v_and_b32_e32 v165, 0xffff0000, v106
	v_lshlrev_b32_e32 v166, 16, v107
	v_and_b32_e32 v167, 0xffff0000, v107
	v_pk_add_f32 v[184:185], v[184:185], v[164:165]
	v_pk_add_f32 v[186:187], v[186:187], v[166:167]
	v_lshlrev_b32_e32 v168, 16, v74
	v_and_b32_e32 v169, 0xffff0000, v74
	v_lshlrev_b32_e32 v170, 16, v75
	v_and_b32_e32 v171, 0xffff0000, v75
	v_pk_add_f32 v[184:185], v[184:185], v[168:169] neg_lo:[0,1] neg_hi:[0,1]
	v_pk_add_f32 v[186:187], v[186:187], v[170:171] neg_lo:[0,1] neg_hi:[0,1]
	v_pk_fma_f32 v[172:173], v[188:189], v[184:185], v[164:165] op_sel_hi:[0,1,1] neg_lo:[0,0,1] neg_hi:[0,0,1]
	v_pk_fma_f32 v[174:175], v[188:189], v[186:187], v[166:167] op_sel_hi:[0,1,1] neg_lo:[0,0,1] neg_hi:[0,0,1]
	v_cvt_pk_bf16_f32 v182, v172, v173
	v_cvt_pk_bf16_f32 v183, v174, v175
	global_store_dwordx2 v194, v[182:183], s[28:29] offset:2048
	s_waitcnt vmcnt(31)
	v_lshlrev_b32_e32 v164, 16, v108
	v_and_b32_e32 v165, 0xffff0000, v108
	v_lshlrev_b32_e32 v166, 16, v109
	v_and_b32_e32 v167, 0xffff0000, v109
	v_pk_add_f32 v[184:185], v[184:185], v[164:165]
	v_pk_add_f32 v[186:187], v[186:187], v[166:167]
	v_lshlrev_b32_e32 v168, 16, v76
	v_and_b32_e32 v169, 0xffff0000, v76
	v_lshlrev_b32_e32 v170, 16, v77
	v_and_b32_e32 v171, 0xffff0000, v77
	v_pk_add_f32 v[184:185], v[184:185], v[168:169] neg_lo:[0,1] neg_hi:[0,1]
	v_pk_add_f32 v[186:187], v[186:187], v[170:171] neg_lo:[0,1] neg_hi:[0,1]
	v_pk_fma_f32 v[172:173], v[188:189], v[184:185], v[164:165] op_sel_hi:[0,1,1] neg_lo:[0,0,1] neg_hi:[0,0,1]
	v_pk_fma_f32 v[174:175], v[188:189], v[186:187], v[166:167] op_sel_hi:[0,1,1] neg_lo:[0,0,1] neg_hi:[0,0,1]
	v_cvt_pk_bf16_f32 v176, v172, v173
	v_cvt_pk_bf16_f32 v177, v174, v175
	v_add_u32_e32 v193, 0x2000, v190
	global_store_dwordx2 v193, v[176:177], s[28:29]
	s_waitcnt vmcnt(31)
	v_lshlrev_b32_e32 v164, 16, v110
	v_and_b32_e32 v165, 0xffff0000, v110
	v_lshlrev_b32_e32 v166, 16, v111
	v_and_b32_e32 v167, 0xffff0000, v111
	v_pk_add_f32 v[184:185], v[184:185], v[164:165]
	v_pk_add_f32 v[186:187], v[186:187], v[166:167]
	v_lshlrev_b32_e32 v168, 16, v78
	v_and_b32_e32 v169, 0xffff0000, v78
	v_lshlrev_b32_e32 v170, 16, v79
	v_and_b32_e32 v171, 0xffff0000, v79
	v_pk_add_f32 v[184:185], v[184:185], v[168:169] neg_lo:[0,1] neg_hi:[0,1]
	v_pk_add_f32 v[186:187], v[186:187], v[170:171] neg_lo:[0,1] neg_hi:[0,1]
	v_pk_fma_f32 v[172:173], v[188:189], v[184:185], v[164:165] op_sel_hi:[0,1,1] neg_lo:[0,0,1] neg_hi:[0,0,1]
	v_pk_fma_f32 v[174:175], v[188:189], v[186:187], v[166:167] op_sel_hi:[0,1,1] neg_lo:[0,0,1] neg_hi:[0,0,1]
	v_cvt_pk_bf16_f32 v178, v172, v173
	v_cvt_pk_bf16_f32 v179, v174, v175
	global_store_dwordx2 v193, v[178:179], s[28:29] offset:2048
	s_waitcnt vmcnt(31)
	v_lshlrev_b32_e32 v164, 16, v112
	v_and_b32_e32 v165, 0xffff0000, v112
	v_lshlrev_b32_e32 v166, 16, v113
	v_and_b32_e32 v167, 0xffff0000, v113
	v_pk_add_f32 v[184:185], v[184:185], v[164:165]
	v_pk_add_f32 v[186:187], v[186:187], v[166:167]
	v_lshlrev_b32_e32 v168, 16, v80
	v_and_b32_e32 v169, 0xffff0000, v80
	v_lshlrev_b32_e32 v170, 16, v81
	v_and_b32_e32 v171, 0xffff0000, v81
	v_pk_add_f32 v[184:185], v[184:185], v[168:169] neg_lo:[0,1] neg_hi:[0,1]
	v_pk_add_f32 v[186:187], v[186:187], v[170:171] neg_lo:[0,1] neg_hi:[0,1]
	v_pk_fma_f32 v[172:173], v[188:189], v[184:185], v[164:165] op_sel_hi:[0,1,1] neg_lo:[0,0,1] neg_hi:[0,0,1]
	v_pk_fma_f32 v[174:175], v[188:189], v[186:187], v[166:167] op_sel_hi:[0,1,1] neg_lo:[0,0,1] neg_hi:[0,0,1]
	v_cvt_pk_bf16_f32 v180, v172, v173
	v_cvt_pk_bf16_f32 v181, v174, v175
	v_add_u32_e32 v194, 0x3000, v190
	global_store_dwordx2 v194, v[180:181], s[28:29]
	s_waitcnt vmcnt(31)
	v_lshlrev_b32_e32 v164, 16, v114
	v_and_b32_e32 v165, 0xffff0000, v114
	v_lshlrev_b32_e32 v166, 16, v115
	v_and_b32_e32 v167, 0xffff0000, v115
	v_pk_add_f32 v[184:185], v[184:185], v[164:165]
	v_pk_add_f32 v[186:187], v[186:187], v[166:167]
	v_lshlrev_b32_e32 v168, 16, v82
	v_and_b32_e32 v169, 0xffff0000, v82
	v_lshlrev_b32_e32 v170, 16, v83
	v_and_b32_e32 v171, 0xffff0000, v83
	v_pk_add_f32 v[184:185], v[184:185], v[168:169] neg_lo:[0,1] neg_hi:[0,1]
	v_pk_add_f32 v[186:187], v[186:187], v[170:171] neg_lo:[0,1] neg_hi:[0,1]
	v_pk_fma_f32 v[172:173], v[188:189], v[184:185], v[164:165] op_sel_hi:[0,1,1] neg_lo:[0,0,1] neg_hi:[0,0,1]
	v_pk_fma_f32 v[174:175], v[188:189], v[186:187], v[166:167] op_sel_hi:[0,1,1] neg_lo:[0,0,1] neg_hi:[0,0,1]
	v_cvt_pk_bf16_f32 v182, v172, v173
	v_cvt_pk_bf16_f32 v183, v174, v175
	global_store_dwordx2 v194, v[182:183], s[28:29] offset:2048
	s_waitcnt vmcnt(31)
; #define GAS __attribute__((address_space(1)))
; __device__ __forceinline__ unsigned pk2(float lo, float hi) { const f32x2 v = {lo, hi}; return __builtin_bit_cast(unsigned, __builtin_convertvector(v, b16x2)); }
; template <int W>
; __device__ __forceinline__ void pool_item(const bf16* U, bf16* Z, int b, int t0, int g, int lane) {
;     ...
;     for (int i = 0; i < 32; ++i) { const int t = t0 + i;
;         const u32x2 v = *(const GAS u32x2*)(U + base + (size_t)t * D);
;         const float c0 = bf2f(v.x & 0xffffu), c1 = bf2f(v.x >> 16), c2 = bf2f(v.y & 0xffffu), c3 = bf2f(v.y >> 16);
;         s[0] += c0; s[1] += c1; s[2] += c2; s[3] += c3;
;         if (t - W >= 0) { const u32x2 o = *(const GAS u32x2*)(U + base + (size_t)(t - W) * D);
;             s[0] -= bf2f(o.x & 0xffffu); s[1] -= bf2f(o.x >> 16); s[2] -= bf2f(o.y & 0xffffu); s[3] -= bf2f(o.y >> 16); }
;         const float inv = 1.0f / (float)((t + 1) < W ? (t + 1) : W);
;         u32x2 w; w.x = pk2(s[0] * inv - c0, s[1] * inv - c1); w.y = pk2(s[2] * inv - c2, s[3] * inv - c3);
;         *(GAS u32x2*)(Z + base + (size_t)t * D) = w; }
; }
	v_lshlrev_b32_e32 v164, 16, v116
	v_and_b32_e32 v165, 0xffff0000, v116
	v_lshlrev_b32_e32 v166, 16, v117
	v_and_b32_e32 v167, 0xffff0000, v117
	v_pk_add_f32 v[184:185], v[184:185], v[164:165]
	v_pk_add_f32 v[186:187], v[186:187], v[166:167]
	v_lshlrev_b32_e32 v168, 16, v84
	v_and_b32_e32 v169, 0xffff0000, v84
	v_lshlrev_b32_e32 v170, 16, v85
	v_and_b32_e32 v171, 0xffff0000, v85
	v_pk_add_f32 v[184:185], v[184:185], v[168:169] neg_lo:[0,1] neg_hi:[0,1]
	v_pk_add_f32 v[186:187], v[186:187], v[170:171] neg_lo:[0,1] neg_hi:[0,1]
	v_pk_fma_f32 v[172:173], v[188:189], v[184:185], v[164:165] op_sel_hi:[0,1,1] neg_lo:[0,0,1] neg_hi:[0,0,1]
	v_pk_fma_f32 v[174:175], v[188:189], v[186:187], v[166:167] op_sel_hi:[0,1,1] neg_lo:[0,0,1] neg_hi:[0,0,1]
	v_cvt_pk_bf16_f32 v176, v172, v173
	v_cvt_pk_bf16_f32 v177, v174, v175
	v_add_u32_e32 v193, 0x4000, v190
	global_store_dwordx2 v193, v[176:177], s[28:29]
	s_waitcnt vmcnt(31)
	v_lshlrev_b32_e32 v164, 16, v118
	v_and_b32_e32 v165, 0xffff0000, v118
	v_lshlrev_b32_e32 v166, 16, v119
	v_and_b32_e32 v167, 0xffff0000, v119
	v_pk_add_f32 v[184:185], v[184:185], v[164:165]
	v_pk_add_f32 v[186:187], v[186:187], v[166:167]
	v_lshlrev_b32_e32 v168, 16, v86
	v_and_b32_e32 v169, 0xffff0000, v86
	v_lshlrev_b32_e32 v170, 16, v87
	v_and_b32_e32 v171, 0xffff0000, v87
	v_pk_add_f32 v[184:185], v[184:185], v[168:169] neg_lo:[0,1] neg_hi:[0,1]
	v_pk_add_f32 v[186:187], v[186:187], v[170:171] neg_lo:[0,1] neg_hi:[0,1]
	v_pk_fma_f32 v[172:173], v[188:189], v[184:185], v[164:165] op_sel_hi:[0,1,1] neg_lo:[0,0,1] neg_hi:[0,0,1]
	v_pk_fma_f32 v[174:175], v[188:189], v[186:187], v[166:167] op_sel_hi:[0,1,1] neg_lo:[0,0,1] neg_hi:[0,0,1]
	v_cvt_pk_bf16_f32 v178, v172, v173
	v_cvt_pk_bf16_f32 v179, v174, v175
	global_store_dwordx2 v193, v[178:179], s[28:29] offset:2048
	s_waitcnt vmcnt(31)
	v_lshlrev_b32_e32 v164, 16, v120
	v_and_b32_e32 v165, 0xffff0000, v120
	v_lshlrev_b32_e32 v166, 16, v121
	v_and_b32_e32 v167, 0xffff0000, v121
	v_pk_add_f32 v[184:185], v[184:185], v[164:165]
	v_pk_add_f32 v[186:187], v[186:187], v[166:167]
	v_lshlrev_b32_e32 v168, 16, v88
	v_and_b32_e32 v169, 0xffff0000, v88
	v_lshlrev_b32_e32 v170, 16, v89
	v_and_b32_e32 v171, 0xffff0000, v89
	v_pk_add_f32 v[184:185], v[184:185], v[168:169] neg_lo:[0,1] neg_hi:[0,1]
	v_pk_add_f32 v[186:187], v[186:187], v[170:171] neg_lo:[0,1] neg_hi:[0,1]
	v_pk_fma_f32 v[172:173], v[188:189], v[184:185], v[164:165] op_sel_hi:[0,1,1] neg_lo:[0,0,1] neg_hi:[0,0,1]
	v_pk_fma_f32 v[174:175], v[188:189], v[186:187], v[166:167] op_sel_hi:[0,1,1] neg_lo:[0,0,1] neg_hi:[0,0,1]
	v_cvt_pk_bf16_f32 v180, v172, v173
	v_cvt_pk_bf16_f32 v181, v174, v175
	v_add_u32_e32 v194, 0x5000, v190
	global_store_dwordx2 v194, v[180:181], s[28:29]
	s_waitcnt vmcnt(31)
	v_lshlrev_b32_e32 v164, 16, v122
	v_and_b32_e32 v165, 0xffff0000, v122
	v_lshlrev_b32_e32 v166, 16, v123
	v_and_b32_e32 v167, 0xffff0000, v123
	v_pk_add_f32 v[184:185], v[184:185], v[164:165]
	v_pk_add_f32 v[186:187], v[186:187], v[166:167]
	v_lshlrev_b32_e32 v168, 16, v90
	v_and_b32_e32 v169, 0xffff0000, v90
	v_lshlrev_b32_e32 v170, 16, v91
	v_and_b32_e32 v171, 0xffff0000, v91
	v_pk_add_f32 v[184:185], v[184:185], v[168:169] neg_lo:[0,1] neg_hi:[0,1]
	v_pk_add_f32 v[186:187], v[186:187], v[170:171] neg_lo:[0,1] neg_hi:[0,1]
	v_pk_fma_f32 v[172:173], v[188:189], v[184:185], v[164:165] op_sel_hi:[0,1,1] neg_lo:[0,0,1] neg_hi:[0,0,1]
	v_pk_fma_f32 v[174:175], v[188:189], v[186:187], v[166:167] op_sel_hi:[0,1,1] neg_lo:[0,0,1] neg_hi:[0,0,1]
	v_cvt_pk_bf16_f32 v182, v172, v173
	v_cvt_pk_bf16_f32 v183, v174, v175
	global_store_dwordx2 v194, v[182:183], s[28:29] offset:2048
	s_waitcnt vmcnt(31)
	v_lshlrev_b32_e32 v164, 16, v124
	v_and_b32_e32 v165, 0xffff0000, v124
	v_lshlrev_b32_e32 v166, 16, v125
	v_and_b32_e32 v167, 0xffff0000, v125
	v_pk_add_f32 v[184:185], v[184:185], v[164:165]
	v_pk_add_f32 v[186:187], v[186:187], v[166:167]
	v_lshlrev_b32_e32 v168, 16, v92
	v_and_b32_e32 v169, 0xffff0000, v92
	v_lshlrev_b32_e32 v170, 16, v93
	v_and_b32_e32 v171, 0xffff0000, v93
	v_pk_add_f32 v[184:185], v[184:185], v[168:169] neg_lo:[0,1] neg_hi:[0,1]
	v_pk_add_f32 v[186:187], v[186:187], v[170:171] neg_lo:[0,1] neg_hi:[0,1]
	v_pk_fma_f32 v[172:173], v[188:189], v[184:185], v[164:165] op_sel_hi:[0,1,1] neg_lo:[0,0,1] neg_hi:[0,0,1]
	v_pk_fma_f32 v[174:175], v[188:189], v[186:187], v[166:167] op_sel_hi:[0,1,1] neg_lo:[0,0,1] neg_hi:[0,0,1]
	v_cvt_pk_bf16_f32 v176, v172, v173
	v_cvt_pk_bf16_f32 v177, v174, v175
	v_add_u32_e32 v193, 0x6000, v190
	global_store_dwordx2 v193, v[176:177], s[28:29]
	s_waitcnt vmcnt(31)
	v_lshlrev_b32_e32 v164, 16, v126
	v_and_b32_e32 v165, 0xffff0000, v126
	v_lshlrev_b32_e32 v166, 16, v127
	v_and_b32_e32 v167, 0xffff0000, v127
	v_pk_add_f32 v[184:185], v[184:185], v[164:165]
	v_pk_add_f32 v[186:187], v[186:187], v[166:167]
	v_lshlrev_b32_e32 v168, 16, v94
	v_and_b32_e32 v169, 0xffff0000, v94
	v_lshlrev_b32_e32 v170, 16, v95
	v_and_b32_e32 v171, 0xffff0000, v95
	v_pk_add_f32 v[184:185], v[184:185], v[168:169] neg_lo:[0,1] neg_hi:[0,1]
	v_pk_add_f32 v[186:187], v[186:187], v[170:171] neg_lo:[0,1] neg_hi:[0,1]
	v_pk_fma_f32 v[172:173], v[188:189], v[184:185], v[164:165] op_sel_hi:[0,1,1] neg_lo:[0,0,1] neg_hi:[0,0,1]
	v_pk_fma_f32 v[174:175], v[188:189], v[186:187], v[166:167] op_sel_hi:[0,1,1] neg_lo:[0,0,1] neg_hi:[0,0,1]
	v_cvt_pk_bf16_f32 v178, v172, v173
	v_cvt_pk_bf16_f32 v179, v174, v175
	global_store_dwordx2 v193, v[178:179], s[28:29] offset:2048
	s_waitcnt vmcnt(31)
; #define GAS __attribute__((address_space(1)))
; __device__ __forceinline__ unsigned pk2(float lo, float hi) { const f32x2 v = {lo, hi}; return __builtin_bit_cast(unsigned, __builtin_convertvector(v, b16x2)); }
; template <int W>
; __device__ __forceinline__ void pool_item(const bf16* U, bf16* Z, int b, int t0, int g, int lane) {
;     ...
;     for (int i = 0; i < 32; ++i) { const int t = t0 + i;
;         const u32x2 v = *(const GAS u32x2*)(U + base + (size_t)t * D);
;         const float c0 = bf2f(v.x & 0xffffu), c1 = bf2f(v.x >> 16), c2 = bf2f(v.y & 0xffffu), c3 = bf2f(v.y >> 16);
;         s[0] += c0; s[1] += c1; s[2] += c2; s[3] += c3;
;         if (t - W >= 0) { const u32x2 o = *(const GAS u32x2*)(U + base + (size_t)(t - W) * D);
;             s[0] -= bf2f(o.x & 0xffffu); s[1] -= bf2f(o.x >> 16); s[2] -= bf2f(o.y & 0xffffu); s[3] -= bf2f(o.y >> 16); }
;         const float inv = 1.0f / (float)((t + 1) < W ? (t + 1) : W);
;         u32x2 w; w.x = pk2(s[0] * inv - c0, s[1] * inv - c1); w.y = pk2(s[2] * inv - c2, s[3] * inv - c3);
;         *(GAS u32x2*)(Z + base + (size_t)t * D) = w; }
; }
	v_lshlrev_b32_e32 v164, 16, v128
	v_and_b32_e32 v165, 0xffff0000, v128
	v_lshlrev_b32_e32 v166, 16, v129
	v_and_b32_e32 v167, 0xffff0000, v129
	v_pk_add_f32 v[184:185], v[184:185], v[164:165]
	v_pk_add_f32 v[186:187], v[186:187], v[166:167]
	v_lshlrev_b32_e32 v168, 16, v96
	v_and_b32_e32 v169, 0xffff0000, v96
	v_lshlrev_b32_e32 v170, 16, v97
	v_and_b32_e32 v171, 0xffff0000, v97
	v_pk_add_f32 v[184:185], v[184:185], v[168:169] neg_lo:[0,1] neg_hi:[0,1]
	v_pk_add_f32 v[186:187], v[186:187], v[170:171] neg_lo:[0,1] neg_hi:[0,1]
	v_pk_fma_f32 v[172:173], v[188:189], v[184:185], v[164:165] op_sel_hi:[0,1,1] neg_lo:[0,0,1] neg_hi:[0,0,1]
	v_pk_fma_f32 v[174:175], v[188:189], v[186:187], v[166:167] op_sel_hi:[0,1,1] neg_lo:[0,0,1] neg_hi:[0,0,1]
	v_cvt_pk_bf16_f32 v180, v172, v173
	v_cvt_pk_bf16_f32 v181, v174, v175
	v_add_u32_e32 v194, 0x7000, v190
	global_store_dwordx2 v194, v[180:181], s[28:29]
	s_waitcnt vmcnt(31)
	v_lshlrev_b32_e32 v164, 16, v130
	v_and_b32_e32 v165, 0xffff0000, v130
	v_lshlrev_b32_e32 v166, 16, v131
	v_and_b32_e32 v167, 0xffff0000, v131
	v_pk_add_f32 v[184:185], v[184:185], v[164:165]
	v_pk_add_f32 v[186:187], v[186:187], v[166:167]
	v_lshlrev_b32_e32 v168, 16, v98
	v_and_b32_e32 v169, 0xffff0000, v98
	v_lshlrev_b32_e32 v170, 16, v99
	v_and_b32_e32 v171, 0xffff0000, v99
	v_pk_add_f32 v[184:185], v[184:185], v[168:169] neg_lo:[0,1] neg_hi:[0,1]
	v_pk_add_f32 v[186:187], v[186:187], v[170:171] neg_lo:[0,1] neg_hi:[0,1]
	v_pk_fma_f32 v[172:173], v[188:189], v[184:185], v[164:165] op_sel_hi:[0,1,1] neg_lo:[0,0,1] neg_hi:[0,0,1]
	v_pk_fma_f32 v[174:175], v[188:189], v[186:187], v[166:167] op_sel_hi:[0,1,1] neg_lo:[0,0,1] neg_hi:[0,0,1]
	v_cvt_pk_bf16_f32 v182, v172, v173
	v_cvt_pk_bf16_f32 v183, v174, v175
	global_store_dwordx2 v194, v[182:183], s[28:29] offset:2048
	s_waitcnt vmcnt(31)
	v_lshlrev_b32_e32 v164, 16, v132
	v_and_b32_e32 v165, 0xffff0000, v132
	v_lshlrev_b32_e32 v166, 16, v133
	v_and_b32_e32 v167, 0xffff0000, v133
	v_pk_add_f32 v[184:185], v[184:185], v[164:165]
	v_pk_add_f32 v[186:187], v[186:187], v[166:167]
	v_lshlrev_b32_e32 v168, 16, v100
	v_and_b32_e32 v169, 0xffff0000, v100
	v_lshlrev_b32_e32 v170, 16, v101
	v_and_b32_e32 v171, 0xffff0000, v101
	v_pk_add_f32 v[184:185], v[184:185], v[168:169] neg_lo:[0,1] neg_hi:[0,1]
	v_pk_add_f32 v[186:187], v[186:187], v[170:171] neg_lo:[0,1] neg_hi:[0,1]
	v_pk_fma_f32 v[172:173], v[188:189], v[184:185], v[164:165] op_sel_hi:[0,1,1] neg_lo:[0,0,1] neg_hi:[0,0,1]
	v_pk_fma_f32 v[174:175], v[188:189], v[186:187], v[166:167] op_sel_hi:[0,1,1] neg_lo:[0,0,1] neg_hi:[0,0,1]
	v_cvt_pk_bf16_f32 v176, v172, v173
	v_cvt_pk_bf16_f32 v177, v174, v175
	v_add_u32_e32 v193, 0x8000, v190
	global_store_dwordx2 v193, v[176:177], s[28:29]
	s_waitcnt vmcnt(31)
	v_lshlrev_b32_e32 v164, 16, v134
	v_and_b32_e32 v165, 0xffff0000, v134
	v_lshlrev_b32_e32 v166, 16, v135
	v_and_b32_e32 v167, 0xffff0000, v135
	v_pk_add_f32 v[184:185], v[184:185], v[164:165]
	v_pk_add_f32 v[186:187], v[186:187], v[166:167]
	v_lshlrev_b32_e32 v168, 16, v102
	v_and_b32_e32 v169, 0xffff0000, v102
	v_lshlrev_b32_e32 v170, 16, v103
	v_and_b32_e32 v171, 0xffff0000, v103
	v_pk_add_f32 v[184:185], v[184:185], v[168:169] neg_lo:[0,1] neg_hi:[0,1]
	v_pk_add_f32 v[186:187], v[186:187], v[170:171] neg_lo:[0,1] neg_hi:[0,1]
	v_pk_fma_f32 v[172:173], v[188:189], v[184:185], v[164:165] op_sel_hi:[0,1,1] neg_lo:[0,0,1] neg_hi:[0,0,1]
	v_pk_fma_f32 v[174:175], v[188:189], v[186:187], v[166:167] op_sel_hi:[0,1,1] neg_lo:[0,0,1] neg_hi:[0,0,1]
	v_cvt_pk_bf16_f32 v178, v172, v173
	v_cvt_pk_bf16_f32 v179, v174, v175
	global_store_dwordx2 v193, v[178:179], s[28:29] offset:2048
	s_waitcnt vmcnt(31)
	v_lshlrev_b32_e32 v164, 16, v136
	v_and_b32_e32 v165, 0xffff0000, v136
	v_lshlrev_b32_e32 v166, 16, v137
	v_and_b32_e32 v167, 0xffff0000, v137
	v_pk_add_f32 v[184:185], v[184:185], v[164:165]
	v_pk_add_f32 v[186:187], v[186:187], v[166:167]
	v_lshlrev_b32_e32 v168, 16, v104
	v_and_b32_e32 v169, 0xffff0000, v104
	v_lshlrev_b32_e32 v170, 16, v105
	v_and_b32_e32 v171, 0xffff0000, v105
	v_pk_add_f32 v[184:185], v[184:185], v[168:169] neg_lo:[0,1] neg_hi:[0,1]
	v_pk_add_f32 v[186:187], v[186:187], v[170:171] neg_lo:[0,1] neg_hi:[0,1]
	v_pk_fma_f32 v[172:173], v[188:189], v[184:185], v[164:165] op_sel_hi:[0,1,1] neg_lo:[0,0,1] neg_hi:[0,0,1]
	v_pk_fma_f32 v[174:175], v[188:189], v[186:187], v[166:167] op_sel_hi:[0,1,1] neg_lo:[0,0,1] neg_hi:[0,0,1]
	v_cvt_pk_bf16_f32 v180, v172, v173
	v_cvt_pk_bf16_f32 v181, v174, v175
	v_add_u32_e32 v194, 0x9000, v190
	global_store_dwordx2 v194, v[180:181], s[28:29]
	s_waitcnt vmcnt(31)
	v_lshlrev_b32_e32 v164, 16, v138
	v_and_b32_e32 v165, 0xffff0000, v138
	v_lshlrev_b32_e32 v166, 16, v139
	v_and_b32_e32 v167, 0xffff0000, v139
	v_pk_add_f32 v[184:185], v[184:185], v[164:165]
	v_pk_add_f32 v[186:187], v[186:187], v[166:167]
	v_lshlrev_b32_e32 v168, 16, v106
	v_and_b32_e32 v169, 0xffff0000, v106
	v_lshlrev_b32_e32 v170, 16, v107
	v_and_b32_e32 v171, 0xffff0000, v107
	v_pk_add_f32 v[184:185], v[184:185], v[168:169] neg_lo:[0,1] neg_hi:[0,1]
	v_pk_add_f32 v[186:187], v[186:187], v[170:171] neg_lo:[0,1] neg_hi:[0,1]
	v_pk_fma_f32 v[172:173], v[188:189], v[184:185], v[164:165] op_sel_hi:[0,1,1] neg_lo:[0,0,1] neg_hi:[0,0,1]
	v_pk_fma_f32 v[174:175], v[188:189], v[186:187], v[166:167] op_sel_hi:[0,1,1] neg_lo:[0,0,1] neg_hi:[0,0,1]
	v_cvt_pk_bf16_f32 v182, v172, v173
	v_cvt_pk_bf16_f32 v183, v174, v175
	global_store_dwordx2 v194, v[182:183], s[28:29] offset:2048
	s_waitcnt vmcnt(31)
; #define GAS __attribute__((address_space(1)))
; __device__ __forceinline__ unsigned pk2(float lo, float hi) { const f32x2 v = {lo, hi}; return __builtin_bit_cast(unsigned, __builtin_convertvector(v, b16x2)); }
; template <int W>
; __device__ __forceinline__ void pool_item(const bf16* U, bf16* Z, int b, int t0, int g, int lane) {
;     ...
;     for (int i = 0; i < 32; ++i) { const int t = t0 + i;
;         const u32x2 v = *(const GAS u32x2*)(U + base + (size_t)t * D);
;         const float c0 = bf2f(v.x & 0xffffu), c1 = bf2f(v.x >> 16), c2 = bf2f(v.y & 0xffffu), c3 = bf2f(v.y >> 16);
;         s[0] += c0; s[1] += c1; s[2] += c2; s[3] += c3;
;         if (t - W >= 0) { const u32x2 o = *(const GAS u32x2*)(U + base + (size_t)(t - W) * D);
;             s[0] -= bf2f(o.x & 0xffffu); s[1] -= bf2f(o.x >> 16); s[2] -= bf2f(o.y & 0xffffu); s[3] -= bf2f(o.y >> 16); }
;         const float inv = 1.0f / (float)((t + 1) < W ? (t + 1) : W);
;         u32x2 w; w.x = pk2(s[0] * inv - c0, s[1] * inv - c1); w.y = pk2(s[2] * inv - c2, s[3] * inv - c3);
;         *(GAS u32x2*)(Z + base + (size_t)t * D) = w; }
; }
	v_lshlrev_b32_e32 v164, 16, v140
	v_and_b32_e32 v165, 0xffff0000, v140
	v_lshlrev_b32_e32 v166, 16, v141
	v_and_b32_e32 v167, 0xffff0000, v141
	v_pk_add_f32 v[184:185], v[184:185], v[164:165]
	v_pk_add_f32 v[186:187], v[186:187], v[166:167]
	v_lshlrev_b32_e32 v168, 16, v108
	v_and_b32_e32 v169, 0xffff0000, v108
	v_lshlrev_b32_e32 v170, 16, v109
	v_and_b32_e32 v171, 0xffff0000, v109
	v_pk_add_f32 v[184:185], v[184:185], v[168:169] neg_lo:[0,1] neg_hi:[0,1]
	v_pk_add_f32 v[186:187], v[186:187], v[170:171] neg_lo:[0,1] neg_hi:[0,1]
	v_pk_fma_f32 v[172:173], v[188:189], v[184:185], v[164:165] op_sel_hi:[0,1,1] neg_lo:[0,0,1] neg_hi:[0,0,1]
	v_pk_fma_f32 v[174:175], v[188:189], v[186:187], v[166:167] op_sel_hi:[0,1,1] neg_lo:[0,0,1] neg_hi:[0,0,1]
	v_cvt_pk_bf16_f32 v176, v172, v173
	v_cvt_pk_bf16_f32 v177, v174, v175
	v_add_u32_e32 v193, 0xa000, v190
	global_store_dwordx2 v193, v[176:177], s[28:29]
	s_waitcnt vmcnt(31)
	v_lshlrev_b32_e32 v164, 16, v142
	v_and_b32_e32 v165, 0xffff0000, v142
	v_lshlrev_b32_e32 v166, 16, v143
	v_and_b32_e32 v167, 0xffff0000, v143
	v_pk_add_f32 v[184:185], v[184:185], v[164:165]
	v_pk_add_f32 v[186:187], v[186:187], v[166:167]
	v_lshlrev_b32_e32 v168, 16, v110
	v_and_b32_e32 v169, 0xffff0000, v110
	v_lshlrev_b32_e32 v170, 16, v111
	v_and_b32_e32 v171, 0xffff0000, v111
	v_pk_add_f32 v[184:185], v[184:185], v[168:169] neg_lo:[0,1] neg_hi:[0,1]
	v_pk_add_f32 v[186:187], v[186:187], v[170:171] neg_lo:[0,1] neg_hi:[0,1]
	v_pk_fma_f32 v[172:173], v[188:189], v[184:185], v[164:165] op_sel_hi:[0,1,1] neg_lo:[0,0,1] neg_hi:[0,0,1]
	v_pk_fma_f32 v[174:175], v[188:189], v[186:187], v[166:167] op_sel_hi:[0,1,1] neg_lo:[0,0,1] neg_hi:[0,0,1]
	v_cvt_pk_bf16_f32 v178, v172, v173
	v_cvt_pk_bf16_f32 v179, v174, v175
	global_store_dwordx2 v193, v[178:179], s[28:29] offset:2048
	s_waitcnt vmcnt(31)
	v_lshlrev_b32_e32 v164, 16, v144
	v_and_b32_e32 v165, 0xffff0000, v144
	v_lshlrev_b32_e32 v166, 16, v145
	v_and_b32_e32 v167, 0xffff0000, v145
	v_pk_add_f32 v[184:185], v[184:185], v[164:165]
	v_pk_add_f32 v[186:187], v[186:187], v[166:167]
	v_lshlrev_b32_e32 v168, 16, v112
	v_and_b32_e32 v169, 0xffff0000, v112
	v_lshlrev_b32_e32 v170, 16, v113
	v_and_b32_e32 v171, 0xffff0000, v113
	v_pk_add_f32 v[184:185], v[184:185], v[168:169] neg_lo:[0,1] neg_hi:[0,1]
	v_pk_add_f32 v[186:187], v[186:187], v[170:171] neg_lo:[0,1] neg_hi:[0,1]
	v_pk_fma_f32 v[172:173], v[188:189], v[184:185], v[164:165] op_sel_hi:[0,1,1] neg_lo:[0,0,1] neg_hi:[0,0,1]
	v_pk_fma_f32 v[174:175], v[188:189], v[186:187], v[166:167] op_sel_hi:[0,1,1] neg_lo:[0,0,1] neg_hi:[0,0,1]
	v_cvt_pk_bf16_f32 v180, v172, v173
	v_cvt_pk_bf16_f32 v181, v174, v175
	v_add_u32_e32 v194, 0xb000, v190
	global_store_dwordx2 v194, v[180:181], s[28:29]
	s_waitcnt vmcnt(31)
	v_lshlrev_b32_e32 v164, 16, v146
	v_and_b32_e32 v165, 0xffff0000, v146
	v_lshlrev_b32_e32 v166, 16, v147
	v_and_b32_e32 v167, 0xffff0000, v147
	v_pk_add_f32 v[184:185], v[184:185], v[164:165]
	v_pk_add_f32 v[186:187], v[186:187], v[166:167]
	v_lshlrev_b32_e32 v168, 16, v114
	v_and_b32_e32 v169, 0xffff0000, v114
	v_lshlrev_b32_e32 v170, 16, v115
	v_and_b32_e32 v171, 0xffff0000, v115
	v_pk_add_f32 v[184:185], v[184:185], v[168:169] neg_lo:[0,1] neg_hi:[0,1]
	v_pk_add_f32 v[186:187], v[186:187], v[170:171] neg_lo:[0,1] neg_hi:[0,1]
	v_pk_fma_f32 v[172:173], v[188:189], v[184:185], v[164:165] op_sel_hi:[0,1,1] neg_lo:[0,0,1] neg_hi:[0,0,1]
	v_pk_fma_f32 v[174:175], v[188:189], v[186:187], v[166:167] op_sel_hi:[0,1,1] neg_lo:[0,0,1] neg_hi:[0,0,1]
	v_cvt_pk_bf16_f32 v182, v172, v173
	v_cvt_pk_bf16_f32 v183, v174, v175
	global_store_dwordx2 v194, v[182:183], s[28:29] offset:2048
	s_waitcnt vmcnt(31)
	v_lshlrev_b32_e32 v164, 16, v148
	v_and_b32_e32 v165, 0xffff0000, v148
	v_lshlrev_b32_e32 v166, 16, v149
	v_and_b32_e32 v167, 0xffff0000, v149
	v_pk_add_f32 v[184:185], v[184:185], v[164:165]
	v_pk_add_f32 v[186:187], v[186:187], v[166:167]
	v_lshlrev_b32_e32 v168, 16, v116
	v_and_b32_e32 v169, 0xffff0000, v116
	v_lshlrev_b32_e32 v170, 16, v117
	v_and_b32_e32 v171, 0xffff0000, v117
	v_pk_add_f32 v[184:185], v[184:185], v[168:169] neg_lo:[0,1] neg_hi:[0,1]
	v_pk_add_f32 v[186:187], v[186:187], v[170:171] neg_lo:[0,1] neg_hi:[0,1]
	v_pk_fma_f32 v[172:173], v[188:189], v[184:185], v[164:165] op_sel_hi:[0,1,1] neg_lo:[0,0,1] neg_hi:[0,0,1]
	v_pk_fma_f32 v[174:175], v[188:189], v[186:187], v[166:167] op_sel_hi:[0,1,1] neg_lo:[0,0,1] neg_hi:[0,0,1]
	v_cvt_pk_bf16_f32 v176, v172, v173
	v_cvt_pk_bf16_f32 v177, v174, v175
	v_add_u32_e32 v193, 0xc000, v190
	global_store_dwordx2 v193, v[176:177], s[28:29]
	s_waitcnt vmcnt(31)
	v_lshlrev_b32_e32 v164, 16, v150
	v_and_b32_e32 v165, 0xffff0000, v150
	v_lshlrev_b32_e32 v166, 16, v151
	v_and_b32_e32 v167, 0xffff0000, v151
	v_pk_add_f32 v[184:185], v[184:185], v[164:165]
	v_pk_add_f32 v[186:187], v[186:187], v[166:167]
	v_lshlrev_b32_e32 v168, 16, v118
	v_and_b32_e32 v169, 0xffff0000, v118
	v_lshlrev_b32_e32 v170, 16, v119
	v_and_b32_e32 v171, 0xffff0000, v119
	v_pk_add_f32 v[184:185], v[184:185], v[168:169] neg_lo:[0,1] neg_hi:[0,1]
	v_pk_add_f32 v[186:187], v[186:187], v[170:171] neg_lo:[0,1] neg_hi:[0,1]
	v_pk_fma_f32 v[172:173], v[188:189], v[184:185], v[164:165] op_sel_hi:[0,1,1] neg_lo:[0,0,1] neg_hi:[0,0,1]
	v_pk_fma_f32 v[174:175], v[188:189], v[186:187], v[166:167] op_sel_hi:[0,1,1] neg_lo:[0,0,1] neg_hi:[0,0,1]
	v_cvt_pk_bf16_f32 v178, v172, v173
	v_cvt_pk_bf16_f32 v179, v174, v175
	global_store_dwordx2 v193, v[178:179], s[28:29] offset:2048
	s_waitcnt vmcnt(31)
; #define GAS __attribute__((address_space(1)))
; __device__ __forceinline__ unsigned pk2(float lo, float hi) { const f32x2 v = {lo, hi}; return __builtin_bit_cast(unsigned, __builtin_convertvector(v, b16x2)); }
; template <int W>
; __device__ __forceinline__ void pool_item(const bf16* U, bf16* Z, int b, int t0, int g, int lane) {
;     ...
;     for (int i = 0; i < 32; ++i) { const int t = t0 + i;
;         const u32x2 v = *(const GAS u32x2*)(U + base + (size_t)t * D);
;         const float c0 = bf2f(v.x & 0xffffu), c1 = bf2f(v.x >> 16), c2 = bf2f(v.y & 0xffffu), c3 = bf2f(v.y >> 16);
;         s[0] += c0; s[1] += c1; s[2] += c2; s[3] += c3;
;         if (t - W >= 0) { const u32x2 o = *(const GAS u32x2*)(U + base + (size_t)(t - W) * D);
;             s[0] -= bf2f(o.x & 0xffffu); s[1] -= bf2f(o.x >> 16); s[2] -= bf2f(o.y & 0xffffu); s[3] -= bf2f(o.y >> 16); }
;         const float inv = 1.0f / (float)((t + 1) < W ? (t + 1) : W);
;         u32x2 w; w.x = pk2(s[0] * inv - c0, s[1] * inv - c1); w.y = pk2(s[2] * inv - c2, s[3] * inv - c3);
;         *(GAS u32x2*)(Z + base + (size_t)t * D) = w; }
; }
	v_lshlrev_b32_e32 v164, 16, v152
	v_and_b32_e32 v165, 0xffff0000, v152
	v_lshlrev_b32_e32 v166, 16, v153
	v_and_b32_e32 v167, 0xffff0000, v153
	v_pk_add_f32 v[184:185], v[184:185], v[164:165]
	v_pk_add_f32 v[186:187], v[186:187], v[166:167]
	v_lshlrev_b32_e32 v168, 16, v120
	v_and_b32_e32 v169, 0xffff0000, v120
	v_lshlrev_b32_e32 v170, 16, v121
	v_and_b32_e32 v171, 0xffff0000, v121
	v_pk_add_f32 v[184:185], v[184:185], v[168:169] neg_lo:[0,1] neg_hi:[0,1]
	v_pk_add_f32 v[186:187], v[186:187], v[170:171] neg_lo:[0,1] neg_hi:[0,1]
	v_pk_fma_f32 v[172:173], v[188:189], v[184:185], v[164:165] op_sel_hi:[0,1,1] neg_lo:[0,0,1] neg_hi:[0,0,1]
	v_pk_fma_f32 v[174:175], v[188:189], v[186:187], v[166:167] op_sel_hi:[0,1,1] neg_lo:[0,0,1] neg_hi:[0,0,1]
	v_cvt_pk_bf16_f32 v180, v172, v173
	v_cvt_pk_bf16_f32 v181, v174, v175
	v_add_u32_e32 v194, 0xd000, v190
	global_store_dwordx2 v194, v[180:181], s[28:29]
	s_waitcnt vmcnt(31)
	v_lshlrev_b32_e32 v164, 16, v154
	v_and_b32_e32 v165, 0xffff0000, v154
	v_lshlrev_b32_e32 v166, 16, v155
	v_and_b32_e32 v167, 0xffff0000, v155
	v_pk_add_f32 v[184:185], v[184:185], v[164:165]
	v_pk_add_f32 v[186:187], v[186:187], v[166:167]
	v_lshlrev_b32_e32 v168, 16, v122
	v_and_b32_e32 v169, 0xffff0000, v122
	v_lshlrev_b32_e32 v170, 16, v123
	v_and_b32_e32 v171, 0xffff0000, v123
	v_pk_add_f32 v[184:185], v[184:185], v[168:169] neg_lo:[0,1] neg_hi:[0,1]
	v_pk_add_f32 v[186:187], v[186:187], v[170:171] neg_lo:[0,1] neg_hi:[0,1]
	v_pk_fma_f32 v[172:173], v[188:189], v[184:185], v[164:165] op_sel_hi:[0,1,1] neg_lo:[0,0,1] neg_hi:[0,0,1]
	v_pk_fma_f32 v[174:175], v[188:189], v[186:187], v[166:167] op_sel_hi:[0,1,1] neg_lo:[0,0,1] neg_hi:[0,0,1]
	v_cvt_pk_bf16_f32 v182, v172, v173
	v_cvt_pk_bf16_f32 v183, v174, v175
	global_store_dwordx2 v194, v[182:183], s[28:29] offset:2048
	s_waitcnt vmcnt(31)
	v_lshlrev_b32_e32 v164, 16, v156
	v_and_b32_e32 v165, 0xffff0000, v156
	v_lshlrev_b32_e32 v166, 16, v157
	v_and_b32_e32 v167, 0xffff0000, v157
	v_pk_add_f32 v[184:185], v[184:185], v[164:165]
	v_pk_add_f32 v[186:187], v[186:187], v[166:167]
	v_lshlrev_b32_e32 v168, 16, v124
	v_and_b32_e32 v169, 0xffff0000, v124
	v_lshlrev_b32_e32 v170, 16, v125
	v_and_b32_e32 v171, 0xffff0000, v125
	v_pk_add_f32 v[184:185], v[184:185], v[168:169] neg_lo:[0,1] neg_hi:[0,1]
	v_pk_add_f32 v[186:187], v[186:187], v[170:171] neg_lo:[0,1] neg_hi:[0,1]
	v_pk_fma_f32 v[172:173], v[188:189], v[184:185], v[164:165] op_sel_hi:[0,1,1] neg_lo:[0,0,1] neg_hi:[0,0,1]
	v_pk_fma_f32 v[174:175], v[188:189], v[186:187], v[166:167] op_sel_hi:[0,1,1] neg_lo:[0,0,1] neg_hi:[0,0,1]
	v_cvt_pk_bf16_f32 v176, v172, v173
	v_cvt_pk_bf16_f32 v177, v174, v175
	v_add_u32_e32 v193, 0xe000, v190
	global_store_dwordx2 v193, v[176:177], s[28:29]
	s_waitcnt vmcnt(31)
	v_lshlrev_b32_e32 v164, 16, v158
	v_and_b32_e32 v165, 0xffff0000, v158
	v_lshlrev_b32_e32 v166, 16, v159
	v_and_b32_e32 v167, 0xffff0000, v159
	v_pk_add_f32 v[184:185], v[184:185], v[164:165]
	v_pk_add_f32 v[186:187], v[186:187], v[166:167]
	v_lshlrev_b32_e32 v168, 16, v126
	v_and_b32_e32 v169, 0xffff0000, v126
	v_lshlrev_b32_e32 v170, 16, v127
	v_and_b32_e32 v171, 0xffff0000, v127
	v_pk_add_f32 v[184:185], v[184:185], v[168:169] neg_lo:[0,1] neg_hi:[0,1]
	v_pk_add_f32 v[186:187], v[186:187], v[170:171] neg_lo:[0,1] neg_hi:[0,1]
	v_pk_fma_f32 v[172:173], v[188:189], v[184:185], v[164:165] op_sel_hi:[0,1,1] neg_lo:[0,0,1] neg_hi:[0,0,1]
	v_pk_fma_f32 v[174:175], v[188:189], v[186:187], v[166:167] op_sel_hi:[0,1,1] neg_lo:[0,0,1] neg_hi:[0,0,1]
	v_cvt_pk_bf16_f32 v178, v172, v173
	v_cvt_pk_bf16_f32 v179, v174, v175
	global_store_dwordx2 v193, v[178:179], s[28:29] offset:2048
	s_waitcnt vmcnt(31)
	v_lshlrev_b32_e32 v164, 16, v160
	v_and_b32_e32 v165, 0xffff0000, v160
	v_lshlrev_b32_e32 v166, 16, v161
	v_and_b32_e32 v167, 0xffff0000, v161
	v_pk_add_f32 v[184:185], v[184:185], v[164:165]
	v_pk_add_f32 v[186:187], v[186:187], v[166:167]
	v_lshlrev_b32_e32 v168, 16, v128
	v_and_b32_e32 v169, 0xffff0000, v128
	v_lshlrev_b32_e32 v170, 16, v129
	v_and_b32_e32 v171, 0xffff0000, v129
	v_pk_add_f32 v[184:185], v[184:185], v[168:169] neg_lo:[0,1] neg_hi:[0,1]
	v_pk_add_f32 v[186:187], v[186:187], v[170:171] neg_lo:[0,1] neg_hi:[0,1]
	v_pk_fma_f32 v[172:173], v[188:189], v[184:185], v[164:165] op_sel_hi:[0,1,1] neg_lo:[0,0,1] neg_hi:[0,0,1]
	v_pk_fma_f32 v[174:175], v[188:189], v[186:187], v[166:167] op_sel_hi:[0,1,1] neg_lo:[0,0,1] neg_hi:[0,0,1]
	v_cvt_pk_bf16_f32 v180, v172, v173
	v_cvt_pk_bf16_f32 v181, v174, v175
	v_add_u32_e32 v194, 0xf000, v190
	global_store_dwordx2 v194, v[180:181], s[28:29]
	s_waitcnt vmcnt(31)
	v_lshlrev_b32_e32 v164, 16, v162
	v_and_b32_e32 v165, 0xffff0000, v162
	v_lshlrev_b32_e32 v166, 16, v163
	v_and_b32_e32 v167, 0xffff0000, v163
	v_pk_add_f32 v[184:185], v[184:185], v[164:165]
	v_pk_add_f32 v[186:187], v[186:187], v[166:167]
	v_lshlrev_b32_e32 v168, 16, v130
	v_and_b32_e32 v169, 0xffff0000, v130
	v_lshlrev_b32_e32 v170, 16, v131
	v_and_b32_e32 v171, 0xffff0000, v131
	v_pk_add_f32 v[184:185], v[184:185], v[168:169] neg_lo:[0,1] neg_hi:[0,1]
	v_pk_add_f32 v[186:187], v[186:187], v[170:171] neg_lo:[0,1] neg_hi:[0,1]
	v_pk_fma_f32 v[172:173], v[188:189], v[184:185], v[164:165] op_sel_hi:[0,1,1] neg_lo:[0,0,1] neg_hi:[0,0,1]
	v_pk_fma_f32 v[174:175], v[188:189], v[186:187], v[166:167] op_sel_hi:[0,1,1] neg_lo:[0,0,1] neg_hi:[0,0,1]
	v_cvt_pk_bf16_f32 v182, v172, v173
	v_cvt_pk_bf16_f32 v183, v174, v175
	global_store_dwordx2 v194, v[182:183], s[28:29] offset:2048
	s_branch .LBB0_861
; #define GAS __attribute__((address_space(1)))
; __device__ __forceinline__ unsigned pk2(float lo, float hi) { const f32x2 v = {lo, hi}; return __builtin_bit_cast(unsigned, __builtin_convertvector(v, b16x2)); }
; template <int W>
; __device__ __forceinline__ void pool_item(const bf16* U, bf16* Z, int b, int t0, int g, int lane) {
;     const size_t base = (size_t)b * SEQ * D + 256 * g + 4 * lane;
;     float s[4] = {0.f, 0.f, 0.f, 0.f};
; #pragma unroll
;     for (int j = 1; j <= W; ++j) { const int t = t0 - j; if (t >= 0) { const u32x2 v = *(const GAS u32x2*)(U + base + (size_t)t * D);
;             s[0] += bf2f(v.x & 0xffffu); s[1] += bf2f(v.x >> 16); s[2] += bf2f(v.y & 0xffffu); s[3] += bf2f(v.y >> 16); } }
; #pragma unroll 8
;     for (int i = 0; i < 32; ++i) { const int t = t0 + i;
;         const u32x2 v = *(const GAS u32x2*)(U + base + (size_t)t * D);
;         const float c0 = bf2f(v.x & 0xffffu), c1 = bf2f(v.x >> 16), c2 = bf2f(v.y & 0xffffu), c3 = bf2f(v.y >> 16);
;         s[0] += c0; s[1] += c1; s[2] += c2; s[3] += c3;
;         if (t - W >= 0) { const u32x2 o = *(const GAS u32x2*)(U + base + (size_t)(t - W) * D);
;             s[0] -= bf2f(o.x & 0xffffu); s[1] -= bf2f(o.x >> 16); s[2] -= bf2f(o.y & 0xffffu); s[3] -= bf2f(o.y >> 16); }
;         const float inv = 1.0f / (float)((t + 1) < W ? (t + 1) : W);
;         u32x2 w; w.x = pk2(s[0] * inv - c0, s[1] * inv - c1); w.y = pk2(s[2] * inv - c2, s[3] * inv - c3);
;         *(GAS u32x2*)(Z + base + (size_t)t * D) = w; }
; }
.Lpool_w8:
	v_mov_b32_e32 v188, 0x3e000000
	v_mov_b32_e32 v189, v188
	v_add_u32_e32 v192, 0x4000, v190
	global_load_dwordx2 v[84:85], v192, s[10:11]
	global_load_dwordx2 v[86:87], v192, s[10:11] offset:2048
	v_add_u32_e32 v191, 0x5000, v190
	global_load_dwordx2 v[88:89], v191, s[10:11]
	global_load_dwordx2 v[90:91], v191, s[10:11] offset:2048
	v_add_u32_e32 v192, 0x6000, v190
	global_load_dwordx2 v[92:93], v192, s[10:11]
	global_load_dwordx2 v[94:95], v192, s[10:11] offset:2048
	v_add_u32_e32 v191, 0x7000, v190
	global_load_dwordx2 v[96:97], v191, s[10:11]
	global_load_dwordx2 v[98:99], v191, s[10:11] offset:2048
	v_add_u32_e32 v192, 0x8000, v190
	global_load_dwordx2 v[100:101], v192, s[10:11]
	global_load_dwordx2 v[102:103], v192, s[10:11] offset:2048
	v_add_u32_e32 v191, 0x9000, v190
	global_load_dwordx2 v[104:105], v191, s[10:11]
	global_load_dwordx2 v[106:107], v191, s[10:11] offset:2048
	v_add_u32_e32 v192, 0xa000, v190
	global_load_dwordx2 v[108:109], v192, s[10:11]
	global_load_dwordx2 v[110:111], v192, s[10:11] offset:2048
	v_add_u32_e32 v191, 0xb000, v190
	global_load_dwordx2 v[112:113], v191, s[10:11]
	global_load_dwordx2 v[114:115], v191, s[10:11] offset:2048
	v_add_u32_e32 v192, 0xc000, v190
	global_load_dwordx2 v[116:117], v192, s[10:11]
	global_load_dwordx2 v[118:119], v192, s[10:11] offset:2048
	v_add_u32_e32 v191, 0xd000, v190
	global_load_dwordx2 v[120:121], v191, s[10:11]
	global_load_dwordx2 v[122:123], v191, s[10:11] offset:2048
	v_add_u32_e32 v192, 0xe000, v190
	global_load_dwordx2 v[124:125], v192, s[10:11]
	global_load_dwordx2 v[126:127], v192, s[10:11] offset:2048
	v_add_u32_e32 v191, 0xf000, v190
	global_load_dwordx2 v[128:129], v191, s[10:11]
	global_load_dwordx2 v[130:131], v191, s[10:11] offset:2048
	v_add_u32_e32 v192, 0x10000, v190
	global_load_dwordx2 v[132:133], v192, s[10:11]
	global_load_dwordx2 v[134:135], v192, s[10:11] offset:2048
	v_add_u32_e32 v191, 0x11000, v190
	global_load_dwordx2 v[136:137], v191, s[10:11]
	global_load_dwordx2 v[138:139], v191, s[10:11] offset:2048
	v_add_u32_e32 v192, 0x12000, v190
	global_load_dwordx2 v[140:141], v192, s[10:11]
	global_load_dwordx2 v[142:143], v192, s[10:11] offset:2048
	v_add_u32_e32 v191, 0x13000, v190
	global_load_dwordx2 v[144:145], v191, s[10:11]
	global_load_dwordx2 v[146:147], v191, s[10:11] offset:2048
	v_add_u32_e32 v192, 0x14000, v190
	global_load_dwordx2 v[148:149], v192, s[10:11]
	global_load_dwordx2 v[150:151], v192, s[10:11] offset:2048
	v_add_u32_e32 v191, 0x15000, v190
	global_load_dwordx2 v[152:153], v191, s[10:11]
	global_load_dwordx2 v[154:155], v191, s[10:11] offset:2048
	v_add_u32_e32 v192, 0x16000, v190
	global_load_dwordx2 v[156:157], v192, s[10:11]
	global_load_dwordx2 v[158:159], v192, s[10:11] offset:2048
	v_add_u32_e32 v191, 0x17000, v190
	global_load_dwordx2 v[160:161], v191, s[10:11]
	global_load_dwordx2 v[162:163], v191, s[10:11] offset:2048
	s_waitcnt vmcnt(32)
	v_lshlrev_b32_e32 v164, 16, v98
	v_and_b32_e32 v165, 0xffff0000, v98
	v_lshlrev_b32_e32 v166, 16, v99
	v_and_b32_e32 v167, 0xffff0000, v99
	v_pk_add_f32 v[184:185], v[164:165], 0 op_sel_hi:[1,0]
	v_pk_add_f32 v[186:187], v[166:167], 0 op_sel_hi:[1,0]
	v_lshlrev_b32_e32 v164, 16, v96
	v_and_b32_e32 v165, 0xffff0000, v96
	v_lshlrev_b32_e32 v166, 16, v97
	v_and_b32_e32 v167, 0xffff0000, v97
	v_pk_add_f32 v[184:185], v[184:185], v[164:165]
	v_pk_add_f32 v[186:187], v[186:187], v[166:167]
	v_lshlrev_b32_e32 v164, 16, v94
	v_and_b32_e32 v165, 0xffff0000, v94
	v_lshlrev_b32_e32 v166, 16, v95
	v_and_b32_e32 v167, 0xffff0000, v95
	v_pk_add_f32 v[184:185], v[184:185], v[164:165]
	v_pk_add_f32 v[186:187], v[186:187], v[166:167]
	v_lshlrev_b32_e32 v164, 16, v92
	v_and_b32_e32 v165, 0xffff0000, v92
	v_lshlrev_b32_e32 v166, 16, v93
	v_and_b32_e32 v167, 0xffff0000, v93
	v_pk_add_f32 v[184:185], v[184:185], v[164:165]
	v_pk_add_f32 v[186:187], v[186:187], v[166:167]
	v_lshlrev_b32_e32 v164, 16, v90
	v_and_b32_e32 v165, 0xffff0000, v90
	v_lshlrev_b32_e32 v166, 16, v91
	v_and_b32_e32 v167, 0xffff0000, v91
	v_pk_add_f32 v[184:185], v[184:185], v[164:165]
	v_pk_add_f32 v[186:187], v[186:187], v[166:167]
	v_lshlrev_b32_e32 v164, 16, v88
	v_and_b32_e32 v165, 0xffff0000, v88
	v_lshlrev_b32_e32 v166, 16, v89
	v_and_b32_e32 v167, 0xffff0000, v89
	v_pk_add_f32 v[184:185], v[184:185], v[164:165]
	v_pk_add_f32 v[186:187], v[186:187], v[166:167]
	v_lshlrev_b32_e32 v164, 16, v86
	v_and_b32_e32 v165, 0xffff0000, v86
	v_lshlrev_b32_e32 v166, 16, v87
	v_and_b32_e32 v167, 0xffff0000, v87
	v_pk_add_f32 v[184:185], v[184:185], v[164:165]
	v_pk_add_f32 v[186:187], v[186:187], v[166:167]
	v_lshlrev_b32_e32 v164, 16, v84
	v_and_b32_e32 v165, 0xffff0000, v84
	v_lshlrev_b32_e32 v166, 16, v85
	v_and_b32_e32 v167, 0xffff0000, v85
	v_pk_add_f32 v[184:185], v[184:185], v[164:165]
	v_pk_add_f32 v[186:187], v[186:187], v[166:167]
	s_waitcnt vmcnt(31)
	v_lshlrev_b32_e32 v164, 16, v100
	v_and_b32_e32 v165, 0xffff0000, v100
	v_lshlrev_b32_e32 v166, 16, v101
	v_and_b32_e32 v167, 0xffff0000, v101
	v_pk_add_f32 v[184:185], v[184:185], v[164:165]
	v_pk_add_f32 v[186:187], v[186:187], v[166:167]
	v_lshlrev_b32_e32 v168, 16, v84
	v_and_b32_e32 v169, 0xffff0000, v84
	v_lshlrev_b32_e32 v170, 16, v85
	v_and_b32_e32 v171, 0xffff0000, v85
	v_pk_add_f32 v[184:185], v[184:185], v[168:169] neg_lo:[0,1] neg_hi:[0,1]
	v_pk_add_f32 v[186:187], v[186:187], v[170:171] neg_lo:[0,1] neg_hi:[0,1]
	v_pk_fma_f32 v[172:173], v[188:189], v[184:185], v[164:165] op_sel_hi:[0,1,1] neg_lo:[0,0,1] neg_hi:[0,0,1]
	v_pk_fma_f32 v[174:175], v[188:189], v[186:187], v[166:167] op_sel_hi:[0,1,1] neg_lo:[0,0,1] neg_hi:[0,0,1]
	v_cvt_pk_bf16_f32 v176, v172, v173
	v_cvt_pk_bf16_f32 v177, v174, v175
	global_store_dwordx2 v190, v[176:177], s[28:29]
	s_waitcnt vmcnt(31)
; #define GAS __attribute__((address_space(1)))
; __device__ __forceinline__ unsigned pk2(float lo, float hi) { const f32x2 v = {lo, hi}; return __builtin_bit_cast(unsigned, __builtin_convertvector(v, b16x2)); }
; template <int W>
; __device__ __forceinline__ void pool_item(const bf16* U, bf16* Z, int b, int t0, int g, int lane) {
;     ...
;     for (int i = 0; i < 32; ++i) { const int t = t0 + i;
;         const u32x2 v = *(const GAS u32x2*)(U + base + (size_t)t * D);
;         const float c0 = bf2f(v.x & 0xffffu), c1 = bf2f(v.x >> 16), c2 = bf2f(v.y & 0xffffu), c3 = bf2f(v.y >> 16);
;         s[0] += c0; s[1] += c1; s[2] += c2; s[3] += c3;
;         if (t - W >= 0) { const u32x2 o = *(const GAS u32x2*)(U + base + (size_t)(t - W) * D);
;             s[0] -= bf2f(o.x & 0xffffu); s[1] -= bf2f(o.x >> 16); s[2] -= bf2f(o.y & 0xffffu); s[3] -= bf2f(o.y >> 16); }
;         const float inv = 1.0f / (float)((t + 1) < W ? (t + 1) : W);
;         u32x2 w; w.x = pk2(s[0] * inv - c0, s[1] * inv - c1); w.y = pk2(s[2] * inv - c2, s[3] * inv - c3);
;         *(GAS u32x2*)(Z + base + (size_t)t * D) = w; }
; }
	v_lshlrev_b32_e32 v164, 16, v102
	v_and_b32_e32 v165, 0xffff0000, v102
	v_lshlrev_b32_e32 v166, 16, v103
	v_and_b32_e32 v167, 0xffff0000, v103
	v_pk_add_f32 v[184:185], v[184:185], v[164:165]
	v_pk_add_f32 v[186:187], v[186:187], v[166:167]
	v_lshlrev_b32_e32 v168, 16, v86
	v_and_b32_e32 v169, 0xffff0000, v86
	v_lshlrev_b32_e32 v170, 16, v87
	v_and_b32_e32 v171, 0xffff0000, v87
	v_pk_add_f32 v[184:185], v[184:185], v[168:169] neg_lo:[0,1] neg_hi:[0,1]
	v_pk_add_f32 v[186:187], v[186:187], v[170:171] neg_lo:[0,1] neg_hi:[0,1]
	v_pk_fma_f32 v[172:173], v[188:189], v[184:185], v[164:165] op_sel_hi:[0,1,1] neg_lo:[0,0,1] neg_hi:[0,0,1]
	v_pk_fma_f32 v[174:175], v[188:189], v[186:187], v[166:167] op_sel_hi:[0,1,1] neg_lo:[0,0,1] neg_hi:[0,0,1]
	v_cvt_pk_bf16_f32 v178, v172, v173
	v_cvt_pk_bf16_f32 v179, v174, v175
	global_store_dwordx2 v190, v[178:179], s[28:29] offset:2048
	s_waitcnt vmcnt(31)
	v_lshlrev_b32_e32 v164, 16, v104
	v_and_b32_e32 v165, 0xffff0000, v104
	v_lshlrev_b32_e32 v166, 16, v105
	v_and_b32_e32 v167, 0xffff0000, v105
	v_pk_add_f32 v[184:185], v[184:185], v[164:165]
	v_pk_add_f32 v[186:187], v[186:187], v[166:167]
	v_lshlrev_b32_e32 v168, 16, v88
	v_and_b32_e32 v169, 0xffff0000, v88
	v_lshlrev_b32_e32 v170, 16, v89
	v_and_b32_e32 v171, 0xffff0000, v89
	v_pk_add_f32 v[184:185], v[184:185], v[168:169] neg_lo:[0,1] neg_hi:[0,1]
	v_pk_add_f32 v[186:187], v[186:187], v[170:171] neg_lo:[0,1] neg_hi:[0,1]
	v_pk_fma_f32 v[172:173], v[188:189], v[184:185], v[164:165] op_sel_hi:[0,1,1] neg_lo:[0,0,1] neg_hi:[0,0,1]
	v_pk_fma_f32 v[174:175], v[188:189], v[186:187], v[166:167] op_sel_hi:[0,1,1] neg_lo:[0,0,1] neg_hi:[0,0,1]
	v_cvt_pk_bf16_f32 v180, v172, v173
	v_cvt_pk_bf16_f32 v181, v174, v175
	v_add_u32_e32 v194, 0x1000, v190
	global_store_dwordx2 v194, v[180:181], s[28:29]
	s_waitcnt vmcnt(31)
	v_lshlrev_b32_e32 v164, 16, v106
	v_and_b32_e32 v165, 0xffff0000, v106
	v_lshlrev_b32_e32 v166, 16, v107
	v_and_b32_e32 v167, 0xffff0000, v107
	v_pk_add_f32 v[184:185], v[184:185], v[164:165]
	v_pk_add_f32 v[186:187], v[186:187], v[166:167]
	v_lshlrev_b32_e32 v168, 16, v90
	v_and_b32_e32 v169, 0xffff0000, v90
	v_lshlrev_b32_e32 v170, 16, v91
	v_and_b32_e32 v171, 0xffff0000, v91
	v_pk_add_f32 v[184:185], v[184:185], v[168:169] neg_lo:[0,1] neg_hi:[0,1]
	v_pk_add_f32 v[186:187], v[186:187], v[170:171] neg_lo:[0,1] neg_hi:[0,1]
	v_pk_fma_f32 v[172:173], v[188:189], v[184:185], v[164:165] op_sel_hi:[0,1,1] neg_lo:[0,0,1] neg_hi:[0,0,1]
	v_pk_fma_f32 v[174:175], v[188:189], v[186:187], v[166:167] op_sel_hi:[0,1,1] neg_lo:[0,0,1] neg_hi:[0,0,1]
	v_cvt_pk_bf16_f32 v182, v172, v173
	v_cvt_pk_bf16_f32 v183, v174, v175
	global_store_dwordx2 v194, v[182:183], s[28:29] offset:2048
	s_waitcnt vmcnt(31)
	v_lshlrev_b32_e32 v164, 16, v108
	v_and_b32_e32 v165, 0xffff0000, v108
	v_lshlrev_b32_e32 v166, 16, v109
	v_and_b32_e32 v167, 0xffff0000, v109
	v_pk_add_f32 v[184:185], v[184:185], v[164:165]
	v_pk_add_f32 v[186:187], v[186:187], v[166:167]
	v_lshlrev_b32_e32 v168, 16, v92
	v_and_b32_e32 v169, 0xffff0000, v92
	v_lshlrev_b32_e32 v170, 16, v93
	v_and_b32_e32 v171, 0xffff0000, v93
	v_pk_add_f32 v[184:185], v[184:185], v[168:169] neg_lo:[0,1] neg_hi:[0,1]
	v_pk_add_f32 v[186:187], v[186:187], v[170:171] neg_lo:[0,1] neg_hi:[0,1]
	v_pk_fma_f32 v[172:173], v[188:189], v[184:185], v[164:165] op_sel_hi:[0,1,1] neg_lo:[0,0,1] neg_hi:[0,0,1]
	v_pk_fma_f32 v[174:175], v[188:189], v[186:187], v[166:167] op_sel_hi:[0,1,1] neg_lo:[0,0,1] neg_hi:[0,0,1]
	v_cvt_pk_bf16_f32 v176, v172, v173
	v_cvt_pk_bf16_f32 v177, v174, v175
	v_add_u32_e32 v193, 0x2000, v190
	global_store_dwordx2 v193, v[176:177], s[28:29]
	s_waitcnt vmcnt(31)
	v_lshlrev_b32_e32 v164, 16, v110
	v_and_b32_e32 v165, 0xffff0000, v110
	v_lshlrev_b32_e32 v166, 16, v111
	v_and_b32_e32 v167, 0xffff0000, v111
	v_pk_add_f32 v[184:185], v[184:185], v[164:165]
	v_pk_add_f32 v[186:187], v[186:187], v[166:167]
	v_lshlrev_b32_e32 v168, 16, v94
	v_and_b32_e32 v169, 0xffff0000, v94
	v_lshlrev_b32_e32 v170, 16, v95
	v_and_b32_e32 v171, 0xffff0000, v95
	v_pk_add_f32 v[184:185], v[184:185], v[168:169] neg_lo:[0,1] neg_hi:[0,1]
	v_pk_add_f32 v[186:187], v[186:187], v[170:171] neg_lo:[0,1] neg_hi:[0,1]
	v_pk_fma_f32 v[172:173], v[188:189], v[184:185], v[164:165] op_sel_hi:[0,1,1] neg_lo:[0,0,1] neg_hi:[0,0,1]
	v_pk_fma_f32 v[174:175], v[188:189], v[186:187], v[166:167] op_sel_hi:[0,1,1] neg_lo:[0,0,1] neg_hi:[0,0,1]
	v_cvt_pk_bf16_f32 v178, v172, v173
	v_cvt_pk_bf16_f32 v179, v174, v175
	global_store_dwordx2 v193, v[178:179], s[28:29] offset:2048
	s_waitcnt vmcnt(31)
	v_lshlrev_b32_e32 v164, 16, v112
	v_and_b32_e32 v165, 0xffff0000, v112
	v_lshlrev_b32_e32 v166, 16, v113
	v_and_b32_e32 v167, 0xffff0000, v113
	v_pk_add_f32 v[184:185], v[184:185], v[164:165]
	v_pk_add_f32 v[186:187], v[186:187], v[166:167]
	v_lshlrev_b32_e32 v168, 16, v96
	v_and_b32_e32 v169, 0xffff0000, v96
	v_lshlrev_b32_e32 v170, 16, v97
	v_and_b32_e32 v171, 0xffff0000, v97
	v_pk_add_f32 v[184:185], v[184:185], v[168:169] neg_lo:[0,1] neg_hi:[0,1]
	v_pk_add_f32 v[186:187], v[186:187], v[170:171] neg_lo:[0,1] neg_hi:[0,1]
	v_pk_fma_f32 v[172:173], v[188:189], v[184:185], v[164:165] op_sel_hi:[0,1,1] neg_lo:[0,0,1] neg_hi:[0,0,1]
	v_pk_fma_f32 v[174:175], v[188:189], v[186:187], v[166:167] op_sel_hi:[0,1,1] neg_lo:[0,0,1] neg_hi:[0,0,1]
	v_cvt_pk_bf16_f32 v180, v172, v173
	v_cvt_pk_bf16_f32 v181, v174, v175
	v_add_u32_e32 v194, 0x3000, v190
	global_store_dwordx2 v194, v[180:181], s[28:29]
	s_waitcnt vmcnt(31)
; #define GAS __attribute__((address_space(1)))
; __device__ __forceinline__ unsigned pk2(float lo, float hi) { const f32x2 v = {lo, hi}; return __builtin_bit_cast(unsigned, __builtin_convertvector(v, b16x2)); }
; template <int W>
; __device__ __forceinline__ void pool_item(const bf16* U, bf16* Z, int b, int t0, int g, int lane) {
;     ...
;     for (int i = 0; i < 32; ++i) { const int t = t0 + i;
;         const u32x2 v = *(const GAS u32x2*)(U + base + (size_t)t * D);
;         const float c0 = bf2f(v.x & 0xffffu), c1 = bf2f(v.x >> 16), c2 = bf2f(v.y & 0xffffu), c3 = bf2f(v.y >> 16);
;         s[0] += c0; s[1] += c1; s[2] += c2; s[3] += c3;
;         if (t - W >= 0) { const u32x2 o = *(const GAS u32x2*)(U + base + (size_t)(t - W) * D);
;             s[0] -= bf2f(o.x & 0xffffu); s[1] -= bf2f(o.x >> 16); s[2] -= bf2f(o.y & 0xffffu); s[3] -= bf2f(o.y >> 16); }
;         const float inv = 1.0f / (float)((t + 1) < W ? (t + 1) : W);
;         u32x2 w; w.x = pk2(s[0] * inv - c0, s[1] * inv - c1); w.y = pk2(s[2] * inv - c2, s[3] * inv - c3);
;         *(GAS u32x2*)(Z + base + (size_t)t * D) = w; }
; }
	v_lshlrev_b32_e32 v164, 16, v114
	v_and_b32_e32 v165, 0xffff0000, v114
	v_lshlrev_b32_e32 v166, 16, v115
	v_and_b32_e32 v167, 0xffff0000, v115
	v_pk_add_f32 v[184:185], v[184:185], v[164:165]
	v_pk_add_f32 v[186:187], v[186:187], v[166:167]
	v_lshlrev_b32_e32 v168, 16, v98
	v_and_b32_e32 v169, 0xffff0000, v98
	v_lshlrev_b32_e32 v170, 16, v99
	v_and_b32_e32 v171, 0xffff0000, v99
	v_pk_add_f32 v[184:185], v[184:185], v[168:169] neg_lo:[0,1] neg_hi:[0,1]
	v_pk_add_f32 v[186:187], v[186:187], v[170:171] neg_lo:[0,1] neg_hi:[0,1]
	v_pk_fma_f32 v[172:173], v[188:189], v[184:185], v[164:165] op_sel_hi:[0,1,1] neg_lo:[0,0,1] neg_hi:[0,0,1]
	v_pk_fma_f32 v[174:175], v[188:189], v[186:187], v[166:167] op_sel_hi:[0,1,1] neg_lo:[0,0,1] neg_hi:[0,0,1]
	v_cvt_pk_bf16_f32 v182, v172, v173
	v_cvt_pk_bf16_f32 v183, v174, v175
	global_store_dwordx2 v194, v[182:183], s[28:29] offset:2048
	s_waitcnt vmcnt(31)
	v_lshlrev_b32_e32 v164, 16, v116
	v_and_b32_e32 v165, 0xffff0000, v116
	v_lshlrev_b32_e32 v166, 16, v117
	v_and_b32_e32 v167, 0xffff0000, v117
	v_pk_add_f32 v[184:185], v[184:185], v[164:165]
	v_pk_add_f32 v[186:187], v[186:187], v[166:167]
	v_lshlrev_b32_e32 v168, 16, v100
	v_and_b32_e32 v169, 0xffff0000, v100
	v_lshlrev_b32_e32 v170, 16, v101
	v_and_b32_e32 v171, 0xffff0000, v101
	v_pk_add_f32 v[184:185], v[184:185], v[168:169] neg_lo:[0,1] neg_hi:[0,1]
	v_pk_add_f32 v[186:187], v[186:187], v[170:171] neg_lo:[0,1] neg_hi:[0,1]
	v_pk_fma_f32 v[172:173], v[188:189], v[184:185], v[164:165] op_sel_hi:[0,1,1] neg_lo:[0,0,1] neg_hi:[0,0,1]
	v_pk_fma_f32 v[174:175], v[188:189], v[186:187], v[166:167] op_sel_hi:[0,1,1] neg_lo:[0,0,1] neg_hi:[0,0,1]
	v_cvt_pk_bf16_f32 v176, v172, v173
	v_cvt_pk_bf16_f32 v177, v174, v175
	v_add_u32_e32 v193, 0x4000, v190
	global_store_dwordx2 v193, v[176:177], s[28:29]
	s_waitcnt vmcnt(31)
	v_lshlrev_b32_e32 v164, 16, v118
	v_and_b32_e32 v165, 0xffff0000, v118
	v_lshlrev_b32_e32 v166, 16, v119
	v_and_b32_e32 v167, 0xffff0000, v119
	v_pk_add_f32 v[184:185], v[184:185], v[164:165]
	v_pk_add_f32 v[186:187], v[186:187], v[166:167]
	v_lshlrev_b32_e32 v168, 16, v102
	v_and_b32_e32 v169, 0xffff0000, v102
	v_lshlrev_b32_e32 v170, 16, v103
	v_and_b32_e32 v171, 0xffff0000, v103
	v_pk_add_f32 v[184:185], v[184:185], v[168:169] neg_lo:[0,1] neg_hi:[0,1]
	v_pk_add_f32 v[186:187], v[186:187], v[170:171] neg_lo:[0,1] neg_hi:[0,1]
	v_pk_fma_f32 v[172:173], v[188:189], v[184:185], v[164:165] op_sel_hi:[0,1,1] neg_lo:[0,0,1] neg_hi:[0,0,1]
	v_pk_fma_f32 v[174:175], v[188:189], v[186:187], v[166:167] op_sel_hi:[0,1,1] neg_lo:[0,0,1] neg_hi:[0,0,1]
	v_cvt_pk_bf16_f32 v178, v172, v173
	v_cvt_pk_bf16_f32 v179, v174, v175
	global_store_dwordx2 v193, v[178:179], s[28:29] offset:2048
	s_waitcnt vmcnt(31)
	v_lshlrev_b32_e32 v164, 16, v120
	v_and_b32_e32 v165, 0xffff0000, v120
	v_lshlrev_b32_e32 v166, 16, v121
	v_and_b32_e32 v167, 0xffff0000, v121
	v_pk_add_f32 v[184:185], v[184:185], v[164:165]
	v_pk_add_f32 v[186:187], v[186:187], v[166:167]
	v_lshlrev_b32_e32 v168, 16, v104
	v_and_b32_e32 v169, 0xffff0000, v104
	v_lshlrev_b32_e32 v170, 16, v105
	v_and_b32_e32 v171, 0xffff0000, v105
	v_pk_add_f32 v[184:185], v[184:185], v[168:169] neg_lo:[0,1] neg_hi:[0,1]
	v_pk_add_f32 v[186:187], v[186:187], v[170:171] neg_lo:[0,1] neg_hi:[0,1]
	v_pk_fma_f32 v[172:173], v[188:189], v[184:185], v[164:165] op_sel_hi:[0,1,1] neg_lo:[0,0,1] neg_hi:[0,0,1]
	v_pk_fma_f32 v[174:175], v[188:189], v[186:187], v[166:167] op_sel_hi:[0,1,1] neg_lo:[0,0,1] neg_hi:[0,0,1]
	v_cvt_pk_bf16_f32 v180, v172, v173
	v_cvt_pk_bf16_f32 v181, v174, v175
	v_add_u32_e32 v194, 0x5000, v190
	global_store_dwordx2 v194, v[180:181], s[28:29]
	s_waitcnt vmcnt(31)
	v_lshlrev_b32_e32 v164, 16, v122
	v_and_b32_e32 v165, 0xffff0000, v122
	v_lshlrev_b32_e32 v166, 16, v123
	v_and_b32_e32 v167, 0xffff0000, v123
	v_pk_add_f32 v[184:185], v[184:185], v[164:165]
	v_pk_add_f32 v[186:187], v[186:187], v[166:167]
	v_lshlrev_b32_e32 v168, 16, v106
	v_and_b32_e32 v169, 0xffff0000, v106
	v_lshlrev_b32_e32 v170, 16, v107
	v_and_b32_e32 v171, 0xffff0000, v107
	v_pk_add_f32 v[184:185], v[184:185], v[168:169] neg_lo:[0,1] neg_hi:[0,1]
	v_pk_add_f32 v[186:187], v[186:187], v[170:171] neg_lo:[0,1] neg_hi:[0,1]
	v_pk_fma_f32 v[172:173], v[188:189], v[184:185], v[164:165] op_sel_hi:[0,1,1] neg_lo:[0,0,1] neg_hi:[0,0,1]
	v_pk_fma_f32 v[174:175], v[188:189], v[186:187], v[166:167] op_sel_hi:[0,1,1] neg_lo:[0,0,1] neg_hi:[0,0,1]
	v_cvt_pk_bf16_f32 v182, v172, v173
	v_cvt_pk_bf16_f32 v183, v174, v175
	global_store_dwordx2 v194, v[182:183], s[28:29] offset:2048
	s_waitcnt vmcnt(31)
	v_lshlrev_b32_e32 v164, 16, v124
	v_and_b32_e32 v165, 0xffff0000, v124
	v_lshlrev_b32_e32 v166, 16, v125
	v_and_b32_e32 v167, 0xffff0000, v125
	v_pk_add_f32 v[184:185], v[184:185], v[164:165]
	v_pk_add_f32 v[186:187], v[186:187], v[166:167]
	v_lshlrev_b32_e32 v168, 16, v108
	v_and_b32_e32 v169, 0xffff0000, v108
	v_lshlrev_b32_e32 v170, 16, v109
	v_and_b32_e32 v171, 0xffff0000, v109
	v_pk_add_f32 v[184:185], v[184:185], v[168:169] neg_lo:[0,1] neg_hi:[0,1]
	v_pk_add_f32 v[186:187], v[186:187], v[170:171] neg_lo:[0,1] neg_hi:[0,1]
	v_pk_fma_f32 v[172:173], v[188:189], v[184:185], v[164:165] op_sel_hi:[0,1,1] neg_lo:[0,0,1] neg_hi:[0,0,1]
	v_pk_fma_f32 v[174:175], v[188:189], v[186:187], v[166:167] op_sel_hi:[0,1,1] neg_lo:[0,0,1] neg_hi:[0,0,1]
	v_cvt_pk_bf16_f32 v176, v172, v173
	v_cvt_pk_bf16_f32 v177, v174, v175
	v_add_u32_e32 v193, 0x6000, v190
	global_store_dwordx2 v193, v[176:177], s[28:29]
	s_waitcnt vmcnt(31)
; #define GAS __attribute__((address_space(1)))
; __device__ __forceinline__ unsigned pk2(float lo, float hi) { const f32x2 v = {lo, hi}; return __builtin_bit_cast(unsigned, __builtin_convertvector(v, b16x2)); }
; template <int W>
; __device__ __forceinline__ void pool_item(const bf16* U, bf16* Z, int b, int t0, int g, int lane) {
;     ...
;     for (int i = 0; i < 32; ++i) { const int t = t0 + i;
;         const u32x2 v = *(const GAS u32x2*)(U + base + (size_t)t * D);
;         const float c0 = bf2f(v.x & 0xffffu), c1 = bf2f(v.x >> 16), c2 = bf2f(v.y & 0xffffu), c3 = bf2f(v.y >> 16);
;         s[0] += c0; s[1] += c1; s[2] += c2; s[3] += c3;
;         if (t - W >= 0) { const u32x2 o = *(const GAS u32x2*)(U + base + (size_t)(t - W) * D);
;             s[0] -= bf2f(o.x & 0xffffu); s[1] -= bf2f(o.x >> 16); s[2] -= bf2f(o.y & 0xffffu); s[3] -= bf2f(o.y >> 16); }
;         const float inv = 1.0f / (float)((t + 1) < W ? (t + 1) : W);
;         u32x2 w; w.x = pk2(s[0] * inv - c0, s[1] * inv - c1); w.y = pk2(s[2] * inv - c2, s[3] * inv - c3);
;         *(GAS u32x2*)(Z + base + (size_t)t * D) = w; }
; }
	v_lshlrev_b32_e32 v164, 16, v126
	v_and_b32_e32 v165, 0xffff0000, v126
	v_lshlrev_b32_e32 v166, 16, v127
	v_and_b32_e32 v167, 0xffff0000, v127
	v_pk_add_f32 v[184:185], v[184:185], v[164:165]
	v_pk_add_f32 v[186:187], v[186:187], v[166:167]
	v_lshlrev_b32_e32 v168, 16, v110
	v_and_b32_e32 v169, 0xffff0000, v110
	v_lshlrev_b32_e32 v170, 16, v111
	v_and_b32_e32 v171, 0xffff0000, v111
	v_pk_add_f32 v[184:185], v[184:185], v[168:169] neg_lo:[0,1] neg_hi:[0,1]
	v_pk_add_f32 v[186:187], v[186:187], v[170:171] neg_lo:[0,1] neg_hi:[0,1]
	v_pk_fma_f32 v[172:173], v[188:189], v[184:185], v[164:165] op_sel_hi:[0,1,1] neg_lo:[0,0,1] neg_hi:[0,0,1]
	v_pk_fma_f32 v[174:175], v[188:189], v[186:187], v[166:167] op_sel_hi:[0,1,1] neg_lo:[0,0,1] neg_hi:[0,0,1]
	v_cvt_pk_bf16_f32 v178, v172, v173
	v_cvt_pk_bf16_f32 v179, v174, v175
	global_store_dwordx2 v193, v[178:179], s[28:29] offset:2048
	s_waitcnt vmcnt(31)
	v_lshlrev_b32_e32 v164, 16, v128
	v_and_b32_e32 v165, 0xffff0000, v128
	v_lshlrev_b32_e32 v166, 16, v129
	v_and_b32_e32 v167, 0xffff0000, v129
	v_pk_add_f32 v[184:185], v[184:185], v[164:165]
	v_pk_add_f32 v[186:187], v[186:187], v[166:167]
	v_lshlrev_b32_e32 v168, 16, v112
	v_and_b32_e32 v169, 0xffff0000, v112
	v_lshlrev_b32_e32 v170, 16, v113
	v_and_b32_e32 v171, 0xffff0000, v113
	v_pk_add_f32 v[184:185], v[184:185], v[168:169] neg_lo:[0,1] neg_hi:[0,1]
	v_pk_add_f32 v[186:187], v[186:187], v[170:171] neg_lo:[0,1] neg_hi:[0,1]
	v_pk_fma_f32 v[172:173], v[188:189], v[184:185], v[164:165] op_sel_hi:[0,1,1] neg_lo:[0,0,1] neg_hi:[0,0,1]
	v_pk_fma_f32 v[174:175], v[188:189], v[186:187], v[166:167] op_sel_hi:[0,1,1] neg_lo:[0,0,1] neg_hi:[0,0,1]
	v_cvt_pk_bf16_f32 v180, v172, v173
	v_cvt_pk_bf16_f32 v181, v174, v175
	v_add_u32_e32 v194, 0x7000, v190
	global_store_dwordx2 v194, v[180:181], s[28:29]
	s_waitcnt vmcnt(31)
	v_lshlrev_b32_e32 v164, 16, v130
	v_and_b32_e32 v165, 0xffff0000, v130
	v_lshlrev_b32_e32 v166, 16, v131
	v_and_b32_e32 v167, 0xffff0000, v131
	v_pk_add_f32 v[184:185], v[184:185], v[164:165]
	v_pk_add_f32 v[186:187], v[186:187], v[166:167]
	v_lshlrev_b32_e32 v168, 16, v114
	v_and_b32_e32 v169, 0xffff0000, v114
	v_lshlrev_b32_e32 v170, 16, v115
	v_and_b32_e32 v171, 0xffff0000, v115
	v_pk_add_f32 v[184:185], v[184:185], v[168:169] neg_lo:[0,1] neg_hi:[0,1]
	v_pk_add_f32 v[186:187], v[186:187], v[170:171] neg_lo:[0,1] neg_hi:[0,1]
	v_pk_fma_f32 v[172:173], v[188:189], v[184:185], v[164:165] op_sel_hi:[0,1,1] neg_lo:[0,0,1] neg_hi:[0,0,1]
	v_pk_fma_f32 v[174:175], v[188:189], v[186:187], v[166:167] op_sel_hi:[0,1,1] neg_lo:[0,0,1] neg_hi:[0,0,1]
	v_cvt_pk_bf16_f32 v182, v172, v173
	v_cvt_pk_bf16_f32 v183, v174, v175
	global_store_dwordx2 v194, v[182:183], s[28:29] offset:2048
	s_waitcnt vmcnt(31)
	v_lshlrev_b32_e32 v164, 16, v132
	v_and_b32_e32 v165, 0xffff0000, v132
	v_lshlrev_b32_e32 v166, 16, v133
	v_and_b32_e32 v167, 0xffff0000, v133
	v_pk_add_f32 v[184:185], v[184:185], v[164:165]
	v_pk_add_f32 v[186:187], v[186:187], v[166:167]
	v_lshlrev_b32_e32 v168, 16, v116
	v_and_b32_e32 v169, 0xffff0000, v116
	v_lshlrev_b32_e32 v170, 16, v117
	v_and_b32_e32 v171, 0xffff0000, v117
	v_pk_add_f32 v[184:185], v[184:185], v[168:169] neg_lo:[0,1] neg_hi:[0,1]
	v_pk_add_f32 v[186:187], v[186:187], v[170:171] neg_lo:[0,1] neg_hi:[0,1]
	v_pk_fma_f32 v[172:173], v[188:189], v[184:185], v[164:165] op_sel_hi:[0,1,1] neg_lo:[0,0,1] neg_hi:[0,0,1]
	v_pk_fma_f32 v[174:175], v[188:189], v[186:187], v[166:167] op_sel_hi:[0,1,1] neg_lo:[0,0,1] neg_hi:[0,0,1]
	v_cvt_pk_bf16_f32 v176, v172, v173
	v_cvt_pk_bf16_f32 v177, v174, v175
	v_add_u32_e32 v193, 0x8000, v190
	global_store_dwordx2 v193, v[176:177], s[28:29]
	s_waitcnt vmcnt(31)
	v_lshlrev_b32_e32 v164, 16, v134
	v_and_b32_e32 v165, 0xffff0000, v134
	v_lshlrev_b32_e32 v166, 16, v135
	v_and_b32_e32 v167, 0xffff0000, v135
	v_pk_add_f32 v[184:185], v[184:185], v[164:165]
	v_pk_add_f32 v[186:187], v[186:187], v[166:167]
	v_lshlrev_b32_e32 v168, 16, v118
	v_and_b32_e32 v169, 0xffff0000, v118
	v_lshlrev_b32_e32 v170, 16, v119
	v_and_b32_e32 v171, 0xffff0000, v119
	v_pk_add_f32 v[184:185], v[184:185], v[168:169] neg_lo:[0,1] neg_hi:[0,1]
	v_pk_add_f32 v[186:187], v[186:187], v[170:171] neg_lo:[0,1] neg_hi:[0,1]
	v_pk_fma_f32 v[172:173], v[188:189], v[184:185], v[164:165] op_sel_hi:[0,1,1] neg_lo:[0,0,1] neg_hi:[0,0,1]
	v_pk_fma_f32 v[174:175], v[188:189], v[186:187], v[166:167] op_sel_hi:[0,1,1] neg_lo:[0,0,1] neg_hi:[0,0,1]
	v_cvt_pk_bf16_f32 v178, v172, v173
	v_cvt_pk_bf16_f32 v179, v174, v175
	global_store_dwordx2 v193, v[178:179], s[28:29] offset:2048
	s_waitcnt vmcnt(31)
	v_lshlrev_b32_e32 v164, 16, v136
	v_and_b32_e32 v165, 0xffff0000, v136
	v_lshlrev_b32_e32 v166, 16, v137
	v_and_b32_e32 v167, 0xffff0000, v137
	v_pk_add_f32 v[184:185], v[184:185], v[164:165]
	v_pk_add_f32 v[186:187], v[186:187], v[166:167]
	v_lshlrev_b32_e32 v168, 16, v120
	v_and_b32_e32 v169, 0xffff0000, v120
	v_lshlrev_b32_e32 v170, 16, v121
	v_and_b32_e32 v171, 0xffff0000, v121
	v_pk_add_f32 v[184:185], v[184:185], v[168:169] neg_lo:[0,1] neg_hi:[0,1]
	v_pk_add_f32 v[186:187], v[186:187], v[170:171] neg_lo:[0,1] neg_hi:[0,1]
	v_pk_fma_f32 v[172:173], v[188:189], v[184:185], v[164:165] op_sel_hi:[0,1,1] neg_lo:[0,0,1] neg_hi:[0,0,1]
	v_pk_fma_f32 v[174:175], v[188:189], v[186:187], v[166:167] op_sel_hi:[0,1,1] neg_lo:[0,0,1] neg_hi:[0,0,1]
	v_cvt_pk_bf16_f32 v180, v172, v173
	v_cvt_pk_bf16_f32 v181, v174, v175
	v_add_u32_e32 v194, 0x9000, v190
	global_store_dwordx2 v194, v[180:181], s[28:29]
	s_waitcnt vmcnt(31)
; #define GAS __attribute__((address_space(1)))
; __device__ __forceinline__ unsigned pk2(float lo, float hi) { const f32x2 v = {lo, hi}; return __builtin_bit_cast(unsigned, __builtin_convertvector(v, b16x2)); }
; template <int W>
; __device__ __forceinline__ void pool_item(const bf16* U, bf16* Z, int b, int t0, int g, int lane) {
;     ...
;     for (int i = 0; i < 32; ++i) { const int t = t0 + i;
;         const u32x2 v = *(const GAS u32x2*)(U + base + (size_t)t * D);
;         const float c0 = bf2f(v.x & 0xffffu), c1 = bf2f(v.x >> 16), c2 = bf2f(v.y & 0xffffu), c3 = bf2f(v.y >> 16);
;         s[0] += c0; s[1] += c1; s[2] += c2; s[3] += c3;
;         if (t - W >= 0) { const u32x2 o = *(const GAS u32x2*)(U + base + (size_t)(t - W) * D);
;             s[0] -= bf2f(o.x & 0xffffu); s[1] -= bf2f(o.x >> 16); s[2] -= bf2f(o.y & 0xffffu); s[3] -= bf2f(o.y >> 16); }
;         const float inv = 1.0f / (float)((t + 1) < W ? (t + 1) : W);
;         u32x2 w; w.x = pk2(s[0] * inv - c0, s[1] * inv - c1); w.y = pk2(s[2] * inv - c2, s[3] * inv - c3);
;         *(GAS u32x2*)(Z + base + (size_t)t * D) = w; }
; }
	v_lshlrev_b32_e32 v164, 16, v138
	v_and_b32_e32 v165, 0xffff0000, v138
	v_lshlrev_b32_e32 v166, 16, v139
	v_and_b32_e32 v167, 0xffff0000, v139
	v_pk_add_f32 v[184:185], v[184:185], v[164:165]
	v_pk_add_f32 v[186:187], v[186:187], v[166:167]
	v_lshlrev_b32_e32 v168, 16, v122
	v_and_b32_e32 v169, 0xffff0000, v122
	v_lshlrev_b32_e32 v170, 16, v123
	v_and_b32_e32 v171, 0xffff0000, v123
	v_pk_add_f32 v[184:185], v[184:185], v[168:169] neg_lo:[0,1] neg_hi:[0,1]
	v_pk_add_f32 v[186:187], v[186:187], v[170:171] neg_lo:[0,1] neg_hi:[0,1]
	v_pk_fma_f32 v[172:173], v[188:189], v[184:185], v[164:165] op_sel_hi:[0,1,1] neg_lo:[0,0,1] neg_hi:[0,0,1]
	v_pk_fma_f32 v[174:175], v[188:189], v[186:187], v[166:167] op_sel_hi:[0,1,1] neg_lo:[0,0,1] neg_hi:[0,0,1]
	v_cvt_pk_bf16_f32 v182, v172, v173
	v_cvt_pk_bf16_f32 v183, v174, v175
	global_store_dwordx2 v194, v[182:183], s[28:29] offset:2048
	s_waitcnt vmcnt(31)
	v_lshlrev_b32_e32 v164, 16, v140
	v_and_b32_e32 v165, 0xffff0000, v140
	v_lshlrev_b32_e32 v166, 16, v141
	v_and_b32_e32 v167, 0xffff0000, v141
	v_pk_add_f32 v[184:185], v[184:185], v[164:165]
	v_pk_add_f32 v[186:187], v[186:187], v[166:167]
	v_lshlrev_b32_e32 v168, 16, v124
	v_and_b32_e32 v169, 0xffff0000, v124
	v_lshlrev_b32_e32 v170, 16, v125
	v_and_b32_e32 v171, 0xffff0000, v125
	v_pk_add_f32 v[184:185], v[184:185], v[168:169] neg_lo:[0,1] neg_hi:[0,1]
	v_pk_add_f32 v[186:187], v[186:187], v[170:171] neg_lo:[0,1] neg_hi:[0,1]
	v_pk_fma_f32 v[172:173], v[188:189], v[184:185], v[164:165] op_sel_hi:[0,1,1] neg_lo:[0,0,1] neg_hi:[0,0,1]
	v_pk_fma_f32 v[174:175], v[188:189], v[186:187], v[166:167] op_sel_hi:[0,1,1] neg_lo:[0,0,1] neg_hi:[0,0,1]
	v_cvt_pk_bf16_f32 v176, v172, v173
	v_cvt_pk_bf16_f32 v177, v174, v175
	v_add_u32_e32 v193, 0xa000, v190
	global_store_dwordx2 v193, v[176:177], s[28:29]
	s_waitcnt vmcnt(31)
	v_lshlrev_b32_e32 v164, 16, v142
	v_and_b32_e32 v165, 0xffff0000, v142
	v_lshlrev_b32_e32 v166, 16, v143
	v_and_b32_e32 v167, 0xffff0000, v143
	v_pk_add_f32 v[184:185], v[184:185], v[164:165]
	v_pk_add_f32 v[186:187], v[186:187], v[166:167]
	v_lshlrev_b32_e32 v168, 16, v126
	v_and_b32_e32 v169, 0xffff0000, v126
	v_lshlrev_b32_e32 v170, 16, v127
	v_and_b32_e32 v171, 0xffff0000, v127
	v_pk_add_f32 v[184:185], v[184:185], v[168:169] neg_lo:[0,1] neg_hi:[0,1]
	v_pk_add_f32 v[186:187], v[186:187], v[170:171] neg_lo:[0,1] neg_hi:[0,1]
	v_pk_fma_f32 v[172:173], v[188:189], v[184:185], v[164:165] op_sel_hi:[0,1,1] neg_lo:[0,0,1] neg_hi:[0,0,1]
	v_pk_fma_f32 v[174:175], v[188:189], v[186:187], v[166:167] op_sel_hi:[0,1,1] neg_lo:[0,0,1] neg_hi:[0,0,1]
	v_cvt_pk_bf16_f32 v178, v172, v173
	v_cvt_pk_bf16_f32 v179, v174, v175
	global_store_dwordx2 v193, v[178:179], s[28:29] offset:2048
	s_waitcnt vmcnt(31)
	v_lshlrev_b32_e32 v164, 16, v144
	v_and_b32_e32 v165, 0xffff0000, v144
	v_lshlrev_b32_e32 v166, 16, v145
	v_and_b32_e32 v167, 0xffff0000, v145
	v_pk_add_f32 v[184:185], v[184:185], v[164:165]
	v_pk_add_f32 v[186:187], v[186:187], v[166:167]
	v_lshlrev_b32_e32 v168, 16, v128
	v_and_b32_e32 v169, 0xffff0000, v128
	v_lshlrev_b32_e32 v170, 16, v129
	v_and_b32_e32 v171, 0xffff0000, v129
	v_pk_add_f32 v[184:185], v[184:185], v[168:169] neg_lo:[0,1] neg_hi:[0,1]
	v_pk_add_f32 v[186:187], v[186:187], v[170:171] neg_lo:[0,1] neg_hi:[0,1]
	v_pk_fma_f32 v[172:173], v[188:189], v[184:185], v[164:165] op_sel_hi:[0,1,1] neg_lo:[0,0,1] neg_hi:[0,0,1]
	v_pk_fma_f32 v[174:175], v[188:189], v[186:187], v[166:167] op_sel_hi:[0,1,1] neg_lo:[0,0,1] neg_hi:[0,0,1]
	v_cvt_pk_bf16_f32 v180, v172, v173
	v_cvt_pk_bf16_f32 v181, v174, v175
	v_add_u32_e32 v194, 0xb000, v190
	global_store_dwordx2 v194, v[180:181], s[28:29]
	s_waitcnt vmcnt(31)
	v_lshlrev_b32_e32 v164, 16, v146
	v_and_b32_e32 v165, 0xffff0000, v146
	v_lshlrev_b32_e32 v166, 16, v147
	v_and_b32_e32 v167, 0xffff0000, v147
	v_pk_add_f32 v[184:185], v[184:185], v[164:165]
	v_pk_add_f32 v[186:187], v[186:187], v[166:167]
	v_lshlrev_b32_e32 v168, 16, v130
	v_and_b32_e32 v169, 0xffff0000, v130
	v_lshlrev_b32_e32 v170, 16, v131
	v_and_b32_e32 v171, 0xffff0000, v131
	v_pk_add_f32 v[184:185], v[184:185], v[168:169] neg_lo:[0,1] neg_hi:[0,1]
	v_pk_add_f32 v[186:187], v[186:187], v[170:171] neg_lo:[0,1] neg_hi:[0,1]
	v_pk_fma_f32 v[172:173], v[188:189], v[184:185], v[164:165] op_sel_hi:[0,1,1] neg_lo:[0,0,1] neg_hi:[0,0,1]
	v_pk_fma_f32 v[174:175], v[188:189], v[186:187], v[166:167] op_sel_hi:[0,1,1] neg_lo:[0,0,1] neg_hi:[0,0,1]
	v_cvt_pk_bf16_f32 v182, v172, v173
	v_cvt_pk_bf16_f32 v183, v174, v175
	global_store_dwordx2 v194, v[182:183], s[28:29] offset:2048
	s_waitcnt vmcnt(31)
	v_lshlrev_b32_e32 v164, 16, v148
	v_and_b32_e32 v165, 0xffff0000, v148
	v_lshlrev_b32_e32 v166, 16, v149
	v_and_b32_e32 v167, 0xffff0000, v149
	v_pk_add_f32 v[184:185], v[184:185], v[164:165]
	v_pk_add_f32 v[186:187], v[186:187], v[166:167]
	v_lshlrev_b32_e32 v168, 16, v132
	v_and_b32_e32 v169, 0xffff0000, v132
	v_lshlrev_b32_e32 v170, 16, v133
	v_and_b32_e32 v171, 0xffff0000, v133
	v_pk_add_f32 v[184:185], v[184:185], v[168:169] neg_lo:[0,1] neg_hi:[0,1]
	v_pk_add_f32 v[186:187], v[186:187], v[170:171] neg_lo:[0,1] neg_hi:[0,1]
	v_pk_fma_f32 v[172:173], v[188:189], v[184:185], v[164:165] op_sel_hi:[0,1,1] neg_lo:[0,0,1] neg_hi:[0,0,1]
	v_pk_fma_f32 v[174:175], v[188:189], v[186:187], v[166:167] op_sel_hi:[0,1,1] neg_lo:[0,0,1] neg_hi:[0,0,1]
	v_cvt_pk_bf16_f32 v176, v172, v173
	v_cvt_pk_bf16_f32 v177, v174, v175
	v_add_u32_e32 v193, 0xc000, v190
	global_store_dwordx2 v193, v[176:177], s[28:29]
	s_waitcnt vmcnt(31)
; #define GAS __attribute__((address_space(1)))
; __device__ __forceinline__ unsigned pk2(float lo, float hi) { const f32x2 v = {lo, hi}; return __builtin_bit_cast(unsigned, __builtin_convertvector(v, b16x2)); }
; template <int W>
; __device__ __forceinline__ void pool_item(const bf16* U, bf16* Z, int b, int t0, int g, int lane) {
;     ...
;     for (int i = 0; i < 32; ++i) { const int t = t0 + i;
;         const u32x2 v = *(const GAS u32x2*)(U + base + (size_t)t * D);
;         const float c0 = bf2f(v.x & 0xffffu), c1 = bf2f(v.x >> 16), c2 = bf2f(v.y & 0xffffu), c3 = bf2f(v.y >> 16);
;         s[0] += c0; s[1] += c1; s[2] += c2; s[3] += c3;
;         if (t - W >= 0) { const u32x2 o = *(const GAS u32x2*)(U + base + (size_t)(t - W) * D);
;             s[0] -= bf2f(o.x & 0xffffu); s[1] -= bf2f(o.x >> 16); s[2] -= bf2f(o.y & 0xffffu); s[3] -= bf2f(o.y >> 16); }
;         const float inv = 1.0f / (float)((t + 1) < W ? (t + 1) : W);
;         u32x2 w; w.x = pk2(s[0] * inv - c0, s[1] * inv - c1); w.y = pk2(s[2] * inv - c2, s[3] * inv - c3);
;         *(GAS u32x2*)(Z + base + (size_t)t * D) = w; }
; }
	v_lshlrev_b32_e32 v164, 16, v150
	v_and_b32_e32 v165, 0xffff0000, v150
	v_lshlrev_b32_e32 v166, 16, v151
	v_and_b32_e32 v167, 0xffff0000, v151
	v_pk_add_f32 v[184:185], v[184:185], v[164:165]
	v_pk_add_f32 v[186:187], v[186:187], v[166:167]
	v_lshlrev_b32_e32 v168, 16, v134
	v_and_b32_e32 v169, 0xffff0000, v134
	v_lshlrev_b32_e32 v170, 16, v135
	v_and_b32_e32 v171, 0xffff0000, v135
	v_pk_add_f32 v[184:185], v[184:185], v[168:169] neg_lo:[0,1] neg_hi:[0,1]
	v_pk_add_f32 v[186:187], v[186:187], v[170:171] neg_lo:[0,1] neg_hi:[0,1]
	v_pk_fma_f32 v[172:173], v[188:189], v[184:185], v[164:165] op_sel_hi:[0,1,1] neg_lo:[0,0,1] neg_hi:[0,0,1]
	v_pk_fma_f32 v[174:175], v[188:189], v[186:187], v[166:167] op_sel_hi:[0,1,1] neg_lo:[0,0,1] neg_hi:[0,0,1]
	v_cvt_pk_bf16_f32 v178, v172, v173
	v_cvt_pk_bf16_f32 v179, v174, v175
	global_store_dwordx2 v193, v[178:179], s[28:29] offset:2048
	s_waitcnt vmcnt(31)
	v_lshlrev_b32_e32 v164, 16, v152
	v_and_b32_e32 v165, 0xffff0000, v152
	v_lshlrev_b32_e32 v166, 16, v153
	v_and_b32_e32 v167, 0xffff0000, v153
	v_pk_add_f32 v[184:185], v[184:185], v[164:165]
	v_pk_add_f32 v[186:187], v[186:187], v[166:167]
	v_lshlrev_b32_e32 v168, 16, v136
	v_and_b32_e32 v169, 0xffff0000, v136
	v_lshlrev_b32_e32 v170, 16, v137
	v_and_b32_e32 v171, 0xffff0000, v137
	v_pk_add_f32 v[184:185], v[184:185], v[168:169] neg_lo:[0,1] neg_hi:[0,1]
	v_pk_add_f32 v[186:187], v[186:187], v[170:171] neg_lo:[0,1] neg_hi:[0,1]
	v_pk_fma_f32 v[172:173], v[188:189], v[184:185], v[164:165] op_sel_hi:[0,1,1] neg_lo:[0,0,1] neg_hi:[0,0,1]
	v_pk_fma_f32 v[174:175], v[188:189], v[186:187], v[166:167] op_sel_hi:[0,1,1] neg_lo:[0,0,1] neg_hi:[0,0,1]
	v_cvt_pk_bf16_f32 v180, v172, v173
	v_cvt_pk_bf16_f32 v181, v174, v175
	v_add_u32_e32 v194, 0xd000, v190
	global_store_dwordx2 v194, v[180:181], s[28:29]
	s_waitcnt vmcnt(31)
	v_lshlrev_b32_e32 v164, 16, v154
	v_and_b32_e32 v165, 0xffff0000, v154
	v_lshlrev_b32_e32 v166, 16, v155
	v_and_b32_e32 v167, 0xffff0000, v155
	v_pk_add_f32 v[184:185], v[184:185], v[164:165]
	v_pk_add_f32 v[186:187], v[186:187], v[166:167]
	v_lshlrev_b32_e32 v168, 16, v138
	v_and_b32_e32 v169, 0xffff0000, v138
	v_lshlrev_b32_e32 v170, 16, v139
	v_and_b32_e32 v171, 0xffff0000, v139
	v_pk_add_f32 v[184:185], v[184:185], v[168:169] neg_lo:[0,1] neg_hi:[0,1]
	v_pk_add_f32 v[186:187], v[186:187], v[170:171] neg_lo:[0,1] neg_hi:[0,1]
	v_pk_fma_f32 v[172:173], v[188:189], v[184:185], v[164:165] op_sel_hi:[0,1,1] neg_lo:[0,0,1] neg_hi:[0,0,1]
	v_pk_fma_f32 v[174:175], v[188:189], v[186:187], v[166:167] op_sel_hi:[0,1,1] neg_lo:[0,0,1] neg_hi:[0,0,1]
	v_cvt_pk_bf16_f32 v182, v172, v173
	v_cvt_pk_bf16_f32 v183, v174, v175
	global_store_dwordx2 v194, v[182:183], s[28:29] offset:2048
	s_waitcnt vmcnt(31)
	v_lshlrev_b32_e32 v164, 16, v156
	v_and_b32_e32 v165, 0xffff0000, v156
	v_lshlrev_b32_e32 v166, 16, v157
	v_and_b32_e32 v167, 0xffff0000, v157
	v_pk_add_f32 v[184:185], v[184:185], v[164:165]
	v_pk_add_f32 v[186:187], v[186:187], v[166:167]
	v_lshlrev_b32_e32 v168, 16, v140
	v_and_b32_e32 v169, 0xffff0000, v140
	v_lshlrev_b32_e32 v170, 16, v141
	v_and_b32_e32 v171, 0xffff0000, v141
	v_pk_add_f32 v[184:185], v[184:185], v[168:169] neg_lo:[0,1] neg_hi:[0,1]
	v_pk_add_f32 v[186:187], v[186:187], v[170:171] neg_lo:[0,1] neg_hi:[0,1]
	v_pk_fma_f32 v[172:173], v[188:189], v[184:185], v[164:165] op_sel_hi:[0,1,1] neg_lo:[0,0,1] neg_hi:[0,0,1]
	v_pk_fma_f32 v[174:175], v[188:189], v[186:187], v[166:167] op_sel_hi:[0,1,1] neg_lo:[0,0,1] neg_hi:[0,0,1]
	v_cvt_pk_bf16_f32 v176, v172, v173
	v_cvt_pk_bf16_f32 v177, v174, v175
	v_add_u32_e32 v193, 0xe000, v190
	global_store_dwordx2 v193, v[176:177], s[28:29]
	s_waitcnt vmcnt(31)
	v_lshlrev_b32_e32 v164, 16, v158
	v_and_b32_e32 v165, 0xffff0000, v158
	v_lshlrev_b32_e32 v166, 16, v159
	v_and_b32_e32 v167, 0xffff0000, v159
	v_pk_add_f32 v[184:185], v[184:185], v[164:165]
	v_pk_add_f32 v[186:187], v[186:187], v[166:167]
	v_lshlrev_b32_e32 v168, 16, v142
	v_and_b32_e32 v169, 0xffff0000, v142
	v_lshlrev_b32_e32 v170, 16, v143
	v_and_b32_e32 v171, 0xffff0000, v143
	v_pk_add_f32 v[184:185], v[184:185], v[168:169] neg_lo:[0,1] neg_hi:[0,1]
	v_pk_add_f32 v[186:187], v[186:187], v[170:171] neg_lo:[0,1] neg_hi:[0,1]
	v_pk_fma_f32 v[172:173], v[188:189], v[184:185], v[164:165] op_sel_hi:[0,1,1] neg_lo:[0,0,1] neg_hi:[0,0,1]
	v_pk_fma_f32 v[174:175], v[188:189], v[186:187], v[166:167] op_sel_hi:[0,1,1] neg_lo:[0,0,1] neg_hi:[0,0,1]
	v_cvt_pk_bf16_f32 v178, v172, v173
	v_cvt_pk_bf16_f32 v179, v174, v175
	global_store_dwordx2 v193, v[178:179], s[28:29] offset:2048
	s_waitcnt vmcnt(31)
	v_lshlrev_b32_e32 v164, 16, v160
	v_and_b32_e32 v165, 0xffff0000, v160
	v_lshlrev_b32_e32 v166, 16, v161
	v_and_b32_e32 v167, 0xffff0000, v161
	v_pk_add_f32 v[184:185], v[184:185], v[164:165]
	v_pk_add_f32 v[186:187], v[186:187], v[166:167]
	v_lshlrev_b32_e32 v168, 16, v144
	v_and_b32_e32 v169, 0xffff0000, v144
	v_lshlrev_b32_e32 v170, 16, v145
	v_and_b32_e32 v171, 0xffff0000, v145
	v_pk_add_f32 v[184:185], v[184:185], v[168:169] neg_lo:[0,1] neg_hi:[0,1]
	v_pk_add_f32 v[186:187], v[186:187], v[170:171] neg_lo:[0,1] neg_hi:[0,1]
	v_pk_fma_f32 v[172:173], v[188:189], v[184:185], v[164:165] op_sel_hi:[0,1,1] neg_lo:[0,0,1] neg_hi:[0,0,1]
	v_pk_fma_f32 v[174:175], v[188:189], v[186:187], v[166:167] op_sel_hi:[0,1,1] neg_lo:[0,0,1] neg_hi:[0,0,1]
	v_cvt_pk_bf16_f32 v180, v172, v173
	v_cvt_pk_bf16_f32 v181, v174, v175
	v_add_u32_e32 v194, 0xf000, v190
	global_store_dwordx2 v194, v[180:181], s[28:29]
	s_waitcnt vmcnt(31)
	v_lshlrev_b32_e32 v164, 16, v162
	v_and_b32_e32 v165, 0xffff0000, v162
	v_lshlrev_b32_e32 v166, 16, v163
	v_and_b32_e32 v167, 0xffff0000, v163
	v_pk_add_f32 v[184:185], v[184:185], v[164:165]
	v_pk_add_f32 v[186:187], v[186:187], v[166:167]
	v_lshlrev_b32_e32 v168, 16, v146
	v_and_b32_e32 v169, 0xffff0000, v146
	v_lshlrev_b32_e32 v170, 16, v147
	v_and_b32_e32 v171, 0xffff0000, v147
	v_pk_add_f32 v[184:185], v[184:185], v[168:169] neg_lo:[0,1] neg_hi:[0,1]
	v_pk_add_f32 v[186:187], v[186:187], v[170:171] neg_lo:[0,1] neg_hi:[0,1]
	v_pk_fma_f32 v[172:173], v[188:189], v[184:185], v[164:165] op_sel_hi:[0,1,1] neg_lo:[0,0,1] neg_hi:[0,0,1]
	v_pk_fma_f32 v[174:175], v[188:189], v[186:187], v[166:167] op_sel_hi:[0,1,1] neg_lo:[0,0,1] neg_hi:[0,0,1]
	v_cvt_pk_bf16_f32 v182, v172, v173
	v_cvt_pk_bf16_f32 v183, v174, v175
	global_store_dwordx2 v194, v[182:183], s[28:29] offset:2048
	s_branch .LBB0_861
; #define GAS __attribute__((address_space(1)))
; __device__ __forceinline__ unsigned pk2(float lo, float hi) { const f32x2 v = {lo, hi}; return __builtin_bit_cast(unsigned, __builtin_convertvector(v, b16x2)); }
; template <int W>
; __device__ __forceinline__ void pool_item(const bf16* U, bf16* Z, int b, int t0, int g, int lane) {
;     const size_t base = (size_t)b * SEQ * D + 256 * g + 4 * lane;
;     float s[4] = {0.f, 0.f, 0.f, 0.f};
; #pragma unroll
;     for (int j = 1; j <= W; ++j) { const int t = t0 - j; if (t >= 0) { const u32x2 v = *(const GAS u32x2*)(U + base + (size_t)t * D);
;             s[0] += bf2f(v.x & 0xffffu); s[1] += bf2f(v.x >> 16); s[2] += bf2f(v.y & 0xffffu); s[3] += bf2f(v.y >> 16); } }
; #pragma unroll 8
;     for (int i = 0; i < 32; ++i) { const int t = t0 + i;
;         const u32x2 v = *(const GAS u32x2*)(U + base + (size_t)t * D);
;         const float c0 = bf2f(v.x & 0xffffu), c1 = bf2f(v.x >> 16), c2 = bf2f(v.y & 0xffffu), c3 = bf2f(v.y >> 16);
;         s[0] += c0; s[1] += c1; s[2] += c2; s[3] += c3;
;         if (t - W >= 0) { const u32x2 o = *(const GAS u32x2*)(U + base + (size_t)(t - W) * D);
;             s[0] -= bf2f(o.x & 0xffffu); s[1] -= bf2f(o.x >> 16); s[2] -= bf2f(o.y & 0xffffu); s[3] -= bf2f(o.y >> 16); }
;         const float inv = 1.0f / (float)((t + 1) < W ? (t + 1) : W);
;         u32x2 w; w.x = pk2(s[0] * inv - c0, s[1] * inv - c1); w.y = pk2(s[2] * inv - c2, s[3] * inv - c3);
;         *(GAS u32x2*)(Z + base + (size_t)t * D) = w; }
; }
.Lpool_w4:
	v_mov_b32_e32 v188, 0x3e800000
	v_mov_b32_e32 v189, v188
	v_add_u32_e32 v192, 0x6000, v190
	global_load_dwordx2 v[92:93], v192, s[10:11]
	global_load_dwordx2 v[94:95], v192, s[10:11] offset:2048
	v_add_u32_e32 v191, 0x7000, v190
	global_load_dwordx2 v[96:97], v191, s[10:11]
	global_load_dwordx2 v[98:99], v191, s[10:11] offset:2048
	v_add_u32_e32 v192, 0x8000, v190
	global_load_dwordx2 v[100:101], v192, s[10:11]
	global_load_dwordx2 v[102:103], v192, s[10:11] offset:2048
	v_add_u32_e32 v191, 0x9000, v190
	global_load_dwordx2 v[104:105], v191, s[10:11]
	global_load_dwordx2 v[106:107], v191, s[10:11] offset:2048
	v_add_u32_e32 v192, 0xa000, v190
	global_load_dwordx2 v[108:109], v192, s[10:11]
	global_load_dwordx2 v[110:111], v192, s[10:11] offset:2048
	v_add_u32_e32 v191, 0xb000, v190
	global_load_dwordx2 v[112:113], v191, s[10:11]
	global_load_dwordx2 v[114:115], v191, s[10:11] offset:2048
	v_add_u32_e32 v192, 0xc000, v190
	global_load_dwordx2 v[116:117], v192, s[10:11]
	global_load_dwordx2 v[118:119], v192, s[10:11] offset:2048
	v_add_u32_e32 v191, 0xd000, v190
	global_load_dwordx2 v[120:121], v191, s[10:11]
	global_load_dwordx2 v[122:123], v191, s[10:11] offset:2048
	v_add_u32_e32 v192, 0xe000, v190
	global_load_dwordx2 v[124:125], v192, s[10:11]
	global_load_dwordx2 v[126:127], v192, s[10:11] offset:2048
	v_add_u32_e32 v191, 0xf000, v190
	global_load_dwordx2 v[128:129], v191, s[10:11]
	global_load_dwordx2 v[130:131], v191, s[10:11] offset:2048
	v_add_u32_e32 v192, 0x10000, v190
	global_load_dwordx2 v[132:133], v192, s[10:11]
	global_load_dwordx2 v[134:135], v192, s[10:11] offset:2048
	v_add_u32_e32 v191, 0x11000, v190
	global_load_dwordx2 v[136:137], v191, s[10:11]
	global_load_dwordx2 v[138:139], v191, s[10:11] offset:2048
	v_add_u32_e32 v192, 0x12000, v190
	global_load_dwordx2 v[140:141], v192, s[10:11]
	global_load_dwordx2 v[142:143], v192, s[10:11] offset:2048
	v_add_u32_e32 v191, 0x13000, v190
	global_load_dwordx2 v[144:145], v191, s[10:11]
	global_load_dwordx2 v[146:147], v191, s[10:11] offset:2048
	v_add_u32_e32 v192, 0x14000, v190
	global_load_dwordx2 v[148:149], v192, s[10:11]
	global_load_dwordx2 v[150:151], v192, s[10:11] offset:2048
	v_add_u32_e32 v191, 0x15000, v190
	global_load_dwordx2 v[152:153], v191, s[10:11]
	global_load_dwordx2 v[154:155], v191, s[10:11] offset:2048
	v_add_u32_e32 v192, 0x16000, v190
	global_load_dwordx2 v[156:157], v192, s[10:11]
	global_load_dwordx2 v[158:159], v192, s[10:11] offset:2048
	v_add_u32_e32 v191, 0x17000, v190
	global_load_dwordx2 v[160:161], v191, s[10:11]
	global_load_dwordx2 v[162:163], v191, s[10:11] offset:2048
	s_waitcnt vmcnt(32)
	v_lshlrev_b32_e32 v164, 16, v98
	v_and_b32_e32 v165, 0xffff0000, v98
	v_lshlrev_b32_e32 v166, 16, v99
	v_and_b32_e32 v167, 0xffff0000, v99
	v_pk_add_f32 v[184:185], v[164:165], 0 op_sel_hi:[1,0]
	v_pk_add_f32 v[186:187], v[166:167], 0 op_sel_hi:[1,0]
	v_lshlrev_b32_e32 v164, 16, v96
	v_and_b32_e32 v165, 0xffff0000, v96
	v_lshlrev_b32_e32 v166, 16, v97
	v_and_b32_e32 v167, 0xffff0000, v97
	v_pk_add_f32 v[184:185], v[184:185], v[164:165]
	v_pk_add_f32 v[186:187], v[186:187], v[166:167]
	v_lshlrev_b32_e32 v164, 16, v94
	v_and_b32_e32 v165, 0xffff0000, v94
	v_lshlrev_b32_e32 v166, 16, v95
	v_and_b32_e32 v167, 0xffff0000, v95
	v_pk_add_f32 v[184:185], v[184:185], v[164:165]
	v_pk_add_f32 v[186:187], v[186:187], v[166:167]
	v_lshlrev_b32_e32 v164, 16, v92
	v_and_b32_e32 v165, 0xffff0000, v92
	v_lshlrev_b32_e32 v166, 16, v93
	v_and_b32_e32 v167, 0xffff0000, v93
	v_pk_add_f32 v[184:185], v[184:185], v[164:165]
	v_pk_add_f32 v[186:187], v[186:187], v[166:167]
	s_waitcnt vmcnt(31)
	v_lshlrev_b32_e32 v164, 16, v100
	v_and_b32_e32 v165, 0xffff0000, v100
	v_lshlrev_b32_e32 v166, 16, v101
	v_and_b32_e32 v167, 0xffff0000, v101
	v_pk_add_f32 v[184:185], v[184:185], v[164:165]
	v_pk_add_f32 v[186:187], v[186:187], v[166:167]
	v_lshlrev_b32_e32 v168, 16, v92
	v_and_b32_e32 v169, 0xffff0000, v92
	v_lshlrev_b32_e32 v170, 16, v93
	v_and_b32_e32 v171, 0xffff0000, v93
	v_pk_add_f32 v[184:185], v[184:185], v[168:169] neg_lo:[0,1] neg_hi:[0,1]
	v_pk_add_f32 v[186:187], v[186:187], v[170:171] neg_lo:[0,1] neg_hi:[0,1]
	v_pk_fma_f32 v[172:173], v[188:189], v[184:185], v[164:165] op_sel_hi:[0,1,1] neg_lo:[0,0,1] neg_hi:[0,0,1]
	v_pk_fma_f32 v[174:175], v[188:189], v[186:187], v[166:167] op_sel_hi:[0,1,1] neg_lo:[0,0,1] neg_hi:[0,0,1]
	v_cvt_pk_bf16_f32 v176, v172, v173
	v_cvt_pk_bf16_f32 v177, v174, v175
	global_store_dwordx2 v190, v[176:177], s[28:29]
	s_waitcnt vmcnt(31)
	v_lshlrev_b32_e32 v164, 16, v102
	v_and_b32_e32 v165, 0xffff0000, v102
	v_lshlrev_b32_e32 v166, 16, v103
	v_and_b32_e32 v167, 0xffff0000, v103
	v_pk_add_f32 v[184:185], v[184:185], v[164:165]
	v_pk_add_f32 v[186:187], v[186:187], v[166:167]
	v_lshlrev_b32_e32 v168, 16, v94
	v_and_b32_e32 v169, 0xffff0000, v94
	v_lshlrev_b32_e32 v170, 16, v95
	v_and_b32_e32 v171, 0xffff0000, v95
	v_pk_add_f32 v[184:185], v[184:185], v[168:169] neg_lo:[0,1] neg_hi:[0,1]
	v_pk_add_f32 v[186:187], v[186:187], v[170:171] neg_lo:[0,1] neg_hi:[0,1]
	v_pk_fma_f32 v[172:173], v[188:189], v[184:185], v[164:165] op_sel_hi:[0,1,1] neg_lo:[0,0,1] neg_hi:[0,0,1]
	v_pk_fma_f32 v[174:175], v[188:189], v[186:187], v[166:167] op_sel_hi:[0,1,1] neg_lo:[0,0,1] neg_hi:[0,0,1]
	v_cvt_pk_bf16_f32 v178, v172, v173
	v_cvt_pk_bf16_f32 v179, v174, v175
	global_store_dwordx2 v190, v[178:179], s[28:29] offset:2048
	s_waitcnt vmcnt(31)
; #define GAS __attribute__((address_space(1)))
; __device__ __forceinline__ unsigned pk2(float lo, float hi) { const f32x2 v = {lo, hi}; return __builtin_bit_cast(unsigned, __builtin_convertvector(v, b16x2)); }
; template <int W>
; __device__ __forceinline__ void pool_item(const bf16* U, bf16* Z, int b, int t0, int g, int lane) {
;     ...
;     for (int i = 0; i < 32; ++i) { const int t = t0 + i;
;         const u32x2 v = *(const GAS u32x2*)(U + base + (size_t)t * D);
;         const float c0 = bf2f(v.x & 0xffffu), c1 = bf2f(v.x >> 16), c2 = bf2f(v.y & 0xffffu), c3 = bf2f(v.y >> 16);
;         s[0] += c0; s[1] += c1; s[2] += c2; s[3] += c3;
;         if (t - W >= 0) { const u32x2 o = *(const GAS u32x2*)(U + base + (size_t)(t - W) * D);
;             s[0] -= bf2f(o.x & 0xffffu); s[1] -= bf2f(o.x >> 16); s[2] -= bf2f(o.y & 0xffffu); s[3] -= bf2f(o.y >> 16); }
;         const float inv = 1.0f / (float)((t + 1) < W ? (t + 1) : W);
;         u32x2 w; w.x = pk2(s[0] * inv - c0, s[1] * inv - c1); w.y = pk2(s[2] * inv - c2, s[3] * inv - c3);
;         *(GAS u32x2*)(Z + base + (size_t)t * D) = w; }
; }
	v_lshlrev_b32_e32 v164, 16, v104
	v_and_b32_e32 v165, 0xffff0000, v104
	v_lshlrev_b32_e32 v166, 16, v105
	v_and_b32_e32 v167, 0xffff0000, v105
	v_pk_add_f32 v[184:185], v[184:185], v[164:165]
	v_pk_add_f32 v[186:187], v[186:187], v[166:167]
	v_lshlrev_b32_e32 v168, 16, v96
	v_and_b32_e32 v169, 0xffff0000, v96
	v_lshlrev_b32_e32 v170, 16, v97
	v_and_b32_e32 v171, 0xffff0000, v97
	v_pk_add_f32 v[184:185], v[184:185], v[168:169] neg_lo:[0,1] neg_hi:[0,1]
	v_pk_add_f32 v[186:187], v[186:187], v[170:171] neg_lo:[0,1] neg_hi:[0,1]
	v_pk_fma_f32 v[172:173], v[188:189], v[184:185], v[164:165] op_sel_hi:[0,1,1] neg_lo:[0,0,1] neg_hi:[0,0,1]
	v_pk_fma_f32 v[174:175], v[188:189], v[186:187], v[166:167] op_sel_hi:[0,1,1] neg_lo:[0,0,1] neg_hi:[0,0,1]
	v_cvt_pk_bf16_f32 v180, v172, v173
	v_cvt_pk_bf16_f32 v181, v174, v175
	v_add_u32_e32 v194, 0x1000, v190
	global_store_dwordx2 v194, v[180:181], s[28:29]
	s_waitcnt vmcnt(31)
	v_lshlrev_b32_e32 v164, 16, v106
	v_and_b32_e32 v165, 0xffff0000, v106
	v_lshlrev_b32_e32 v166, 16, v107
	v_and_b32_e32 v167, 0xffff0000, v107
	v_pk_add_f32 v[184:185], v[184:185], v[164:165]
	v_pk_add_f32 v[186:187], v[186:187], v[166:167]
	v_lshlrev_b32_e32 v168, 16, v98
	v_and_b32_e32 v169, 0xffff0000, v98
	v_lshlrev_b32_e32 v170, 16, v99
	v_and_b32_e32 v171, 0xffff0000, v99
	v_pk_add_f32 v[184:185], v[184:185], v[168:169] neg_lo:[0,1] neg_hi:[0,1]
	v_pk_add_f32 v[186:187], v[186:187], v[170:171] neg_lo:[0,1] neg_hi:[0,1]
	v_pk_fma_f32 v[172:173], v[188:189], v[184:185], v[164:165] op_sel_hi:[0,1,1] neg_lo:[0,0,1] neg_hi:[0,0,1]
	v_pk_fma_f32 v[174:175], v[188:189], v[186:187], v[166:167] op_sel_hi:[0,1,1] neg_lo:[0,0,1] neg_hi:[0,0,1]
	v_cvt_pk_bf16_f32 v182, v172, v173
	v_cvt_pk_bf16_f32 v183, v174, v175
	global_store_dwordx2 v194, v[182:183], s[28:29] offset:2048
	s_waitcnt vmcnt(31)
	v_lshlrev_b32_e32 v164, 16, v108
	v_and_b32_e32 v165, 0xffff0000, v108
	v_lshlrev_b32_e32 v166, 16, v109
	v_and_b32_e32 v167, 0xffff0000, v109
	v_pk_add_f32 v[184:185], v[184:185], v[164:165]
	v_pk_add_f32 v[186:187], v[186:187], v[166:167]
	v_lshlrev_b32_e32 v168, 16, v100
	v_and_b32_e32 v169, 0xffff0000, v100
	v_lshlrev_b32_e32 v170, 16, v101
	v_and_b32_e32 v171, 0xffff0000, v101
	v_pk_add_f32 v[184:185], v[184:185], v[168:169] neg_lo:[0,1] neg_hi:[0,1]
	v_pk_add_f32 v[186:187], v[186:187], v[170:171] neg_lo:[0,1] neg_hi:[0,1]
	v_pk_fma_f32 v[172:173], v[188:189], v[184:185], v[164:165] op_sel_hi:[0,1,1] neg_lo:[0,0,1] neg_hi:[0,0,1]
	v_pk_fma_f32 v[174:175], v[188:189], v[186:187], v[166:167] op_sel_hi:[0,1,1] neg_lo:[0,0,1] neg_hi:[0,0,1]
	v_cvt_pk_bf16_f32 v176, v172, v173
	v_cvt_pk_bf16_f32 v177, v174, v175
	v_add_u32_e32 v193, 0x2000, v190
	global_store_dwordx2 v193, v[176:177], s[28:29]
	s_waitcnt vmcnt(31)
	v_lshlrev_b32_e32 v164, 16, v110
	v_and_b32_e32 v165, 0xffff0000, v110
	v_lshlrev_b32_e32 v166, 16, v111
	v_and_b32_e32 v167, 0xffff0000, v111
	v_pk_add_f32 v[184:185], v[184:185], v[164:165]
	v_pk_add_f32 v[186:187], v[186:187], v[166:167]
	v_lshlrev_b32_e32 v168, 16, v102
	v_and_b32_e32 v169, 0xffff0000, v102
	v_lshlrev_b32_e32 v170, 16, v103
	v_and_b32_e32 v171, 0xffff0000, v103
	v_pk_add_f32 v[184:185], v[184:185], v[168:169] neg_lo:[0,1] neg_hi:[0,1]
	v_pk_add_f32 v[186:187], v[186:187], v[170:171] neg_lo:[0,1] neg_hi:[0,1]
	v_pk_fma_f32 v[172:173], v[188:189], v[184:185], v[164:165] op_sel_hi:[0,1,1] neg_lo:[0,0,1] neg_hi:[0,0,1]
	v_pk_fma_f32 v[174:175], v[188:189], v[186:187], v[166:167] op_sel_hi:[0,1,1] neg_lo:[0,0,1] neg_hi:[0,0,1]
	v_cvt_pk_bf16_f32 v178, v172, v173
	v_cvt_pk_bf16_f32 v179, v174, v175
	global_store_dwordx2 v193, v[178:179], s[28:29] offset:2048
	s_waitcnt vmcnt(31)
	v_lshlrev_b32_e32 v164, 16, v112
	v_and_b32_e32 v165, 0xffff0000, v112
	v_lshlrev_b32_e32 v166, 16, v113
	v_and_b32_e32 v167, 0xffff0000, v113
	v_pk_add_f32 v[184:185], v[184:185], v[164:165]
	v_pk_add_f32 v[186:187], v[186:187], v[166:167]
	v_lshlrev_b32_e32 v168, 16, v104
	v_and_b32_e32 v169, 0xffff0000, v104
	v_lshlrev_b32_e32 v170, 16, v105
	v_and_b32_e32 v171, 0xffff0000, v105
	v_pk_add_f32 v[184:185], v[184:185], v[168:169] neg_lo:[0,1] neg_hi:[0,1]
	v_pk_add_f32 v[186:187], v[186:187], v[170:171] neg_lo:[0,1] neg_hi:[0,1]
	v_pk_fma_f32 v[172:173], v[188:189], v[184:185], v[164:165] op_sel_hi:[0,1,1] neg_lo:[0,0,1] neg_hi:[0,0,1]
	v_pk_fma_f32 v[174:175], v[188:189], v[186:187], v[166:167] op_sel_hi:[0,1,1] neg_lo:[0,0,1] neg_hi:[0,0,1]
	v_cvt_pk_bf16_f32 v180, v172, v173
	v_cvt_pk_bf16_f32 v181, v174, v175
	v_add_u32_e32 v194, 0x3000, v190
	global_store_dwordx2 v194, v[180:181], s[28:29]
	s_waitcnt vmcnt(31)
	v_lshlrev_b32_e32 v164, 16, v114
	v_and_b32_e32 v165, 0xffff0000, v114
	v_lshlrev_b32_e32 v166, 16, v115
	v_and_b32_e32 v167, 0xffff0000, v115
	v_pk_add_f32 v[184:185], v[184:185], v[164:165]
	v_pk_add_f32 v[186:187], v[186:187], v[166:167]
	v_lshlrev_b32_e32 v168, 16, v106
	v_and_b32_e32 v169, 0xffff0000, v106
	v_lshlrev_b32_e32 v170, 16, v107
	v_and_b32_e32 v171, 0xffff0000, v107
	v_pk_add_f32 v[184:185], v[184:185], v[168:169] neg_lo:[0,1] neg_hi:[0,1]
	v_pk_add_f32 v[186:187], v[186:187], v[170:171] neg_lo:[0,1] neg_hi:[0,1]
	v_pk_fma_f32 v[172:173], v[188:189], v[184:185], v[164:165] op_sel_hi:[0,1,1] neg_lo:[0,0,1] neg_hi:[0,0,1]
	v_pk_fma_f32 v[174:175], v[188:189], v[186:187], v[166:167] op_sel_hi:[0,1,1] neg_lo:[0,0,1] neg_hi:[0,0,1]
	v_cvt_pk_bf16_f32 v182, v172, v173
	v_cvt_pk_bf16_f32 v183, v174, v175
	global_store_dwordx2 v194, v[182:183], s[28:29] offset:2048
	s_waitcnt vmcnt(31)
; #define GAS __attribute__((address_space(1)))
; __device__ __forceinline__ unsigned pk2(float lo, float hi) { const f32x2 v = {lo, hi}; return __builtin_bit_cast(unsigned, __builtin_convertvector(v, b16x2)); }
; template <int W>
; __device__ __forceinline__ void pool_item(const bf16* U, bf16* Z, int b, int t0, int g, int lane) {
;     ...
;     for (int i = 0; i < 32; ++i) { const int t = t0 + i;
;         const u32x2 v = *(const GAS u32x2*)(U + base + (size_t)t * D);
;         const float c0 = bf2f(v.x & 0xffffu), c1 = bf2f(v.x >> 16), c2 = bf2f(v.y & 0xffffu), c3 = bf2f(v.y >> 16);
;         s[0] += c0; s[1] += c1; s[2] += c2; s[3] += c3;
;         if (t - W >= 0) { const u32x2 o = *(const GAS u32x2*)(U + base + (size_t)(t - W) * D);
;             s[0] -= bf2f(o.x & 0xffffu); s[1] -= bf2f(o.x >> 16); s[2] -= bf2f(o.y & 0xffffu); s[3] -= bf2f(o.y >> 16); }
;         const float inv = 1.0f / (float)((t + 1) < W ? (t + 1) : W);
;         u32x2 w; w.x = pk2(s[0] * inv - c0, s[1] * inv - c1); w.y = pk2(s[2] * inv - c2, s[3] * inv - c3);
;         *(GAS u32x2*)(Z + base + (size_t)t * D) = w; }
; }
	v_lshlrev_b32_e32 v164, 16, v116
	v_and_b32_e32 v165, 0xffff0000, v116
	v_lshlrev_b32_e32 v166, 16, v117
	v_and_b32_e32 v167, 0xffff0000, v117
	v_pk_add_f32 v[184:185], v[184:185], v[164:165]
	v_pk_add_f32 v[186:187], v[186:187], v[166:167]
	v_lshlrev_b32_e32 v168, 16, v108
	v_and_b32_e32 v169, 0xffff0000, v108
	v_lshlrev_b32_e32 v170, 16, v109
	v_and_b32_e32 v171, 0xffff0000, v109
	v_pk_add_f32 v[184:185], v[184:185], v[168:169] neg_lo:[0,1] neg_hi:[0,1]
	v_pk_add_f32 v[186:187], v[186:187], v[170:171] neg_lo:[0,1] neg_hi:[0,1]
	v_pk_fma_f32 v[172:173], v[188:189], v[184:185], v[164:165] op_sel_hi:[0,1,1] neg_lo:[0,0,1] neg_hi:[0,0,1]
	v_pk_fma_f32 v[174:175], v[188:189], v[186:187], v[166:167] op_sel_hi:[0,1,1] neg_lo:[0,0,1] neg_hi:[0,0,1]
	v_cvt_pk_bf16_f32 v176, v172, v173
	v_cvt_pk_bf16_f32 v177, v174, v175
	v_add_u32_e32 v193, 0x4000, v190
	global_store_dwordx2 v193, v[176:177], s[28:29]
	s_waitcnt vmcnt(31)
	v_lshlrev_b32_e32 v164, 16, v118
	v_and_b32_e32 v165, 0xffff0000, v118
	v_lshlrev_b32_e32 v166, 16, v119
	v_and_b32_e32 v167, 0xffff0000, v119
	v_pk_add_f32 v[184:185], v[184:185], v[164:165]
	v_pk_add_f32 v[186:187], v[186:187], v[166:167]
	v_lshlrev_b32_e32 v168, 16, v110
	v_and_b32_e32 v169, 0xffff0000, v110
	v_lshlrev_b32_e32 v170, 16, v111
	v_and_b32_e32 v171, 0xffff0000, v111
	v_pk_add_f32 v[184:185], v[184:185], v[168:169] neg_lo:[0,1] neg_hi:[0,1]
	v_pk_add_f32 v[186:187], v[186:187], v[170:171] neg_lo:[0,1] neg_hi:[0,1]
	v_pk_fma_f32 v[172:173], v[188:189], v[184:185], v[164:165] op_sel_hi:[0,1,1] neg_lo:[0,0,1] neg_hi:[0,0,1]
	v_pk_fma_f32 v[174:175], v[188:189], v[186:187], v[166:167] op_sel_hi:[0,1,1] neg_lo:[0,0,1] neg_hi:[0,0,1]
	v_cvt_pk_bf16_f32 v178, v172, v173
	v_cvt_pk_bf16_f32 v179, v174, v175
	global_store_dwordx2 v193, v[178:179], s[28:29] offset:2048
	s_waitcnt vmcnt(31)
	v_lshlrev_b32_e32 v164, 16, v120
	v_and_b32_e32 v165, 0xffff0000, v120
	v_lshlrev_b32_e32 v166, 16, v121
	v_and_b32_e32 v167, 0xffff0000, v121
	v_pk_add_f32 v[184:185], v[184:185], v[164:165]
	v_pk_add_f32 v[186:187], v[186:187], v[166:167]
	v_lshlrev_b32_e32 v168, 16, v112
	v_and_b32_e32 v169, 0xffff0000, v112
	v_lshlrev_b32_e32 v170, 16, v113
	v_and_b32_e32 v171, 0xffff0000, v113
	v_pk_add_f32 v[184:185], v[184:185], v[168:169] neg_lo:[0,1] neg_hi:[0,1]
	v_pk_add_f32 v[186:187], v[186:187], v[170:171] neg_lo:[0,1] neg_hi:[0,1]
	v_pk_fma_f32 v[172:173], v[188:189], v[184:185], v[164:165] op_sel_hi:[0,1,1] neg_lo:[0,0,1] neg_hi:[0,0,1]
	v_pk_fma_f32 v[174:175], v[188:189], v[186:187], v[166:167] op_sel_hi:[0,1,1] neg_lo:[0,0,1] neg_hi:[0,0,1]
	v_cvt_pk_bf16_f32 v180, v172, v173
	v_cvt_pk_bf16_f32 v181, v174, v175
	v_add_u32_e32 v194, 0x5000, v190
	global_store_dwordx2 v194, v[180:181], s[28:29]
	s_waitcnt vmcnt(31)
	v_lshlrev_b32_e32 v164, 16, v122
	v_and_b32_e32 v165, 0xffff0000, v122
	v_lshlrev_b32_e32 v166, 16, v123
	v_and_b32_e32 v167, 0xffff0000, v123
	v_pk_add_f32 v[184:185], v[184:185], v[164:165]
	v_pk_add_f32 v[186:187], v[186:187], v[166:167]
	v_lshlrev_b32_e32 v168, 16, v114
	v_and_b32_e32 v169, 0xffff0000, v114
	v_lshlrev_b32_e32 v170, 16, v115
	v_and_b32_e32 v171, 0xffff0000, v115
	v_pk_add_f32 v[184:185], v[184:185], v[168:169] neg_lo:[0,1] neg_hi:[0,1]
	v_pk_add_f32 v[186:187], v[186:187], v[170:171] neg_lo:[0,1] neg_hi:[0,1]
	v_pk_fma_f32 v[172:173], v[188:189], v[184:185], v[164:165] op_sel_hi:[0,1,1] neg_lo:[0,0,1] neg_hi:[0,0,1]
	v_pk_fma_f32 v[174:175], v[188:189], v[186:187], v[166:167] op_sel_hi:[0,1,1] neg_lo:[0,0,1] neg_hi:[0,0,1]
	v_cvt_pk_bf16_f32 v182, v172, v173
	v_cvt_pk_bf16_f32 v183, v174, v175
	global_store_dwordx2 v194, v[182:183], s[28:29] offset:2048
	s_waitcnt vmcnt(31)
	v_lshlrev_b32_e32 v164, 16, v124
	v_and_b32_e32 v165, 0xffff0000, v124
	v_lshlrev_b32_e32 v166, 16, v125
	v_and_b32_e32 v167, 0xffff0000, v125
	v_pk_add_f32 v[184:185], v[184:185], v[164:165]
	v_pk_add_f32 v[186:187], v[186:187], v[166:167]
	v_lshlrev_b32_e32 v168, 16, v116
	v_and_b32_e32 v169, 0xffff0000, v116
	v_lshlrev_b32_e32 v170, 16, v117
	v_and_b32_e32 v171, 0xffff0000, v117
	v_pk_add_f32 v[184:185], v[184:185], v[168:169] neg_lo:[0,1] neg_hi:[0,1]
	v_pk_add_f32 v[186:187], v[186:187], v[170:171] neg_lo:[0,1] neg_hi:[0,1]
	v_pk_fma_f32 v[172:173], v[188:189], v[184:185], v[164:165] op_sel_hi:[0,1,1] neg_lo:[0,0,1] neg_hi:[0,0,1]
	v_pk_fma_f32 v[174:175], v[188:189], v[186:187], v[166:167] op_sel_hi:[0,1,1] neg_lo:[0,0,1] neg_hi:[0,0,1]
	v_cvt_pk_bf16_f32 v176, v172, v173
	v_cvt_pk_bf16_f32 v177, v174, v175
	v_add_u32_e32 v193, 0x6000, v190
	global_store_dwordx2 v193, v[176:177], s[28:29]
	s_waitcnt vmcnt(31)
	v_lshlrev_b32_e32 v164, 16, v126
	v_and_b32_e32 v165, 0xffff0000, v126
	v_lshlrev_b32_e32 v166, 16, v127
	v_and_b32_e32 v167, 0xffff0000, v127
	v_pk_add_f32 v[184:185], v[184:185], v[164:165]
	v_pk_add_f32 v[186:187], v[186:187], v[166:167]
	v_lshlrev_b32_e32 v168, 16, v118
	v_and_b32_e32 v169, 0xffff0000, v118
	v_lshlrev_b32_e32 v170, 16, v119
	v_and_b32_e32 v171, 0xffff0000, v119
	v_pk_add_f32 v[184:185], v[184:185], v[168:169] neg_lo:[0,1] neg_hi:[0,1]
	v_pk_add_f32 v[186:187], v[186:187], v[170:171] neg_lo:[0,1] neg_hi:[0,1]
	v_pk_fma_f32 v[172:173], v[188:189], v[184:185], v[164:165] op_sel_hi:[0,1,1] neg_lo:[0,0,1] neg_hi:[0,0,1]
	v_pk_fma_f32 v[174:175], v[188:189], v[186:187], v[166:167] op_sel_hi:[0,1,1] neg_lo:[0,0,1] neg_hi:[0,0,1]
	v_cvt_pk_bf16_f32 v178, v172, v173
	v_cvt_pk_bf16_f32 v179, v174, v175
	global_store_dwordx2 v193, v[178:179], s[28:29] offset:2048
	s_waitcnt vmcnt(31)
; #define GAS __attribute__((address_space(1)))
; __device__ __forceinline__ unsigned pk2(float lo, float hi) { const f32x2 v = {lo, hi}; return __builtin_bit_cast(unsigned, __builtin_convertvector(v, b16x2)); }
; template <int W>
; __device__ __forceinline__ void pool_item(const bf16* U, bf16* Z, int b, int t0, int g, int lane) {
;     ...
;     for (int i = 0; i < 32; ++i) { const int t = t0 + i;
;         const u32x2 v = *(const GAS u32x2*)(U + base + (size_t)t * D);
;         const float c0 = bf2f(v.x & 0xffffu), c1 = bf2f(v.x >> 16), c2 = bf2f(v.y & 0xffffu), c3 = bf2f(v.y >> 16);
;         s[0] += c0; s[1] += c1; s[2] += c2; s[3] += c3;
;         if (t - W >= 0) { const u32x2 o = *(const GAS u32x2*)(U + base + (size_t)(t - W) * D);
;             s[0] -= bf2f(o.x & 0xffffu); s[1] -= bf2f(o.x >> 16); s[2] -= bf2f(o.y & 0xffffu); s[3] -= bf2f(o.y >> 16); }
;         const float inv = 1.0f / (float)((t + 1) < W ? (t + 1) : W);
;         u32x2 w; w.x = pk2(s[0] * inv - c0, s[1] * inv - c1); w.y = pk2(s[2] * inv - c2, s[3] * inv - c3);
;         *(GAS u32x2*)(Z + base + (size_t)t * D) = w; }
; }
	v_lshlrev_b32_e32 v164, 16, v128
	v_and_b32_e32 v165, 0xffff0000, v128
	v_lshlrev_b32_e32 v166, 16, v129
	v_and_b32_e32 v167, 0xffff0000, v129
	v_pk_add_f32 v[184:185], v[184:185], v[164:165]
	v_pk_add_f32 v[186:187], v[186:187], v[166:167]
	v_lshlrev_b32_e32 v168, 16, v120
	v_and_b32_e32 v169, 0xffff0000, v120
	v_lshlrev_b32_e32 v170, 16, v121
	v_and_b32_e32 v171, 0xffff0000, v121
	v_pk_add_f32 v[184:185], v[184:185], v[168:169] neg_lo:[0,1] neg_hi:[0,1]
	v_pk_add_f32 v[186:187], v[186:187], v[170:171] neg_lo:[0,1] neg_hi:[0,1]
	v_pk_fma_f32 v[172:173], v[188:189], v[184:185], v[164:165] op_sel_hi:[0,1,1] neg_lo:[0,0,1] neg_hi:[0,0,1]
	v_pk_fma_f32 v[174:175], v[188:189], v[186:187], v[166:167] op_sel_hi:[0,1,1] neg_lo:[0,0,1] neg_hi:[0,0,1]
	v_cvt_pk_bf16_f32 v180, v172, v173
	v_cvt_pk_bf16_f32 v181, v174, v175
	v_add_u32_e32 v194, 0x7000, v190
	global_store_dwordx2 v194, v[180:181], s[28:29]
	s_waitcnt vmcnt(31)
	v_lshlrev_b32_e32 v164, 16, v130
	v_and_b32_e32 v165, 0xffff0000, v130
	v_lshlrev_b32_e32 v166, 16, v131
	v_and_b32_e32 v167, 0xffff0000, v131
	v_pk_add_f32 v[184:185], v[184:185], v[164:165]
	v_pk_add_f32 v[186:187], v[186:187], v[166:167]
	v_lshlrev_b32_e32 v168, 16, v122
	v_and_b32_e32 v169, 0xffff0000, v122
	v_lshlrev_b32_e32 v170, 16, v123
	v_and_b32_e32 v171, 0xffff0000, v123
	v_pk_add_f32 v[184:185], v[184:185], v[168:169] neg_lo:[0,1] neg_hi:[0,1]
	v_pk_add_f32 v[186:187], v[186:187], v[170:171] neg_lo:[0,1] neg_hi:[0,1]
	v_pk_fma_f32 v[172:173], v[188:189], v[184:185], v[164:165] op_sel_hi:[0,1,1] neg_lo:[0,0,1] neg_hi:[0,0,1]
	v_pk_fma_f32 v[174:175], v[188:189], v[186:187], v[166:167] op_sel_hi:[0,1,1] neg_lo:[0,0,1] neg_hi:[0,0,1]
	v_cvt_pk_bf16_f32 v182, v172, v173
	v_cvt_pk_bf16_f32 v183, v174, v175
	global_store_dwordx2 v194, v[182:183], s[28:29] offset:2048
	s_waitcnt vmcnt(31)
	v_lshlrev_b32_e32 v164, 16, v132
	v_and_b32_e32 v165, 0xffff0000, v132
	v_lshlrev_b32_e32 v166, 16, v133
	v_and_b32_e32 v167, 0xffff0000, v133
	v_pk_add_f32 v[184:185], v[184:185], v[164:165]
	v_pk_add_f32 v[186:187], v[186:187], v[166:167]
	v_lshlrev_b32_e32 v168, 16, v124
	v_and_b32_e32 v169, 0xffff0000, v124
	v_lshlrev_b32_e32 v170, 16, v125
	v_and_b32_e32 v171, 0xffff0000, v125
	v_pk_add_f32 v[184:185], v[184:185], v[168:169] neg_lo:[0,1] neg_hi:[0,1]
	v_pk_add_f32 v[186:187], v[186:187], v[170:171] neg_lo:[0,1] neg_hi:[0,1]
	v_pk_fma_f32 v[172:173], v[188:189], v[184:185], v[164:165] op_sel_hi:[0,1,1] neg_lo:[0,0,1] neg_hi:[0,0,1]
	v_pk_fma_f32 v[174:175], v[188:189], v[186:187], v[166:167] op_sel_hi:[0,1,1] neg_lo:[0,0,1] neg_hi:[0,0,1]
	v_cvt_pk_bf16_f32 v176, v172, v173
	v_cvt_pk_bf16_f32 v177, v174, v175
	v_add_u32_e32 v193, 0x8000, v190
	global_store_dwordx2 v193, v[176:177], s[28:29]
	s_waitcnt vmcnt(31)
	v_lshlrev_b32_e32 v164, 16, v134
	v_and_b32_e32 v165, 0xffff0000, v134
	v_lshlrev_b32_e32 v166, 16, v135
	v_and_b32_e32 v167, 0xffff0000, v135
	v_pk_add_f32 v[184:185], v[184:185], v[164:165]
	v_pk_add_f32 v[186:187], v[186:187], v[166:167]
	v_lshlrev_b32_e32 v168, 16, v126
	v_and_b32_e32 v169, 0xffff0000, v126
	v_lshlrev_b32_e32 v170, 16, v127
	v_and_b32_e32 v171, 0xffff0000, v127
	v_pk_add_f32 v[184:185], v[184:185], v[168:169] neg_lo:[0,1] neg_hi:[0,1]
	v_pk_add_f32 v[186:187], v[186:187], v[170:171] neg_lo:[0,1] neg_hi:[0,1]
	v_pk_fma_f32 v[172:173], v[188:189], v[184:185], v[164:165] op_sel_hi:[0,1,1] neg_lo:[0,0,1] neg_hi:[0,0,1]
	v_pk_fma_f32 v[174:175], v[188:189], v[186:187], v[166:167] op_sel_hi:[0,1,1] neg_lo:[0,0,1] neg_hi:[0,0,1]
	v_cvt_pk_bf16_f32 v178, v172, v173
	v_cvt_pk_bf16_f32 v179, v174, v175
	global_store_dwordx2 v193, v[178:179], s[28:29] offset:2048
	s_waitcnt vmcnt(31)
	v_lshlrev_b32_e32 v164, 16, v136
	v_and_b32_e32 v165, 0xffff0000, v136
	v_lshlrev_b32_e32 v166, 16, v137
	v_and_b32_e32 v167, 0xffff0000, v137
	v_pk_add_f32 v[184:185], v[184:185], v[164:165]
	v_pk_add_f32 v[186:187], v[186:187], v[166:167]
	v_lshlrev_b32_e32 v168, 16, v128
	v_and_b32_e32 v169, 0xffff0000, v128
	v_lshlrev_b32_e32 v170, 16, v129
	v_and_b32_e32 v171, 0xffff0000, v129
	v_pk_add_f32 v[184:185], v[184:185], v[168:169] neg_lo:[0,1] neg_hi:[0,1]
	v_pk_add_f32 v[186:187], v[186:187], v[170:171] neg_lo:[0,1] neg_hi:[0,1]
	v_pk_fma_f32 v[172:173], v[188:189], v[184:185], v[164:165] op_sel_hi:[0,1,1] neg_lo:[0,0,1] neg_hi:[0,0,1]
	v_pk_fma_f32 v[174:175], v[188:189], v[186:187], v[166:167] op_sel_hi:[0,1,1] neg_lo:[0,0,1] neg_hi:[0,0,1]
	v_cvt_pk_bf16_f32 v180, v172, v173
	v_cvt_pk_bf16_f32 v181, v174, v175
	v_add_u32_e32 v194, 0x9000, v190
	global_store_dwordx2 v194, v[180:181], s[28:29]
	s_waitcnt vmcnt(31)
	v_lshlrev_b32_e32 v164, 16, v138
	v_and_b32_e32 v165, 0xffff0000, v138
	v_lshlrev_b32_e32 v166, 16, v139
	v_and_b32_e32 v167, 0xffff0000, v139
	v_pk_add_f32 v[184:185], v[184:185], v[164:165]
	v_pk_add_f32 v[186:187], v[186:187], v[166:167]
	v_lshlrev_b32_e32 v168, 16, v130
	v_and_b32_e32 v169, 0xffff0000, v130
	v_lshlrev_b32_e32 v170, 16, v131
	v_and_b32_e32 v171, 0xffff0000, v131
	v_pk_add_f32 v[184:185], v[184:185], v[168:169] neg_lo:[0,1] neg_hi:[0,1]
	v_pk_add_f32 v[186:187], v[186:187], v[170:171] neg_lo:[0,1] neg_hi:[0,1]
	v_pk_fma_f32 v[172:173], v[188:189], v[184:185], v[164:165] op_sel_hi:[0,1,1] neg_lo:[0,0,1] neg_hi:[0,0,1]
	v_pk_fma_f32 v[174:175], v[188:189], v[186:187], v[166:167] op_sel_hi:[0,1,1] neg_lo:[0,0,1] neg_hi:[0,0,1]
	v_cvt_pk_bf16_f32 v182, v172, v173
	v_cvt_pk_bf16_f32 v183, v174, v175
	global_store_dwordx2 v194, v[182:183], s[28:29] offset:2048
	s_waitcnt vmcnt(31)
; #define GAS __attribute__((address_space(1)))
; __device__ __forceinline__ unsigned pk2(float lo, float hi) { const f32x2 v = {lo, hi}; return __builtin_bit_cast(unsigned, __builtin_convertvector(v, b16x2)); }
; template <int W>
; __device__ __forceinline__ void pool_item(const bf16* U, bf16* Z, int b, int t0, int g, int lane) {
;     ...
;     for (int i = 0; i < 32; ++i) { const int t = t0 + i;
;         const u32x2 v = *(const GAS u32x2*)(U + base + (size_t)t * D);
;         const float c0 = bf2f(v.x & 0xffffu), c1 = bf2f(v.x >> 16), c2 = bf2f(v.y & 0xffffu), c3 = bf2f(v.y >> 16);
;         s[0] += c0; s[1] += c1; s[2] += c2; s[3] += c3;
;         if (t - W >= 0) { const u32x2 o = *(const GAS u32x2*)(U + base + (size_t)(t - W) * D);
;             s[0] -= bf2f(o.x & 0xffffu); s[1] -= bf2f(o.x >> 16); s[2] -= bf2f(o.y & 0xffffu); s[3] -= bf2f(o.y >> 16); }
;         const float inv = 1.0f / (float)((t + 1) < W ? (t + 1) : W);
;         u32x2 w; w.x = pk2(s[0] * inv - c0, s[1] * inv - c1); w.y = pk2(s[2] * inv - c2, s[3] * inv - c3);
;         *(GAS u32x2*)(Z + base + (size_t)t * D) = w; }
; }
	v_lshlrev_b32_e32 v164, 16, v140
	v_and_b32_e32 v165, 0xffff0000, v140
	v_lshlrev_b32_e32 v166, 16, v141
	v_and_b32_e32 v167, 0xffff0000, v141
	v_pk_add_f32 v[184:185], v[184:185], v[164:165]
	v_pk_add_f32 v[186:187], v[186:187], v[166:167]
	v_lshlrev_b32_e32 v168, 16, v132
	v_and_b32_e32 v169, 0xffff0000, v132
	v_lshlrev_b32_e32 v170, 16, v133
	v_and_b32_e32 v171, 0xffff0000, v133
	v_pk_add_f32 v[184:185], v[184:185], v[168:169] neg_lo:[0,1] neg_hi:[0,1]
	v_pk_add_f32 v[186:187], v[186:187], v[170:171] neg_lo:[0,1] neg_hi:[0,1]
	v_pk_fma_f32 v[172:173], v[188:189], v[184:185], v[164:165] op_sel_hi:[0,1,1] neg_lo:[0,0,1] neg_hi:[0,0,1]
	v_pk_fma_f32 v[174:175], v[188:189], v[186:187], v[166:167] op_sel_hi:[0,1,1] neg_lo:[0,0,1] neg_hi:[0,0,1]
	v_cvt_pk_bf16_f32 v176, v172, v173
	v_cvt_pk_bf16_f32 v177, v174, v175
	v_add_u32_e32 v193, 0xa000, v190
	global_store_dwordx2 v193, v[176:177], s[28:29]
	s_waitcnt vmcnt(31)
	v_lshlrev_b32_e32 v164, 16, v142
	v_and_b32_e32 v165, 0xffff0000, v142
	v_lshlrev_b32_e32 v166, 16, v143
	v_and_b32_e32 v167, 0xffff0000, v143
	v_pk_add_f32 v[184:185], v[184:185], v[164:165]
	v_pk_add_f32 v[186:187], v[186:187], v[166:167]
	v_lshlrev_b32_e32 v168, 16, v134
	v_and_b32_e32 v169, 0xffff0000, v134
	v_lshlrev_b32_e32 v170, 16, v135
	v_and_b32_e32 v171, 0xffff0000, v135
	v_pk_add_f32 v[184:185], v[184:185], v[168:169] neg_lo:[0,1] neg_hi:[0,1]
	v_pk_add_f32 v[186:187], v[186:187], v[170:171] neg_lo:[0,1] neg_hi:[0,1]
	v_pk_fma_f32 v[172:173], v[188:189], v[184:185], v[164:165] op_sel_hi:[0,1,1] neg_lo:[0,0,1] neg_hi:[0,0,1]
	v_pk_fma_f32 v[174:175], v[188:189], v[186:187], v[166:167] op_sel_hi:[0,1,1] neg_lo:[0,0,1] neg_hi:[0,0,1]
	v_cvt_pk_bf16_f32 v178, v172, v173
	v_cvt_pk_bf16_f32 v179, v174, v175
	global_store_dwordx2 v193, v[178:179], s[28:29] offset:2048
	s_waitcnt vmcnt(31)
	v_lshlrev_b32_e32 v164, 16, v144
	v_and_b32_e32 v165, 0xffff0000, v144
	v_lshlrev_b32_e32 v166, 16, v145
	v_and_b32_e32 v167, 0xffff0000, v145
	v_pk_add_f32 v[184:185], v[184:185], v[164:165]
	v_pk_add_f32 v[186:187], v[186:187], v[166:167]
	v_lshlrev_b32_e32 v168, 16, v136
	v_and_b32_e32 v169, 0xffff0000, v136
	v_lshlrev_b32_e32 v170, 16, v137
	v_and_b32_e32 v171, 0xffff0000, v137
	v_pk_add_f32 v[184:185], v[184:185], v[168:169] neg_lo:[0,1] neg_hi:[0,1]
	v_pk_add_f32 v[186:187], v[186:187], v[170:171] neg_lo:[0,1] neg_hi:[0,1]
	v_pk_fma_f32 v[172:173], v[188:189], v[184:185], v[164:165] op_sel_hi:[0,1,1] neg_lo:[0,0,1] neg_hi:[0,0,1]
	v_pk_fma_f32 v[174:175], v[188:189], v[186:187], v[166:167] op_sel_hi:[0,1,1] neg_lo:[0,0,1] neg_hi:[0,0,1]
	v_cvt_pk_bf16_f32 v180, v172, v173
	v_cvt_pk_bf16_f32 v181, v174, v175
	v_add_u32_e32 v194, 0xb000, v190
	global_store_dwordx2 v194, v[180:181], s[28:29]
	s_waitcnt vmcnt(31)
	v_lshlrev_b32_e32 v164, 16, v146
	v_and_b32_e32 v165, 0xffff0000, v146
	v_lshlrev_b32_e32 v166, 16, v147
	v_and_b32_e32 v167, 0xffff0000, v147
	v_pk_add_f32 v[184:185], v[184:185], v[164:165]
	v_pk_add_f32 v[186:187], v[186:187], v[166:167]
	v_lshlrev_b32_e32 v168, 16, v138
	v_and_b32_e32 v169, 0xffff0000, v138
	v_lshlrev_b32_e32 v170, 16, v139
	v_and_b32_e32 v171, 0xffff0000, v139
	v_pk_add_f32 v[184:185], v[184:185], v[168:169] neg_lo:[0,1] neg_hi:[0,1]
	v_pk_add_f32 v[186:187], v[186:187], v[170:171] neg_lo:[0,1] neg_hi:[0,1]
	v_pk_fma_f32 v[172:173], v[188:189], v[184:185], v[164:165] op_sel_hi:[0,1,1] neg_lo:[0,0,1] neg_hi:[0,0,1]
	v_pk_fma_f32 v[174:175], v[188:189], v[186:187], v[166:167] op_sel_hi:[0,1,1] neg_lo:[0,0,1] neg_hi:[0,0,1]
	v_cvt_pk_bf16_f32 v182, v172, v173
	v_cvt_pk_bf16_f32 v183, v174, v175
	global_store_dwordx2 v194, v[182:183], s[28:29] offset:2048
	s_waitcnt vmcnt(31)
	v_lshlrev_b32_e32 v164, 16, v148
	v_and_b32_e32 v165, 0xffff0000, v148
	v_lshlrev_b32_e32 v166, 16, v149
	v_and_b32_e32 v167, 0xffff0000, v149
	v_pk_add_f32 v[184:185], v[184:185], v[164:165]
	v_pk_add_f32 v[186:187], v[186:187], v[166:167]
	v_lshlrev_b32_e32 v168, 16, v140
	v_and_b32_e32 v169, 0xffff0000, v140
	v_lshlrev_b32_e32 v170, 16, v141
	v_and_b32_e32 v171, 0xffff0000, v141
	v_pk_add_f32 v[184:185], v[184:185], v[168:169] neg_lo:[0,1] neg_hi:[0,1]
	v_pk_add_f32 v[186:187], v[186:187], v[170:171] neg_lo:[0,1] neg_hi:[0,1]
	v_pk_fma_f32 v[172:173], v[188:189], v[184:185], v[164:165] op_sel_hi:[0,1,1] neg_lo:[0,0,1] neg_hi:[0,0,1]
	v_pk_fma_f32 v[174:175], v[188:189], v[186:187], v[166:167] op_sel_hi:[0,1,1] neg_lo:[0,0,1] neg_hi:[0,0,1]
	v_cvt_pk_bf16_f32 v176, v172, v173
	v_cvt_pk_bf16_f32 v177, v174, v175
	v_add_u32_e32 v193, 0xc000, v190
	global_store_dwordx2 v193, v[176:177], s[28:29]
	s_waitcnt vmcnt(31)
	v_lshlrev_b32_e32 v164, 16, v150
	v_and_b32_e32 v165, 0xffff0000, v150
	v_lshlrev_b32_e32 v166, 16, v151
	v_and_b32_e32 v167, 0xffff0000, v151
	v_pk_add_f32 v[184:185], v[184:185], v[164:165]
	v_pk_add_f32 v[186:187], v[186:187], v[166:167]
	v_lshlrev_b32_e32 v168, 16, v142
	v_and_b32_e32 v169, 0xffff0000, v142
	v_lshlrev_b32_e32 v170, 16, v143
	v_and_b32_e32 v171, 0xffff0000, v143
	v_pk_add_f32 v[184:185], v[184:185], v[168:169] neg_lo:[0,1] neg_hi:[0,1]
	v_pk_add_f32 v[186:187], v[186:187], v[170:171] neg_lo:[0,1] neg_hi:[0,1]
	v_pk_fma_f32 v[172:173], v[188:189], v[184:185], v[164:165] op_sel_hi:[0,1,1] neg_lo:[0,0,1] neg_hi:[0,0,1]
	v_pk_fma_f32 v[174:175], v[188:189], v[186:187], v[166:167] op_sel_hi:[0,1,1] neg_lo:[0,0,1] neg_hi:[0,0,1]
	v_cvt_pk_bf16_f32 v178, v172, v173
	v_cvt_pk_bf16_f32 v179, v174, v175
	global_store_dwordx2 v193, v[178:179], s[28:29] offset:2048
	s_waitcnt vmcnt(31)
; #define GAS __attribute__((address_space(1)))
; __device__ __forceinline__ unsigned pk2(float lo, float hi) { const f32x2 v = {lo, hi}; return __builtin_bit_cast(unsigned, __builtin_convertvector(v, b16x2)); }
; template <int W>
; __device__ __forceinline__ void pool_item(const bf16* U, bf16* Z, int b, int t0, int g, int lane) {
;     ...
;     for (int i = 0; i < 32; ++i) { const int t = t0 + i;
;         const u32x2 v = *(const GAS u32x2*)(U + base + (size_t)t * D);
;         const float c0 = bf2f(v.x & 0xffffu), c1 = bf2f(v.x >> 16), c2 = bf2f(v.y & 0xffffu), c3 = bf2f(v.y >> 16);
;         s[0] += c0; s[1] += c1; s[2] += c2; s[3] += c3;
;         if (t - W >= 0) { const u32x2 o = *(const GAS u32x2*)(U + base + (size_t)(t - W) * D);
;             s[0] -= bf2f(o.x & 0xffffu); s[1] -= bf2f(o.x >> 16); s[2] -= bf2f(o.y & 0xffffu); s[3] -= bf2f(o.y >> 16); }
;         const float inv = 1.0f / (float)((t + 1) < W ? (t + 1) : W);
;         u32x2 w; w.x = pk2(s[0] * inv - c0, s[1] * inv - c1); w.y = pk2(s[2] * inv - c2, s[3] * inv - c3);
;         *(GAS u32x2*)(Z + base + (size_t)t * D) = w; }
; }
	v_lshlrev_b32_e32 v164, 16, v152
	v_and_b32_e32 v165, 0xffff0000, v152
	v_lshlrev_b32_e32 v166, 16, v153
	v_and_b32_e32 v167, 0xffff0000, v153
	v_pk_add_f32 v[184:185], v[184:185], v[164:165]
	v_pk_add_f32 v[186:187], v[186:187], v[166:167]
	v_lshlrev_b32_e32 v168, 16, v144
	v_and_b32_e32 v169, 0xffff0000, v144
	v_lshlrev_b32_e32 v170, 16, v145
	v_and_b32_e32 v171, 0xffff0000, v145
	v_pk_add_f32 v[184:185], v[184:185], v[168:169] neg_lo:[0,1] neg_hi:[0,1]
	v_pk_add_f32 v[186:187], v[186:187], v[170:171] neg_lo:[0,1] neg_hi:[0,1]
	v_pk_fma_f32 v[172:173], v[188:189], v[184:185], v[164:165] op_sel_hi:[0,1,1] neg_lo:[0,0,1] neg_hi:[0,0,1]
	v_pk_fma_f32 v[174:175], v[188:189], v[186:187], v[166:167] op_sel_hi:[0,1,1] neg_lo:[0,0,1] neg_hi:[0,0,1]
	v_cvt_pk_bf16_f32 v180, v172, v173
	v_cvt_pk_bf16_f32 v181, v174, v175
	v_add_u32_e32 v194, 0xd000, v190
	global_store_dwordx2 v194, v[180:181], s[28:29]
	s_waitcnt vmcnt(31)
	v_lshlrev_b32_e32 v164, 16, v154
	v_and_b32_e32 v165, 0xffff0000, v154
	v_lshlrev_b32_e32 v166, 16, v155
	v_and_b32_e32 v167, 0xffff0000, v155
	v_pk_add_f32 v[184:185], v[184:185], v[164:165]
	v_pk_add_f32 v[186:187], v[186:187], v[166:167]
	v_lshlrev_b32_e32 v168, 16, v146
	v_and_b32_e32 v169, 0xffff0000, v146
	v_lshlrev_b32_e32 v170, 16, v147
	v_and_b32_e32 v171, 0xffff0000, v147
	v_pk_add_f32 v[184:185], v[184:185], v[168:169] neg_lo:[0,1] neg_hi:[0,1]
	v_pk_add_f32 v[186:187], v[186:187], v[170:171] neg_lo:[0,1] neg_hi:[0,1]
	v_pk_fma_f32 v[172:173], v[188:189], v[184:185], v[164:165] op_sel_hi:[0,1,1] neg_lo:[0,0,1] neg_hi:[0,0,1]
	v_pk_fma_f32 v[174:175], v[188:189], v[186:187], v[166:167] op_sel_hi:[0,1,1] neg_lo:[0,0,1] neg_hi:[0,0,1]
	v_cvt_pk_bf16_f32 v182, v172, v173
	v_cvt_pk_bf16_f32 v183, v174, v175
	global_store_dwordx2 v194, v[182:183], s[28:29] offset:2048
	s_waitcnt vmcnt(31)
	v_lshlrev_b32_e32 v164, 16, v156
	v_and_b32_e32 v165, 0xffff0000, v156
	v_lshlrev_b32_e32 v166, 16, v157
	v_and_b32_e32 v167, 0xffff0000, v157
	v_pk_add_f32 v[184:185], v[184:185], v[164:165]
	v_pk_add_f32 v[186:187], v[186:187], v[166:167]
	v_lshlrev_b32_e32 v168, 16, v148
	v_and_b32_e32 v169, 0xffff0000, v148
	v_lshlrev_b32_e32 v170, 16, v149
	v_and_b32_e32 v171, 0xffff0000, v149
	v_pk_add_f32 v[184:185], v[184:185], v[168:169] neg_lo:[0,1] neg_hi:[0,1]
	v_pk_add_f32 v[186:187], v[186:187], v[170:171] neg_lo:[0,1] neg_hi:[0,1]
	v_pk_fma_f32 v[172:173], v[188:189], v[184:185], v[164:165] op_sel_hi:[0,1,1] neg_lo:[0,0,1] neg_hi:[0,0,1]
	v_pk_fma_f32 v[174:175], v[188:189], v[186:187], v[166:167] op_sel_hi:[0,1,1] neg_lo:[0,0,1] neg_hi:[0,0,1]
	v_cvt_pk_bf16_f32 v176, v172, v173
	v_cvt_pk_bf16_f32 v177, v174, v175
	v_add_u32_e32 v193, 0xe000, v190
	global_store_dwordx2 v193, v[176:177], s[28:29]
	s_waitcnt vmcnt(31)
	v_lshlrev_b32_e32 v164, 16, v158
	v_and_b32_e32 v165, 0xffff0000, v158
	v_lshlrev_b32_e32 v166, 16, v159
	v_and_b32_e32 v167, 0xffff0000, v159
	v_pk_add_f32 v[184:185], v[184:185], v[164:165]
	v_pk_add_f32 v[186:187], v[186:187], v[166:167]
	v_lshlrev_b32_e32 v168, 16, v150
	v_and_b32_e32 v169, 0xffff0000, v150
	v_lshlrev_b32_e32 v170, 16, v151
	v_and_b32_e32 v171, 0xffff0000, v151
	v_pk_add_f32 v[184:185], v[184:185], v[168:169] neg_lo:[0,1] neg_hi:[0,1]
	v_pk_add_f32 v[186:187], v[186:187], v[170:171] neg_lo:[0,1] neg_hi:[0,1]
	v_pk_fma_f32 v[172:173], v[188:189], v[184:185], v[164:165] op_sel_hi:[0,1,1] neg_lo:[0,0,1] neg_hi:[0,0,1]
	v_pk_fma_f32 v[174:175], v[188:189], v[186:187], v[166:167] op_sel_hi:[0,1,1] neg_lo:[0,0,1] neg_hi:[0,0,1]
	v_cvt_pk_bf16_f32 v178, v172, v173
	v_cvt_pk_bf16_f32 v179, v174, v175
	global_store_dwordx2 v193, v[178:179], s[28:29] offset:2048
	s_waitcnt vmcnt(31)
	v_lshlrev_b32_e32 v164, 16, v160
	v_and_b32_e32 v165, 0xffff0000, v160
	v_lshlrev_b32_e32 v166, 16, v161
	v_and_b32_e32 v167, 0xffff0000, v161
	v_pk_add_f32 v[184:185], v[184:185], v[164:165]
	v_pk_add_f32 v[186:187], v[186:187], v[166:167]
	v_lshlrev_b32_e32 v168, 16, v152
	v_and_b32_e32 v169, 0xffff0000, v152
	v_lshlrev_b32_e32 v170, 16, v153
	v_and_b32_e32 v171, 0xffff0000, v153
	v_pk_add_f32 v[184:185], v[184:185], v[168:169] neg_lo:[0,1] neg_hi:[0,1]
	v_pk_add_f32 v[186:187], v[186:187], v[170:171] neg_lo:[0,1] neg_hi:[0,1]
	v_pk_fma_f32 v[172:173], v[188:189], v[184:185], v[164:165] op_sel_hi:[0,1,1] neg_lo:[0,0,1] neg_hi:[0,0,1]
	v_pk_fma_f32 v[174:175], v[188:189], v[186:187], v[166:167] op_sel_hi:[0,1,1] neg_lo:[0,0,1] neg_hi:[0,0,1]
	v_cvt_pk_bf16_f32 v180, v172, v173
	v_cvt_pk_bf16_f32 v181, v174, v175
	v_add_u32_e32 v194, 0xf000, v190
	global_store_dwordx2 v194, v[180:181], s[28:29]
	s_waitcnt vmcnt(31)
	v_lshlrev_b32_e32 v164, 16, v162
	v_and_b32_e32 v165, 0xffff0000, v162
	v_lshlrev_b32_e32 v166, 16, v163
	v_and_b32_e32 v167, 0xffff0000, v163
	v_pk_add_f32 v[184:185], v[184:185], v[164:165]
	v_pk_add_f32 v[186:187], v[186:187], v[166:167]
	v_lshlrev_b32_e32 v168, 16, v154
	v_and_b32_e32 v169, 0xffff0000, v154
	v_lshlrev_b32_e32 v170, 16, v155
	v_and_b32_e32 v171, 0xffff0000, v155
	v_pk_add_f32 v[184:185], v[184:185], v[168:169] neg_lo:[0,1] neg_hi:[0,1]
	v_pk_add_f32 v[186:187], v[186:187], v[170:171] neg_lo:[0,1] neg_hi:[0,1]
	v_pk_fma_f32 v[172:173], v[188:189], v[184:185], v[164:165] op_sel_hi:[0,1,1] neg_lo:[0,0,1] neg_hi:[0,0,1]
	v_pk_fma_f32 v[174:175], v[188:189], v[186:187], v[166:167] op_sel_hi:[0,1,1] neg_lo:[0,0,1] neg_hi:[0,0,1]
	v_cvt_pk_bf16_f32 v182, v172, v173
	v_cvt_pk_bf16_f32 v183, v174, v175
	global_store_dwordx2 v194, v[182:183], s[28:29] offset:2048
	s_branch .LBB0_861
; #define GAS __attribute__((address_space(1)))
; __device__ __forceinline__ unsigned pk2(float lo, float hi) { const f32x2 v = {lo, hi}; return __builtin_bit_cast(unsigned, __builtin_convertvector(v, b16x2)); }
; template <int W>
; __device__ __forceinline__ void pool_item(const bf16* U, bf16* Z, int b, int t0, int g, int lane) {
;     const size_t base = (size_t)b * SEQ * D + 256 * g + 4 * lane;
;     float s[4] = {0.f, 0.f, 0.f, 0.f};
; #pragma unroll
;     for (int j = 1; j <= W; ++j) { const int t = t0 - j; if (t >= 0) { const u32x2 v = *(const GAS u32x2*)(U + base + (size_t)t * D);
;             s[0] += bf2f(v.x & 0xffffu); s[1] += bf2f(v.x >> 16); s[2] += bf2f(v.y & 0xffffu); s[3] += bf2f(v.y >> 16); } }
; #pragma unroll 8
;     for (int i = 0; i < 32; ++i) { const int t = t0 + i;
;         const u32x2 v = *(const GAS u32x2*)(U + base + (size_t)t * D);
;         const float c0 = bf2f(v.x & 0xffffu), c1 = bf2f(v.x >> 16), c2 = bf2f(v.y & 0xffffu), c3 = bf2f(v.y >> 16);
;         s[0] += c0; s[1] += c1; s[2] += c2; s[3] += c3;
;         if (t - W >= 0) { const u32x2 o = *(const GAS u32x2*)(U + base + (size_t)(t - W) * D);
;             s[0] -= bf2f(o.x & 0xffffu); s[1] -= bf2f(o.x >> 16); s[2] -= bf2f(o.y & 0xffffu); s[3] -= bf2f(o.y >> 16); }
;         const float inv = 1.0f / (float)((t + 1) < W ? (t + 1) : W);
;         u32x2 w; w.x = pk2(s[0] * inv - c0, s[1] * inv - c1); w.y = pk2(s[2] * inv - c2, s[3] * inv - c3);
;         *(GAS u32x2*)(Z + base + (size_t)t * D) = w; }
; }
.Lpool_w2:
	v_mov_b32_e32 v188, 0.5
	v_mov_b32_e32 v189, v188
	v_add_u32_e32 v192, 0x7000, v190
	global_load_dwordx2 v[96:97], v192, s[10:11]
	global_load_dwordx2 v[98:99], v192, s[10:11] offset:2048
	v_add_u32_e32 v191, 0x8000, v190
	global_load_dwordx2 v[100:101], v191, s[10:11]
	global_load_dwordx2 v[102:103], v191, s[10:11] offset:2048
	v_add_u32_e32 v192, 0x9000, v190
	global_load_dwordx2 v[104:105], v192, s[10:11]
	global_load_dwordx2 v[106:107], v192, s[10:11] offset:2048
	v_add_u32_e32 v191, 0xa000, v190
	global_load_dwordx2 v[108:109], v191, s[10:11]
	global_load_dwordx2 v[110:111], v191, s[10:11] offset:2048
	v_add_u32_e32 v192, 0xb000, v190
	global_load_dwordx2 v[112:113], v192, s[10:11]
	global_load_dwordx2 v[114:115], v192, s[10:11] offset:2048
	v_add_u32_e32 v191, 0xc000, v190
	global_load_dwordx2 v[116:117], v191, s[10:11]
	global_load_dwordx2 v[118:119], v191, s[10:11] offset:2048
	v_add_u32_e32 v192, 0xd000, v190
	global_load_dwordx2 v[120:121], v192, s[10:11]
	global_load_dwordx2 v[122:123], v192, s[10:11] offset:2048
	v_add_u32_e32 v191, 0xe000, v190
	global_load_dwordx2 v[124:125], v191, s[10:11]
	global_load_dwordx2 v[126:127], v191, s[10:11] offset:2048
	v_add_u32_e32 v192, 0xf000, v190
	global_load_dwordx2 v[128:129], v192, s[10:11]
	global_load_dwordx2 v[130:131], v192, s[10:11] offset:2048
	v_add_u32_e32 v191, 0x10000, v190
	global_load_dwordx2 v[132:133], v191, s[10:11]
	global_load_dwordx2 v[134:135], v191, s[10:11] offset:2048
	v_add_u32_e32 v192, 0x11000, v190
	global_load_dwordx2 v[136:137], v192, s[10:11]
	global_load_dwordx2 v[138:139], v192, s[10:11] offset:2048
	v_add_u32_e32 v191, 0x12000, v190
	global_load_dwordx2 v[140:141], v191, s[10:11]
	global_load_dwordx2 v[142:143], v191, s[10:11] offset:2048
	v_add_u32_e32 v192, 0x13000, v190
	global_load_dwordx2 v[144:145], v192, s[10:11]
	global_load_dwordx2 v[146:147], v192, s[10:11] offset:2048
	v_add_u32_e32 v191, 0x14000, v190
	global_load_dwordx2 v[148:149], v191, s[10:11]
	global_load_dwordx2 v[150:151], v191, s[10:11] offset:2048
	v_add_u32_e32 v192, 0x15000, v190
	global_load_dwordx2 v[152:153], v192, s[10:11]
	global_load_dwordx2 v[154:155], v192, s[10:11] offset:2048
	v_add_u32_e32 v191, 0x16000, v190
	global_load_dwordx2 v[156:157], v191, s[10:11]
	global_load_dwordx2 v[158:159], v191, s[10:11] offset:2048
	v_add_u32_e32 v192, 0x17000, v190
	global_load_dwordx2 v[160:161], v192, s[10:11]
	global_load_dwordx2 v[162:163], v192, s[10:11] offset:2048
	s_waitcnt vmcnt(32)
	v_lshlrev_b32_e32 v164, 16, v98
	v_and_b32_e32 v165, 0xffff0000, v98
	v_lshlrev_b32_e32 v166, 16, v99
	v_and_b32_e32 v167, 0xffff0000, v99
	v_pk_add_f32 v[184:185], v[164:165], 0 op_sel_hi:[1,0]
	v_pk_add_f32 v[186:187], v[166:167], 0 op_sel_hi:[1,0]
	v_lshlrev_b32_e32 v164, 16, v96
	v_and_b32_e32 v165, 0xffff0000, v96
	v_lshlrev_b32_e32 v166, 16, v97
	v_and_b32_e32 v167, 0xffff0000, v97
	v_pk_add_f32 v[184:185], v[184:185], v[164:165]
	v_pk_add_f32 v[186:187], v[186:187], v[166:167]
	s_waitcnt vmcnt(31)
	v_lshlrev_b32_e32 v164, 16, v100
	v_and_b32_e32 v165, 0xffff0000, v100
	v_lshlrev_b32_e32 v166, 16, v101
	v_and_b32_e32 v167, 0xffff0000, v101
	v_pk_add_f32 v[184:185], v[184:185], v[164:165]
	v_pk_add_f32 v[186:187], v[186:187], v[166:167]
	v_lshlrev_b32_e32 v168, 16, v96
	v_and_b32_e32 v169, 0xffff0000, v96
	v_lshlrev_b32_e32 v170, 16, v97
	v_and_b32_e32 v171, 0xffff0000, v97
	v_pk_add_f32 v[184:185], v[184:185], v[168:169] neg_lo:[0,1] neg_hi:[0,1]
	v_pk_add_f32 v[186:187], v[186:187], v[170:171] neg_lo:[0,1] neg_hi:[0,1]
	v_pk_fma_f32 v[172:173], v[188:189], v[184:185], v[164:165] op_sel_hi:[0,1,1] neg_lo:[0,0,1] neg_hi:[0,0,1]
	v_pk_fma_f32 v[174:175], v[188:189], v[186:187], v[166:167] op_sel_hi:[0,1,1] neg_lo:[0,0,1] neg_hi:[0,0,1]
	v_cvt_pk_bf16_f32 v176, v172, v173
	v_cvt_pk_bf16_f32 v177, v174, v175
	global_store_dwordx2 v190, v[176:177], s[28:29]
	s_waitcnt vmcnt(31)
	v_lshlrev_b32_e32 v164, 16, v102
	v_and_b32_e32 v165, 0xffff0000, v102
	v_lshlrev_b32_e32 v166, 16, v103
	v_and_b32_e32 v167, 0xffff0000, v103
	v_pk_add_f32 v[184:185], v[184:185], v[164:165]
	v_pk_add_f32 v[186:187], v[186:187], v[166:167]
	v_lshlrev_b32_e32 v168, 16, v98
	v_and_b32_e32 v169, 0xffff0000, v98
	v_lshlrev_b32_e32 v170, 16, v99
	v_and_b32_e32 v171, 0xffff0000, v99
	v_pk_add_f32 v[184:185], v[184:185], v[168:169] neg_lo:[0,1] neg_hi:[0,1]
	v_pk_add_f32 v[186:187], v[186:187], v[170:171] neg_lo:[0,1] neg_hi:[0,1]
	v_pk_fma_f32 v[172:173], v[188:189], v[184:185], v[164:165] op_sel_hi:[0,1,1] neg_lo:[0,0,1] neg_hi:[0,0,1]
	v_pk_fma_f32 v[174:175], v[188:189], v[186:187], v[166:167] op_sel_hi:[0,1,1] neg_lo:[0,0,1] neg_hi:[0,0,1]
	v_cvt_pk_bf16_f32 v178, v172, v173
	v_cvt_pk_bf16_f32 v179, v174, v175
	global_store_dwordx2 v190, v[178:179], s[28:29] offset:2048
	s_waitcnt vmcnt(31)
	v_lshlrev_b32_e32 v164, 16, v104
	v_and_b32_e32 v165, 0xffff0000, v104
	v_lshlrev_b32_e32 v166, 16, v105
	v_and_b32_e32 v167, 0xffff0000, v105
	v_pk_add_f32 v[184:185], v[184:185], v[164:165]
	v_pk_add_f32 v[186:187], v[186:187], v[166:167]
	v_lshlrev_b32_e32 v168, 16, v100
	v_and_b32_e32 v169, 0xffff0000, v100
	v_lshlrev_b32_e32 v170, 16, v101
	v_and_b32_e32 v171, 0xffff0000, v101
	v_pk_add_f32 v[184:185], v[184:185], v[168:169] neg_lo:[0,1] neg_hi:[0,1]
	v_pk_add_f32 v[186:187], v[186:187], v[170:171] neg_lo:[0,1] neg_hi:[0,1]
	v_pk_fma_f32 v[172:173], v[188:189], v[184:185], v[164:165] op_sel_hi:[0,1,1] neg_lo:[0,0,1] neg_hi:[0,0,1]
	v_pk_fma_f32 v[174:175], v[188:189], v[186:187], v[166:167] op_sel_hi:[0,1,1] neg_lo:[0,0,1] neg_hi:[0,0,1]
	v_cvt_pk_bf16_f32 v180, v172, v173
	v_cvt_pk_bf16_f32 v181, v174, v175
	v_add_u32_e32 v194, 0x1000, v190
	global_store_dwordx2 v194, v[180:181], s[28:29]
	s_waitcnt vmcnt(31)
; #define GAS __attribute__((address_space(1)))
; __device__ __forceinline__ unsigned pk2(float lo, float hi) { const f32x2 v = {lo, hi}; return __builtin_bit_cast(unsigned, __builtin_convertvector(v, b16x2)); }
; template <int W>
; __device__ __forceinline__ void pool_item(const bf16* U, bf16* Z, int b, int t0, int g, int lane) {
;     ...
;     for (int i = 0; i < 32; ++i) { const int t = t0 + i;
;         const u32x2 v = *(const GAS u32x2*)(U + base + (size_t)t * D);
;         const float c0 = bf2f(v.x & 0xffffu), c1 = bf2f(v.x >> 16), c2 = bf2f(v.y & 0xffffu), c3 = bf2f(v.y >> 16);
;         s[0] += c0; s[1] += c1; s[2] += c2; s[3] += c3;
;         if (t - W >= 0) { const u32x2 o = *(const GAS u32x2*)(U + base + (size_t)(t - W) * D);
;             s[0] -= bf2f(o.x & 0xffffu); s[1] -= bf2f(o.x >> 16); s[2] -= bf2f(o.y & 0xffffu); s[3] -= bf2f(o.y >> 16); }
;         const float inv = 1.0f / (float)((t + 1) < W ? (t + 1) : W);
;         u32x2 w; w.x = pk2(s[0] * inv - c0, s[1] * inv - c1); w.y = pk2(s[2] * inv - c2, s[3] * inv - c3);
;         *(GAS u32x2*)(Z + base + (size_t)t * D) = w; }
; }
	v_lshlrev_b32_e32 v164, 16, v106
	v_and_b32_e32 v165, 0xffff0000, v106
	v_lshlrev_b32_e32 v166, 16, v107
	v_and_b32_e32 v167, 0xffff0000, v107
	v_pk_add_f32 v[184:185], v[184:185], v[164:165]
	v_pk_add_f32 v[186:187], v[186:187], v[166:167]
	v_lshlrev_b32_e32 v168, 16, v102
	v_and_b32_e32 v169, 0xffff0000, v102
	v_lshlrev_b32_e32 v170, 16, v103
	v_and_b32_e32 v171, 0xffff0000, v103
	v_pk_add_f32 v[184:185], v[184:185], v[168:169] neg_lo:[0,1] neg_hi:[0,1]
	v_pk_add_f32 v[186:187], v[186:187], v[170:171] neg_lo:[0,1] neg_hi:[0,1]
	v_pk_fma_f32 v[172:173], v[188:189], v[184:185], v[164:165] op_sel_hi:[0,1,1] neg_lo:[0,0,1] neg_hi:[0,0,1]
	v_pk_fma_f32 v[174:175], v[188:189], v[186:187], v[166:167] op_sel_hi:[0,1,1] neg_lo:[0,0,1] neg_hi:[0,0,1]
	v_cvt_pk_bf16_f32 v182, v172, v173
	v_cvt_pk_bf16_f32 v183, v174, v175
	global_store_dwordx2 v194, v[182:183], s[28:29] offset:2048
	s_waitcnt vmcnt(31)
	v_lshlrev_b32_e32 v164, 16, v108
	v_and_b32_e32 v165, 0xffff0000, v108
	v_lshlrev_b32_e32 v166, 16, v109
	v_and_b32_e32 v167, 0xffff0000, v109
	v_pk_add_f32 v[184:185], v[184:185], v[164:165]
	v_pk_add_f32 v[186:187], v[186:187], v[166:167]
	v_lshlrev_b32_e32 v168, 16, v104
	v_and_b32_e32 v169, 0xffff0000, v104
	v_lshlrev_b32_e32 v170, 16, v105
	v_and_b32_e32 v171, 0xffff0000, v105
	v_pk_add_f32 v[184:185], v[184:185], v[168:169] neg_lo:[0,1] neg_hi:[0,1]
	v_pk_add_f32 v[186:187], v[186:187], v[170:171] neg_lo:[0,1] neg_hi:[0,1]
	v_pk_fma_f32 v[172:173], v[188:189], v[184:185], v[164:165] op_sel_hi:[0,1,1] neg_lo:[0,0,1] neg_hi:[0,0,1]
	v_pk_fma_f32 v[174:175], v[188:189], v[186:187], v[166:167] op_sel_hi:[0,1,1] neg_lo:[0,0,1] neg_hi:[0,0,1]
	v_cvt_pk_bf16_f32 v176, v172, v173
	v_cvt_pk_bf16_f32 v177, v174, v175
	v_add_u32_e32 v193, 0x2000, v190
	global_store_dwordx2 v193, v[176:177], s[28:29]
	s_waitcnt vmcnt(31)
	v_lshlrev_b32_e32 v164, 16, v110
	v_and_b32_e32 v165, 0xffff0000, v110
	v_lshlrev_b32_e32 v166, 16, v111
	v_and_b32_e32 v167, 0xffff0000, v111
	v_pk_add_f32 v[184:185], v[184:185], v[164:165]
	v_pk_add_f32 v[186:187], v[186:187], v[166:167]
	v_lshlrev_b32_e32 v168, 16, v106
	v_and_b32_e32 v169, 0xffff0000, v106
	v_lshlrev_b32_e32 v170, 16, v107
	v_and_b32_e32 v171, 0xffff0000, v107
	v_pk_add_f32 v[184:185], v[184:185], v[168:169] neg_lo:[0,1] neg_hi:[0,1]
	v_pk_add_f32 v[186:187], v[186:187], v[170:171] neg_lo:[0,1] neg_hi:[0,1]
	v_pk_fma_f32 v[172:173], v[188:189], v[184:185], v[164:165] op_sel_hi:[0,1,1] neg_lo:[0,0,1] neg_hi:[0,0,1]
	v_pk_fma_f32 v[174:175], v[188:189], v[186:187], v[166:167] op_sel_hi:[0,1,1] neg_lo:[0,0,1] neg_hi:[0,0,1]
	v_cvt_pk_bf16_f32 v178, v172, v173
	v_cvt_pk_bf16_f32 v179, v174, v175
	global_store_dwordx2 v193, v[178:179], s[28:29] offset:2048
	s_waitcnt vmcnt(31)
	v_lshlrev_b32_e32 v164, 16, v112
	v_and_b32_e32 v165, 0xffff0000, v112
	v_lshlrev_b32_e32 v166, 16, v113
	v_and_b32_e32 v167, 0xffff0000, v113
	v_pk_add_f32 v[184:185], v[184:185], v[164:165]
	v_pk_add_f32 v[186:187], v[186:187], v[166:167]
	v_lshlrev_b32_e32 v168, 16, v108
	v_and_b32_e32 v169, 0xffff0000, v108
	v_lshlrev_b32_e32 v170, 16, v109
	v_and_b32_e32 v171, 0xffff0000, v109
	v_pk_add_f32 v[184:185], v[184:185], v[168:169] neg_lo:[0,1] neg_hi:[0,1]
	v_pk_add_f32 v[186:187], v[186:187], v[170:171] neg_lo:[0,1] neg_hi:[0,1]
	v_pk_fma_f32 v[172:173], v[188:189], v[184:185], v[164:165] op_sel_hi:[0,1,1] neg_lo:[0,0,1] neg_hi:[0,0,1]
	v_pk_fma_f32 v[174:175], v[188:189], v[186:187], v[166:167] op_sel_hi:[0,1,1] neg_lo:[0,0,1] neg_hi:[0,0,1]
	v_cvt_pk_bf16_f32 v180, v172, v173
	v_cvt_pk_bf16_f32 v181, v174, v175
	v_add_u32_e32 v194, 0x3000, v190
	global_store_dwordx2 v194, v[180:181], s[28:29]
	s_waitcnt vmcnt(31)
	v_lshlrev_b32_e32 v164, 16, v114
	v_and_b32_e32 v165, 0xffff0000, v114
	v_lshlrev_b32_e32 v166, 16, v115
	v_and_b32_e32 v167, 0xffff0000, v115
	v_pk_add_f32 v[184:185], v[184:185], v[164:165]
	v_pk_add_f32 v[186:187], v[186:187], v[166:167]
	v_lshlrev_b32_e32 v168, 16, v110
	v_and_b32_e32 v169, 0xffff0000, v110
	v_lshlrev_b32_e32 v170, 16, v111
	v_and_b32_e32 v171, 0xffff0000, v111
	v_pk_add_f32 v[184:185], v[184:185], v[168:169] neg_lo:[0,1] neg_hi:[0,1]
	v_pk_add_f32 v[186:187], v[186:187], v[170:171] neg_lo:[0,1] neg_hi:[0,1]
	v_pk_fma_f32 v[172:173], v[188:189], v[184:185], v[164:165] op_sel_hi:[0,1,1] neg_lo:[0,0,1] neg_hi:[0,0,1]
	v_pk_fma_f32 v[174:175], v[188:189], v[186:187], v[166:167] op_sel_hi:[0,1,1] neg_lo:[0,0,1] neg_hi:[0,0,1]
	v_cvt_pk_bf16_f32 v182, v172, v173
	v_cvt_pk_bf16_f32 v183, v174, v175
	global_store_dwordx2 v194, v[182:183], s[28:29] offset:2048
	s_waitcnt vmcnt(31)
	v_lshlrev_b32_e32 v164, 16, v116
	v_and_b32_e32 v165, 0xffff0000, v116
	v_lshlrev_b32_e32 v166, 16, v117
	v_and_b32_e32 v167, 0xffff0000, v117
	v_pk_add_f32 v[184:185], v[184:185], v[164:165]
	v_pk_add_f32 v[186:187], v[186:187], v[166:167]
	v_lshlrev_b32_e32 v168, 16, v112
	v_and_b32_e32 v169, 0xffff0000, v112
	v_lshlrev_b32_e32 v170, 16, v113
	v_and_b32_e32 v171, 0xffff0000, v113
	v_pk_add_f32 v[184:185], v[184:185], v[168:169] neg_lo:[0,1] neg_hi:[0,1]
	v_pk_add_f32 v[186:187], v[186:187], v[170:171] neg_lo:[0,1] neg_hi:[0,1]
	v_pk_fma_f32 v[172:173], v[188:189], v[184:185], v[164:165] op_sel_hi:[0,1,1] neg_lo:[0,0,1] neg_hi:[0,0,1]
	v_pk_fma_f32 v[174:175], v[188:189], v[186:187], v[166:167] op_sel_hi:[0,1,1] neg_lo:[0,0,1] neg_hi:[0,0,1]
	v_cvt_pk_bf16_f32 v176, v172, v173
	v_cvt_pk_bf16_f32 v177, v174, v175
	v_add_u32_e32 v193, 0x4000, v190
	global_store_dwordx2 v193, v[176:177], s[28:29]
	s_waitcnt vmcnt(31)
; #define GAS __attribute__((address_space(1)))
; __device__ __forceinline__ unsigned pk2(float lo, float hi) { const f32x2 v = {lo, hi}; return __builtin_bit_cast(unsigned, __builtin_convertvector(v, b16x2)); }
; template <int W>
; __device__ __forceinline__ void pool_item(const bf16* U, bf16* Z, int b, int t0, int g, int lane) {
;     ...
;     for (int i = 0; i < 32; ++i) { const int t = t0 + i;
;         const u32x2 v = *(const GAS u32x2*)(U + base + (size_t)t * D);
;         const float c0 = bf2f(v.x & 0xffffu), c1 = bf2f(v.x >> 16), c2 = bf2f(v.y & 0xffffu), c3 = bf2f(v.y >> 16);
;         s[0] += c0; s[1] += c1; s[2] += c2; s[3] += c3;
;         if (t - W >= 0) { const u32x2 o = *(const GAS u32x2*)(U + base + (size_t)(t - W) * D);
;             s[0] -= bf2f(o.x & 0xffffu); s[1] -= bf2f(o.x >> 16); s[2] -= bf2f(o.y & 0xffffu); s[3] -= bf2f(o.y >> 16); }
;         const float inv = 1.0f / (float)((t + 1) < W ? (t + 1) : W);
;         u32x2 w; w.x = pk2(s[0] * inv - c0, s[1] * inv - c1); w.y = pk2(s[2] * inv - c2, s[3] * inv - c3);
;         *(GAS u32x2*)(Z + base + (size_t)t * D) = w; }
; }
	v_lshlrev_b32_e32 v164, 16, v118
	v_and_b32_e32 v165, 0xffff0000, v118
	v_lshlrev_b32_e32 v166, 16, v119
	v_and_b32_e32 v167, 0xffff0000, v119
	v_pk_add_f32 v[184:185], v[184:185], v[164:165]
	v_pk_add_f32 v[186:187], v[186:187], v[166:167]
	v_lshlrev_b32_e32 v168, 16, v114
	v_and_b32_e32 v169, 0xffff0000, v114
	v_lshlrev_b32_e32 v170, 16, v115
	v_and_b32_e32 v171, 0xffff0000, v115
	v_pk_add_f32 v[184:185], v[184:185], v[168:169] neg_lo:[0,1] neg_hi:[0,1]
	v_pk_add_f32 v[186:187], v[186:187], v[170:171] neg_lo:[0,1] neg_hi:[0,1]
	v_pk_fma_f32 v[172:173], v[188:189], v[184:185], v[164:165] op_sel_hi:[0,1,1] neg_lo:[0,0,1] neg_hi:[0,0,1]
	v_pk_fma_f32 v[174:175], v[188:189], v[186:187], v[166:167] op_sel_hi:[0,1,1] neg_lo:[0,0,1] neg_hi:[0,0,1]
	v_cvt_pk_bf16_f32 v178, v172, v173
	v_cvt_pk_bf16_f32 v179, v174, v175
	global_store_dwordx2 v193, v[178:179], s[28:29] offset:2048
	s_waitcnt vmcnt(31)
	v_lshlrev_b32_e32 v164, 16, v120
	v_and_b32_e32 v165, 0xffff0000, v120
	v_lshlrev_b32_e32 v166, 16, v121
	v_and_b32_e32 v167, 0xffff0000, v121
	v_pk_add_f32 v[184:185], v[184:185], v[164:165]
	v_pk_add_f32 v[186:187], v[186:187], v[166:167]
	v_lshlrev_b32_e32 v168, 16, v116
	v_and_b32_e32 v169, 0xffff0000, v116
	v_lshlrev_b32_e32 v170, 16, v117
	v_and_b32_e32 v171, 0xffff0000, v117
	v_pk_add_f32 v[184:185], v[184:185], v[168:169] neg_lo:[0,1] neg_hi:[0,1]
	v_pk_add_f32 v[186:187], v[186:187], v[170:171] neg_lo:[0,1] neg_hi:[0,1]
	v_pk_fma_f32 v[172:173], v[188:189], v[184:185], v[164:165] op_sel_hi:[0,1,1] neg_lo:[0,0,1] neg_hi:[0,0,1]
	v_pk_fma_f32 v[174:175], v[188:189], v[186:187], v[166:167] op_sel_hi:[0,1,1] neg_lo:[0,0,1] neg_hi:[0,0,1]
	v_cvt_pk_bf16_f32 v180, v172, v173
	v_cvt_pk_bf16_f32 v181, v174, v175
	v_add_u32_e32 v194, 0x5000, v190
	global_store_dwordx2 v194, v[180:181], s[28:29]
	s_waitcnt vmcnt(31)
	v_lshlrev_b32_e32 v164, 16, v122
	v_and_b32_e32 v165, 0xffff0000, v122
	v_lshlrev_b32_e32 v166, 16, v123
	v_and_b32_e32 v167, 0xffff0000, v123
	v_pk_add_f32 v[184:185], v[184:185], v[164:165]
	v_pk_add_f32 v[186:187], v[186:187], v[166:167]
	v_lshlrev_b32_e32 v168, 16, v118
	v_and_b32_e32 v169, 0xffff0000, v118
	v_lshlrev_b32_e32 v170, 16, v119
	v_and_b32_e32 v171, 0xffff0000, v119
	v_pk_add_f32 v[184:185], v[184:185], v[168:169] neg_lo:[0,1] neg_hi:[0,1]
	v_pk_add_f32 v[186:187], v[186:187], v[170:171] neg_lo:[0,1] neg_hi:[0,1]
	v_pk_fma_f32 v[172:173], v[188:189], v[184:185], v[164:165] op_sel_hi:[0,1,1] neg_lo:[0,0,1] neg_hi:[0,0,1]
	v_pk_fma_f32 v[174:175], v[188:189], v[186:187], v[166:167] op_sel_hi:[0,1,1] neg_lo:[0,0,1] neg_hi:[0,0,1]
	v_cvt_pk_bf16_f32 v182, v172, v173
	v_cvt_pk_bf16_f32 v183, v174, v175
	global_store_dwordx2 v194, v[182:183], s[28:29] offset:2048
	s_waitcnt vmcnt(31)
	v_lshlrev_b32_e32 v164, 16, v124
	v_and_b32_e32 v165, 0xffff0000, v124
	v_lshlrev_b32_e32 v166, 16, v125
	v_and_b32_e32 v167, 0xffff0000, v125
	v_pk_add_f32 v[184:185], v[184:185], v[164:165]
	v_pk_add_f32 v[186:187], v[186:187], v[166:167]
	v_lshlrev_b32_e32 v168, 16, v120
	v_and_b32_e32 v169, 0xffff0000, v120
	v_lshlrev_b32_e32 v170, 16, v121
	v_and_b32_e32 v171, 0xffff0000, v121
	v_pk_add_f32 v[184:185], v[184:185], v[168:169] neg_lo:[0,1] neg_hi:[0,1]
	v_pk_add_f32 v[186:187], v[186:187], v[170:171] neg_lo:[0,1] neg_hi:[0,1]
	v_pk_fma_f32 v[172:173], v[188:189], v[184:185], v[164:165] op_sel_hi:[0,1,1] neg_lo:[0,0,1] neg_hi:[0,0,1]
	v_pk_fma_f32 v[174:175], v[188:189], v[186:187], v[166:167] op_sel_hi:[0,1,1] neg_lo:[0,0,1] neg_hi:[0,0,1]
	v_cvt_pk_bf16_f32 v176, v172, v173
	v_cvt_pk_bf16_f32 v177, v174, v175
	v_add_u32_e32 v193, 0x6000, v190
	global_store_dwordx2 v193, v[176:177], s[28:29]
	s_waitcnt vmcnt(31)
	v_lshlrev_b32_e32 v164, 16, v126
	v_and_b32_e32 v165, 0xffff0000, v126
	v_lshlrev_b32_e32 v166, 16, v127
	v_and_b32_e32 v167, 0xffff0000, v127
	v_pk_add_f32 v[184:185], v[184:185], v[164:165]
	v_pk_add_f32 v[186:187], v[186:187], v[166:167]
	v_lshlrev_b32_e32 v168, 16, v122
	v_and_b32_e32 v169, 0xffff0000, v122
	v_lshlrev_b32_e32 v170, 16, v123
	v_and_b32_e32 v171, 0xffff0000, v123
	v_pk_add_f32 v[184:185], v[184:185], v[168:169] neg_lo:[0,1] neg_hi:[0,1]
	v_pk_add_f32 v[186:187], v[186:187], v[170:171] neg_lo:[0,1] neg_hi:[0,1]
	v_pk_fma_f32 v[172:173], v[188:189], v[184:185], v[164:165] op_sel_hi:[0,1,1] neg_lo:[0,0,1] neg_hi:[0,0,1]
	v_pk_fma_f32 v[174:175], v[188:189], v[186:187], v[166:167] op_sel_hi:[0,1,1] neg_lo:[0,0,1] neg_hi:[0,0,1]
	v_cvt_pk_bf16_f32 v178, v172, v173
	v_cvt_pk_bf16_f32 v179, v174, v175
	global_store_dwordx2 v193, v[178:179], s[28:29] offset:2048
	s_waitcnt vmcnt(31)
	v_lshlrev_b32_e32 v164, 16, v128
	v_and_b32_e32 v165, 0xffff0000, v128
	v_lshlrev_b32_e32 v166, 16, v129
	v_and_b32_e32 v167, 0xffff0000, v129
	v_pk_add_f32 v[184:185], v[184:185], v[164:165]
	v_pk_add_f32 v[186:187], v[186:187], v[166:167]
	v_lshlrev_b32_e32 v168, 16, v124
	v_and_b32_e32 v169, 0xffff0000, v124
	v_lshlrev_b32_e32 v170, 16, v125
	v_and_b32_e32 v171, 0xffff0000, v125
	v_pk_add_f32 v[184:185], v[184:185], v[168:169] neg_lo:[0,1] neg_hi:[0,1]
	v_pk_add_f32 v[186:187], v[186:187], v[170:171] neg_lo:[0,1] neg_hi:[0,1]
	v_pk_fma_f32 v[172:173], v[188:189], v[184:185], v[164:165] op_sel_hi:[0,1,1] neg_lo:[0,0,1] neg_hi:[0,0,1]
	v_pk_fma_f32 v[174:175], v[188:189], v[186:187], v[166:167] op_sel_hi:[0,1,1] neg_lo:[0,0,1] neg_hi:[0,0,1]
	v_cvt_pk_bf16_f32 v180, v172, v173
	v_cvt_pk_bf16_f32 v181, v174, v175
	v_add_u32_e32 v194, 0x7000, v190
	global_store_dwordx2 v194, v[180:181], s[28:29]
	s_waitcnt vmcnt(31)
; #define GAS __attribute__((address_space(1)))
; __device__ __forceinline__ unsigned pk2(float lo, float hi) { const f32x2 v = {lo, hi}; return __builtin_bit_cast(unsigned, __builtin_convertvector(v, b16x2)); }
; template <int W>
; __device__ __forceinline__ void pool_item(const bf16* U, bf16* Z, int b, int t0, int g, int lane) {
;     ...
;     for (int i = 0; i < 32; ++i) { const int t = t0 + i;
;         const u32x2 v = *(const GAS u32x2*)(U + base + (size_t)t * D);
;         const float c0 = bf2f(v.x & 0xffffu), c1 = bf2f(v.x >> 16), c2 = bf2f(v.y & 0xffffu), c3 = bf2f(v.y >> 16);
;         s[0] += c0; s[1] += c1; s[2] += c2; s[3] += c3;
;         if (t - W >= 0) { const u32x2 o = *(const GAS u32x2*)(U + base + (size_t)(t - W) * D);
;             s[0] -= bf2f(o.x & 0xffffu); s[1] -= bf2f(o.x >> 16); s[2] -= bf2f(o.y & 0xffffu); s[3] -= bf2f(o.y >> 16); }
;         const float inv = 1.0f / (float)((t + 1) < W ? (t + 1) : W);
;         u32x2 w; w.x = pk2(s[0] * inv - c0, s[1] * inv - c1); w.y = pk2(s[2] * inv - c2, s[3] * inv - c3);
;         *(GAS u32x2*)(Z + base + (size_t)t * D) = w; }
; }
	v_lshlrev_b32_e32 v164, 16, v130
	v_and_b32_e32 v165, 0xffff0000, v130
	v_lshlrev_b32_e32 v166, 16, v131
	v_and_b32_e32 v167, 0xffff0000, v131
	v_pk_add_f32 v[184:185], v[184:185], v[164:165]
	v_pk_add_f32 v[186:187], v[186:187], v[166:167]
	v_lshlrev_b32_e32 v168, 16, v126
	v_and_b32_e32 v169, 0xffff0000, v126
	v_lshlrev_b32_e32 v170, 16, v127
	v_and_b32_e32 v171, 0xffff0000, v127
	v_pk_add_f32 v[184:185], v[184:185], v[168:169] neg_lo:[0,1] neg_hi:[0,1]
	v_pk_add_f32 v[186:187], v[186:187], v[170:171] neg_lo:[0,1] neg_hi:[0,1]
	v_pk_fma_f32 v[172:173], v[188:189], v[184:185], v[164:165] op_sel_hi:[0,1,1] neg_lo:[0,0,1] neg_hi:[0,0,1]
	v_pk_fma_f32 v[174:175], v[188:189], v[186:187], v[166:167] op_sel_hi:[0,1,1] neg_lo:[0,0,1] neg_hi:[0,0,1]
	v_cvt_pk_bf16_f32 v182, v172, v173
	v_cvt_pk_bf16_f32 v183, v174, v175
	global_store_dwordx2 v194, v[182:183], s[28:29] offset:2048
	s_waitcnt vmcnt(31)
	v_lshlrev_b32_e32 v164, 16, v132
	v_and_b32_e32 v165, 0xffff0000, v132
	v_lshlrev_b32_e32 v166, 16, v133
	v_and_b32_e32 v167, 0xffff0000, v133
	v_pk_add_f32 v[184:185], v[184:185], v[164:165]
	v_pk_add_f32 v[186:187], v[186:187], v[166:167]
	v_lshlrev_b32_e32 v168, 16, v128
	v_and_b32_e32 v169, 0xffff0000, v128
	v_lshlrev_b32_e32 v170, 16, v129
	v_and_b32_e32 v171, 0xffff0000, v129
	v_pk_add_f32 v[184:185], v[184:185], v[168:169] neg_lo:[0,1] neg_hi:[0,1]
	v_pk_add_f32 v[186:187], v[186:187], v[170:171] neg_lo:[0,1] neg_hi:[0,1]
	v_pk_fma_f32 v[172:173], v[188:189], v[184:185], v[164:165] op_sel_hi:[0,1,1] neg_lo:[0,0,1] neg_hi:[0,0,1]
	v_pk_fma_f32 v[174:175], v[188:189], v[186:187], v[166:167] op_sel_hi:[0,1,1] neg_lo:[0,0,1] neg_hi:[0,0,1]
	v_cvt_pk_bf16_f32 v176, v172, v173
	v_cvt_pk_bf16_f32 v177, v174, v175
	v_add_u32_e32 v193, 0x8000, v190
	global_store_dwordx2 v193, v[176:177], s[28:29]
	s_waitcnt vmcnt(31)
	v_lshlrev_b32_e32 v164, 16, v134
	v_and_b32_e32 v165, 0xffff0000, v134
	v_lshlrev_b32_e32 v166, 16, v135
	v_and_b32_e32 v167, 0xffff0000, v135
	v_pk_add_f32 v[184:185], v[184:185], v[164:165]
	v_pk_add_f32 v[186:187], v[186:187], v[166:167]
	v_lshlrev_b32_e32 v168, 16, v130
	v_and_b32_e32 v169, 0xffff0000, v130
	v_lshlrev_b32_e32 v170, 16, v131
	v_and_b32_e32 v171, 0xffff0000, v131
	v_pk_add_f32 v[184:185], v[184:185], v[168:169] neg_lo:[0,1] neg_hi:[0,1]
	v_pk_add_f32 v[186:187], v[186:187], v[170:171] neg_lo:[0,1] neg_hi:[0,1]
	v_pk_fma_f32 v[172:173], v[188:189], v[184:185], v[164:165] op_sel_hi:[0,1,1] neg_lo:[0,0,1] neg_hi:[0,0,1]
	v_pk_fma_f32 v[174:175], v[188:189], v[186:187], v[166:167] op_sel_hi:[0,1,1] neg_lo:[0,0,1] neg_hi:[0,0,1]
	v_cvt_pk_bf16_f32 v178, v172, v173
	v_cvt_pk_bf16_f32 v179, v174, v175
	global_store_dwordx2 v193, v[178:179], s[28:29] offset:2048
	s_waitcnt vmcnt(31)
	v_lshlrev_b32_e32 v164, 16, v136
	v_and_b32_e32 v165, 0xffff0000, v136
	v_lshlrev_b32_e32 v166, 16, v137
	v_and_b32_e32 v167, 0xffff0000, v137
	v_pk_add_f32 v[184:185], v[184:185], v[164:165]
	v_pk_add_f32 v[186:187], v[186:187], v[166:167]
	v_lshlrev_b32_e32 v168, 16, v132
	v_and_b32_e32 v169, 0xffff0000, v132
	v_lshlrev_b32_e32 v170, 16, v133
	v_and_b32_e32 v171, 0xffff0000, v133
	v_pk_add_f32 v[184:185], v[184:185], v[168:169] neg_lo:[0,1] neg_hi:[0,1]
	v_pk_add_f32 v[186:187], v[186:187], v[170:171] neg_lo:[0,1] neg_hi:[0,1]
	v_pk_fma_f32 v[172:173], v[188:189], v[184:185], v[164:165] op_sel_hi:[0,1,1] neg_lo:[0,0,1] neg_hi:[0,0,1]
	v_pk_fma_f32 v[174:175], v[188:189], v[186:187], v[166:167] op_sel_hi:[0,1,1] neg_lo:[0,0,1] neg_hi:[0,0,1]
	v_cvt_pk_bf16_f32 v180, v172, v173
	v_cvt_pk_bf16_f32 v181, v174, v175
	v_add_u32_e32 v194, 0x9000, v190
	global_store_dwordx2 v194, v[180:181], s[28:29]
	s_waitcnt vmcnt(31)
	v_lshlrev_b32_e32 v164, 16, v138
	v_and_b32_e32 v165, 0xffff0000, v138
	v_lshlrev_b32_e32 v166, 16, v139
	v_and_b32_e32 v167, 0xffff0000, v139
	v_pk_add_f32 v[184:185], v[184:185], v[164:165]
	v_pk_add_f32 v[186:187], v[186:187], v[166:167]
	v_lshlrev_b32_e32 v168, 16, v134
	v_and_b32_e32 v169, 0xffff0000, v134
	v_lshlrev_b32_e32 v170, 16, v135
	v_and_b32_e32 v171, 0xffff0000, v135
	v_pk_add_f32 v[184:185], v[184:185], v[168:169] neg_lo:[0,1] neg_hi:[0,1]
	v_pk_add_f32 v[186:187], v[186:187], v[170:171] neg_lo:[0,1] neg_hi:[0,1]
	v_pk_fma_f32 v[172:173], v[188:189], v[184:185], v[164:165] op_sel_hi:[0,1,1] neg_lo:[0,0,1] neg_hi:[0,0,1]
	v_pk_fma_f32 v[174:175], v[188:189], v[186:187], v[166:167] op_sel_hi:[0,1,1] neg_lo:[0,0,1] neg_hi:[0,0,1]
	v_cvt_pk_bf16_f32 v182, v172, v173
	v_cvt_pk_bf16_f32 v183, v174, v175
	global_store_dwordx2 v194, v[182:183], s[28:29] offset:2048
	s_waitcnt vmcnt(31)
	v_lshlrev_b32_e32 v164, 16, v140
	v_and_b32_e32 v165, 0xffff0000, v140
	v_lshlrev_b32_e32 v166, 16, v141
	v_and_b32_e32 v167, 0xffff0000, v141
	v_pk_add_f32 v[184:185], v[184:185], v[164:165]
	v_pk_add_f32 v[186:187], v[186:187], v[166:167]
	v_lshlrev_b32_e32 v168, 16, v136
	v_and_b32_e32 v169, 0xffff0000, v136
	v_lshlrev_b32_e32 v170, 16, v137
	v_and_b32_e32 v171, 0xffff0000, v137
	v_pk_add_f32 v[184:185], v[184:185], v[168:169] neg_lo:[0,1] neg_hi:[0,1]
	v_pk_add_f32 v[186:187], v[186:187], v[170:171] neg_lo:[0,1] neg_hi:[0,1]
	v_pk_fma_f32 v[172:173], v[188:189], v[184:185], v[164:165] op_sel_hi:[0,1,1] neg_lo:[0,0,1] neg_hi:[0,0,1]
	v_pk_fma_f32 v[174:175], v[188:189], v[186:187], v[166:167] op_sel_hi:[0,1,1] neg_lo:[0,0,1] neg_hi:[0,0,1]
	v_cvt_pk_bf16_f32 v176, v172, v173
	v_cvt_pk_bf16_f32 v177, v174, v175
	v_add_u32_e32 v193, 0xa000, v190
	global_store_dwordx2 v193, v[176:177], s[28:29]
	s_waitcnt vmcnt(31)
; #define GAS __attribute__((address_space(1)))
; __device__ __forceinline__ unsigned pk2(float lo, float hi) { const f32x2 v = {lo, hi}; return __builtin_bit_cast(unsigned, __builtin_convertvector(v, b16x2)); }
; template <int W>
; __device__ __forceinline__ void pool_item(const bf16* U, bf16* Z, int b, int t0, int g, int lane) {
;     ...
;     for (int i = 0; i < 32; ++i) { const int t = t0 + i;
;         const u32x2 v = *(const GAS u32x2*)(U + base + (size_t)t * D);
;         const float c0 = bf2f(v.x & 0xffffu), c1 = bf2f(v.x >> 16), c2 = bf2f(v.y & 0xffffu), c3 = bf2f(v.y >> 16);
;         s[0] += c0; s[1] += c1; s[2] += c2; s[3] += c3;
;         if (t - W >= 0) { const u32x2 o = *(const GAS u32x2*)(U + base + (size_t)(t - W) * D);
;             s[0] -= bf2f(o.x & 0xffffu); s[1] -= bf2f(o.x >> 16); s[2] -= bf2f(o.y & 0xffffu); s[3] -= bf2f(o.y >> 16); }
;         const float inv = 1.0f / (float)((t + 1) < W ? (t + 1) : W);
;         u32x2 w; w.x = pk2(s[0] * inv - c0, s[1] * inv - c1); w.y = pk2(s[2] * inv - c2, s[3] * inv - c3);
;         *(GAS u32x2*)(Z + base + (size_t)t * D) = w; }
; }
	v_lshlrev_b32_e32 v164, 16, v142
	v_and_b32_e32 v165, 0xffff0000, v142
	v_lshlrev_b32_e32 v166, 16, v143
	v_and_b32_e32 v167, 0xffff0000, v143
	v_pk_add_f32 v[184:185], v[184:185], v[164:165]
	v_pk_add_f32 v[186:187], v[186:187], v[166:167]
	v_lshlrev_b32_e32 v168, 16, v138
	v_and_b32_e32 v169, 0xffff0000, v138
	v_lshlrev_b32_e32 v170, 16, v139
	v_and_b32_e32 v171, 0xffff0000, v139
	v_pk_add_f32 v[184:185], v[184:185], v[168:169] neg_lo:[0,1] neg_hi:[0,1]
	v_pk_add_f32 v[186:187], v[186:187], v[170:171] neg_lo:[0,1] neg_hi:[0,1]
	v_pk_fma_f32 v[172:173], v[188:189], v[184:185], v[164:165] op_sel_hi:[0,1,1] neg_lo:[0,0,1] neg_hi:[0,0,1]
	v_pk_fma_f32 v[174:175], v[188:189], v[186:187], v[166:167] op_sel_hi:[0,1,1] neg_lo:[0,0,1] neg_hi:[0,0,1]
	v_cvt_pk_bf16_f32 v178, v172, v173
	v_cvt_pk_bf16_f32 v179, v174, v175
	global_store_dwordx2 v193, v[178:179], s[28:29] offset:2048
	s_waitcnt vmcnt(31)
	v_lshlrev_b32_e32 v164, 16, v144
	v_and_b32_e32 v165, 0xffff0000, v144
	v_lshlrev_b32_e32 v166, 16, v145
	v_and_b32_e32 v167, 0xffff0000, v145
	v_pk_add_f32 v[184:185], v[184:185], v[164:165]
	v_pk_add_f32 v[186:187], v[186:187], v[166:167]
	v_lshlrev_b32_e32 v168, 16, v140
	v_and_b32_e32 v169, 0xffff0000, v140
	v_lshlrev_b32_e32 v170, 16, v141
	v_and_b32_e32 v171, 0xffff0000, v141
	v_pk_add_f32 v[184:185], v[184:185], v[168:169] neg_lo:[0,1] neg_hi:[0,1]
	v_pk_add_f32 v[186:187], v[186:187], v[170:171] neg_lo:[0,1] neg_hi:[0,1]
	v_pk_fma_f32 v[172:173], v[188:189], v[184:185], v[164:165] op_sel_hi:[0,1,1] neg_lo:[0,0,1] neg_hi:[0,0,1]
	v_pk_fma_f32 v[174:175], v[188:189], v[186:187], v[166:167] op_sel_hi:[0,1,1] neg_lo:[0,0,1] neg_hi:[0,0,1]
	v_cvt_pk_bf16_f32 v180, v172, v173
	v_cvt_pk_bf16_f32 v181, v174, v175
	v_add_u32_e32 v194, 0xb000, v190
	global_store_dwordx2 v194, v[180:181], s[28:29]
	s_waitcnt vmcnt(31)
	v_lshlrev_b32_e32 v164, 16, v146
	v_and_b32_e32 v165, 0xffff0000, v146
	v_lshlrev_b32_e32 v166, 16, v147
	v_and_b32_e32 v167, 0xffff0000, v147
	v_pk_add_f32 v[184:185], v[184:185], v[164:165]
	v_pk_add_f32 v[186:187], v[186:187], v[166:167]
	v_lshlrev_b32_e32 v168, 16, v142
	v_and_b32_e32 v169, 0xffff0000, v142
	v_lshlrev_b32_e32 v170, 16, v143
	v_and_b32_e32 v171, 0xffff0000, v143
	v_pk_add_f32 v[184:185], v[184:185], v[168:169] neg_lo:[0,1] neg_hi:[0,1]
	v_pk_add_f32 v[186:187], v[186:187], v[170:171] neg_lo:[0,1] neg_hi:[0,1]
	v_pk_fma_f32 v[172:173], v[188:189], v[184:185], v[164:165] op_sel_hi:[0,1,1] neg_lo:[0,0,1] neg_hi:[0,0,1]
	v_pk_fma_f32 v[174:175], v[188:189], v[186:187], v[166:167] op_sel_hi:[0,1,1] neg_lo:[0,0,1] neg_hi:[0,0,1]
	v_cvt_pk_bf16_f32 v182, v172, v173
	v_cvt_pk_bf16_f32 v183, v174, v175
	global_store_dwordx2 v194, v[182:183], s[28:29] offset:2048
	s_waitcnt vmcnt(31)
	v_lshlrev_b32_e32 v164, 16, v148
	v_and_b32_e32 v165, 0xffff0000, v148
	v_lshlrev_b32_e32 v166, 16, v149
	v_and_b32_e32 v167, 0xffff0000, v149
	v_pk_add_f32 v[184:185], v[184:185], v[164:165]
	v_pk_add_f32 v[186:187], v[186:187], v[166:167]
	v_lshlrev_b32_e32 v168, 16, v144
	v_and_b32_e32 v169, 0xffff0000, v144
	v_lshlrev_b32_e32 v170, 16, v145
	v_and_b32_e32 v171, 0xffff0000, v145
	v_pk_add_f32 v[184:185], v[184:185], v[168:169] neg_lo:[0,1] neg_hi:[0,1]
	v_pk_add_f32 v[186:187], v[186:187], v[170:171] neg_lo:[0,1] neg_hi:[0,1]
	v_pk_fma_f32 v[172:173], v[188:189], v[184:185], v[164:165] op_sel_hi:[0,1,1] neg_lo:[0,0,1] neg_hi:[0,0,1]
	v_pk_fma_f32 v[174:175], v[188:189], v[186:187], v[166:167] op_sel_hi:[0,1,1] neg_lo:[0,0,1] neg_hi:[0,0,1]
	v_cvt_pk_bf16_f32 v176, v172, v173
	v_cvt_pk_bf16_f32 v177, v174, v175
	v_add_u32_e32 v193, 0xc000, v190
	global_store_dwordx2 v193, v[176:177], s[28:29]
	s_waitcnt vmcnt(31)
	v_lshlrev_b32_e32 v164, 16, v150
	v_and_b32_e32 v165, 0xffff0000, v150
	v_lshlrev_b32_e32 v166, 16, v151
	v_and_b32_e32 v167, 0xffff0000, v151
	v_pk_add_f32 v[184:185], v[184:185], v[164:165]
	v_pk_add_f32 v[186:187], v[186:187], v[166:167]
	v_lshlrev_b32_e32 v168, 16, v146
	v_and_b32_e32 v169, 0xffff0000, v146
	v_lshlrev_b32_e32 v170, 16, v147
	v_and_b32_e32 v171, 0xffff0000, v147
	v_pk_add_f32 v[184:185], v[184:185], v[168:169] neg_lo:[0,1] neg_hi:[0,1]
	v_pk_add_f32 v[186:187], v[186:187], v[170:171] neg_lo:[0,1] neg_hi:[0,1]
	v_pk_fma_f32 v[172:173], v[188:189], v[184:185], v[164:165] op_sel_hi:[0,1,1] neg_lo:[0,0,1] neg_hi:[0,0,1]
	v_pk_fma_f32 v[174:175], v[188:189], v[186:187], v[166:167] op_sel_hi:[0,1,1] neg_lo:[0,0,1] neg_hi:[0,0,1]
	v_cvt_pk_bf16_f32 v178, v172, v173
	v_cvt_pk_bf16_f32 v179, v174, v175
	global_store_dwordx2 v193, v[178:179], s[28:29] offset:2048
	s_waitcnt vmcnt(31)
	v_lshlrev_b32_e32 v164, 16, v152
	v_and_b32_e32 v165, 0xffff0000, v152
	v_lshlrev_b32_e32 v166, 16, v153
	v_and_b32_e32 v167, 0xffff0000, v153
	v_pk_add_f32 v[184:185], v[184:185], v[164:165]
	v_pk_add_f32 v[186:187], v[186:187], v[166:167]
	v_lshlrev_b32_e32 v168, 16, v148
	v_and_b32_e32 v169, 0xffff0000, v148
	v_lshlrev_b32_e32 v170, 16, v149
	v_and_b32_e32 v171, 0xffff0000, v149
	v_pk_add_f32 v[184:185], v[184:185], v[168:169] neg_lo:[0,1] neg_hi:[0,1]
	v_pk_add_f32 v[186:187], v[186:187], v[170:171] neg_lo:[0,1] neg_hi:[0,1]
	v_pk_fma_f32 v[172:173], v[188:189], v[184:185], v[164:165] op_sel_hi:[0,1,1] neg_lo:[0,0,1] neg_hi:[0,0,1]
	v_pk_fma_f32 v[174:175], v[188:189], v[186:187], v[166:167] op_sel_hi:[0,1,1] neg_lo:[0,0,1] neg_hi:[0,0,1]
	v_cvt_pk_bf16_f32 v180, v172, v173
	v_cvt_pk_bf16_f32 v181, v174, v175
	v_add_u32_e32 v194, 0xd000, v190
	global_store_dwordx2 v194, v[180:181], s[28:29]
	s_waitcnt vmcnt(31)
; #define GAS __attribute__((address_space(1)))
; __device__ __forceinline__ unsigned pk2(float lo, float hi) { const f32x2 v = {lo, hi}; return __builtin_bit_cast(unsigned, __builtin_convertvector(v, b16x2)); }
; template <int W>
; __device__ __forceinline__ void pool_item(const bf16* U, bf16* Z, int b, int t0, int g, int lane) {
;     const size_t base = (size_t)b * SEQ * D + 256 * g + 4 * lane;
;     float s[4] = {0.f, 0.f, 0.f, 0.f};
; #pragma unroll
;     for (int j = 1; j <= W; ++j) { const int t = t0 - j; if (t >= 0) { const u32x2 v = *(const GAS u32x2*)(U + base + (size_t)t * D);
;             s[0] += bf2f(v.x & 0xffffu); s[1] += bf2f(v.x >> 16); s[2] += bf2f(v.y & 0xffffu); s[3] += bf2f(v.y >> 16); } }
;     ...
;     for (int i = 0; i < 32; ++i) { const int t = t0 + i;
;         const u32x2 v = *(const GAS u32x2*)(U + base + (size_t)t * D);
;         const float c0 = bf2f(v.x & 0xffffu), c1 = bf2f(v.x >> 16), c2 = bf2f(v.y & 0xffffu), c3 = bf2f(v.y >> 16);
;         s[0] += c0; s[1] += c1; s[2] += c2; s[3] += c3;
;         if (t - W >= 0) { const u32x2 o = *(const GAS u32x2*)(U + base + (size_t)(t - W) * D);
;             s[0] -= bf2f(o.x & 0xffffu); s[1] -= bf2f(o.x >> 16); s[2] -= bf2f(o.y & 0xffffu); s[3] -= bf2f(o.y >> 16); }
;         const float inv = 1.0f / (float)((t + 1) < W ? (t + 1) : W);
;         u32x2 w; w.x = pk2(s[0] * inv - c0, s[1] * inv - c1); w.y = pk2(s[2] * inv - c2, s[3] * inv - c3);
;         *(GAS u32x2*)(Z + base + (size_t)t * D) = w; }
; }
	v_lshlrev_b32_e32 v164, 16, v154
	v_and_b32_e32 v165, 0xffff0000, v154
	v_lshlrev_b32_e32 v166, 16, v155
	v_and_b32_e32 v167, 0xffff0000, v155
	v_pk_add_f32 v[184:185], v[184:185], v[164:165]
	v_pk_add_f32 v[186:187], v[186:187], v[166:167]
	v_lshlrev_b32_e32 v168, 16, v150
	v_and_b32_e32 v169, 0xffff0000, v150
	v_lshlrev_b32_e32 v170, 16, v151
	v_and_b32_e32 v171, 0xffff0000, v151
	v_pk_add_f32 v[184:185], v[184:185], v[168:169] neg_lo:[0,1] neg_hi:[0,1]
	v_pk_add_f32 v[186:187], v[186:187], v[170:171] neg_lo:[0,1] neg_hi:[0,1]
	v_pk_fma_f32 v[172:173], v[188:189], v[184:185], v[164:165] op_sel_hi:[0,1,1] neg_lo:[0,0,1] neg_hi:[0,0,1]
	v_pk_fma_f32 v[174:175], v[188:189], v[186:187], v[166:167] op_sel_hi:[0,1,1] neg_lo:[0,0,1] neg_hi:[0,0,1]
	v_cvt_pk_bf16_f32 v182, v172, v173
	v_cvt_pk_bf16_f32 v183, v174, v175
	global_store_dwordx2 v194, v[182:183], s[28:29] offset:2048
	s_waitcnt vmcnt(31)
	v_lshlrev_b32_e32 v164, 16, v156
	v_and_b32_e32 v165, 0xffff0000, v156
	v_lshlrev_b32_e32 v166, 16, v157
	v_and_b32_e32 v167, 0xffff0000, v157
	v_pk_add_f32 v[184:185], v[184:185], v[164:165]
	v_pk_add_f32 v[186:187], v[186:187], v[166:167]
	v_lshlrev_b32_e32 v168, 16, v152
	v_and_b32_e32 v169, 0xffff0000, v152
	v_lshlrev_b32_e32 v170, 16, v153
	v_and_b32_e32 v171, 0xffff0000, v153
	v_pk_add_f32 v[184:185], v[184:185], v[168:169] neg_lo:[0,1] neg_hi:[0,1]
	v_pk_add_f32 v[186:187], v[186:187], v[170:171] neg_lo:[0,1] neg_hi:[0,1]
	v_pk_fma_f32 v[172:173], v[188:189], v[184:185], v[164:165] op_sel_hi:[0,1,1] neg_lo:[0,0,1] neg_hi:[0,0,1]
	v_pk_fma_f32 v[174:175], v[188:189], v[186:187], v[166:167] op_sel_hi:[0,1,1] neg_lo:[0,0,1] neg_hi:[0,0,1]
	v_cvt_pk_bf16_f32 v176, v172, v173
	v_cvt_pk_bf16_f32 v177, v174, v175
	v_add_u32_e32 v193, 0xe000, v190
	global_store_dwordx2 v193, v[176:177], s[28:29]
	s_waitcnt vmcnt(31)
	v_lshlrev_b32_e32 v164, 16, v158
	v_and_b32_e32 v165, 0xffff0000, v158
	v_lshlrev_b32_e32 v166, 16, v159
	v_and_b32_e32 v167, 0xffff0000, v159
	v_pk_add_f32 v[184:185], v[184:185], v[164:165]
	v_pk_add_f32 v[186:187], v[186:187], v[166:167]
	v_lshlrev_b32_e32 v168, 16, v154
	v_and_b32_e32 v169, 0xffff0000, v154
	v_lshlrev_b32_e32 v170, 16, v155
	v_and_b32_e32 v171, 0xffff0000, v155
	v_pk_add_f32 v[184:185], v[184:185], v[168:169] neg_lo:[0,1] neg_hi:[0,1]
	v_pk_add_f32 v[186:187], v[186:187], v[170:171] neg_lo:[0,1] neg_hi:[0,1]
	v_pk_fma_f32 v[172:173], v[188:189], v[184:185], v[164:165] op_sel_hi:[0,1,1] neg_lo:[0,0,1] neg_hi:[0,0,1]
	v_pk_fma_f32 v[174:175], v[188:189], v[186:187], v[166:167] op_sel_hi:[0,1,1] neg_lo:[0,0,1] neg_hi:[0,0,1]
	v_cvt_pk_bf16_f32 v178, v172, v173
	v_cvt_pk_bf16_f32 v179, v174, v175
	global_store_dwordx2 v193, v[178:179], s[28:29] offset:2048
	s_waitcnt vmcnt(31)
	v_lshlrev_b32_e32 v164, 16, v160
	v_and_b32_e32 v165, 0xffff0000, v160
	v_lshlrev_b32_e32 v166, 16, v161
	v_and_b32_e32 v167, 0xffff0000, v161
	v_pk_add_f32 v[184:185], v[184:185], v[164:165]
	v_pk_add_f32 v[186:187], v[186:187], v[166:167]
	v_lshlrev_b32_e32 v168, 16, v156
	v_and_b32_e32 v169, 0xffff0000, v156
	v_lshlrev_b32_e32 v170, 16, v157
	v_and_b32_e32 v171, 0xffff0000, v157
	v_pk_add_f32 v[184:185], v[184:185], v[168:169] neg_lo:[0,1] neg_hi:[0,1]
	v_pk_add_f32 v[186:187], v[186:187], v[170:171] neg_lo:[0,1] neg_hi:[0,1]
	v_pk_fma_f32 v[172:173], v[188:189], v[184:185], v[164:165] op_sel_hi:[0,1,1] neg_lo:[0,0,1] neg_hi:[0,0,1]
	v_pk_fma_f32 v[174:175], v[188:189], v[186:187], v[166:167] op_sel_hi:[0,1,1] neg_lo:[0,0,1] neg_hi:[0,0,1]
	v_cvt_pk_bf16_f32 v180, v172, v173
	v_cvt_pk_bf16_f32 v181, v174, v175
	v_add_u32_e32 v194, 0xf000, v190
	global_store_dwordx2 v194, v[180:181], s[28:29]
	s_waitcnt vmcnt(31)
	v_lshlrev_b32_e32 v164, 16, v162
	v_and_b32_e32 v165, 0xffff0000, v162
	v_lshlrev_b32_e32 v166, 16, v163
	v_and_b32_e32 v167, 0xffff0000, v163
	v_pk_add_f32 v[184:185], v[184:185], v[164:165]
	v_pk_add_f32 v[186:187], v[186:187], v[166:167]
	v_lshlrev_b32_e32 v168, 16, v158
	v_and_b32_e32 v169, 0xffff0000, v158
	v_lshlrev_b32_e32 v170, 16, v159
	v_and_b32_e32 v171, 0xffff0000, v159
	v_pk_add_f32 v[184:185], v[184:185], v[168:169] neg_lo:[0,1] neg_hi:[0,1]
	v_pk_add_f32 v[186:187], v[186:187], v[170:171] neg_lo:[0,1] neg_hi:[0,1]
	v_pk_fma_f32 v[172:173], v[188:189], v[184:185], v[164:165] op_sel_hi:[0,1,1] neg_lo:[0,0,1] neg_hi:[0,0,1]
	v_pk_fma_f32 v[174:175], v[188:189], v[186:187], v[166:167] op_sel_hi:[0,1,1] neg_lo:[0,0,1] neg_hi:[0,0,1]
	v_cvt_pk_bf16_f32 v182, v172, v173
	v_cvt_pk_bf16_f32 v183, v174, v175
	global_store_dwordx2 v194, v[182:183], s[28:29] offset:2048
	s_branch .LBB0_861
.Lpool_orig:
	s_cmp_lt_i32 s9, 1
	s_mov_b64 s[54:55], 0
	s_cbranch_scc1 .LBB0_882
	v_readlane_b32 s9, v255, 3
	s_cmp_gt_i32 s9, 1
	s_cbranch_scc0 .LBB0_911
	s_cmp_eq_u32 s9, 2
	s_mov_b64 s[54:55], -1
	s_cbranch_scc0 .LBB0_910
	v_mov_b32_e32 v19, s51
	v_or_b32_e32 v18, s50, v6
	s_andn2_b64 vcc, exec, s[40:41]
	s_cbranch_vccnz .LBB0_1013
	s_add_i32 s22, s46, -1
	s_lshl_b64 s[10:11], s[22:23], 11
	s_add_u32 s10, s44, s10
	s_addc_u32 s11, s45, s11
	v_lshl_add_u64 v[20:21], v[18:19], 1, s[10:11]
	global_load_dwordx2 v[20:21], v[20:21], off
	s_waitcnt vmcnt(0)
	v_and_b32_e32 v22, 0xffff0000, v20
	v_lshlrev_b32_e32 v23, 16, v20
	v_and_b32_e32 v20, 0xffff0000, v21
	v_lshlrev_b32_e32 v21, 16, v21
	v_pk_add_f32 v[22:23], v[22:23], 0 op_sel_hi:[1,0]
	v_pk_add_f32 v[24:25], v[20:21], 0 op_sel_hi:[1,0]
	s_cmp_lt_i32 s46, 2
	s_cbranch_scc1 .LBB0_876
